# baseline (speedup 1.0000x reference)
.LBB2_13:
	s_or_b64 exec, exec, s[10:11]
	v_cvt_f32_f16_e32 v89, v24
	v_cvt_f32_f16_e32 v49, v108
	v_lshlrev_b32_e32 v52, 3, v107
	s_movk_i32 s0, 0x50
	v_mad_u32_u24 v24, v136, s0, v52
	v_mad_u32_u24 v218, v135, s0, v52
	v_mov_b32_e32 v164, 0x3fb8aa3b
	v_mov_b32_e32 v165, 0x3fb8aa3b
	v_mov_b32_e32 v166, 0x3f317218
	v_mov_b32_e32 v167, 0x3f317218
	v_mov_b32_e32 v168, 1.0
	v_mov_b32_e32 v169, 1.0
	v_mov_b32_e32 v212, v134
	v_mov_b32_e32 v214, v133
	v_mov_b32_e32 v216, v131
	v_mov_b32_e32 v220, v121
	v_mfma_f32_16x16x32_f16 v[170:173], v[42:45], v[34:37], 0
	v_mfma_f32_16x16x32_f16 v[186:189], v[38:41], v[34:37], 0
	v_mfma_f32_16x16x32_f16 v[174:177], v[42:45], v[30:33], 0
	v_mfma_f32_16x16x32_f16 v[190:193], v[38:41], v[30:33], 0
	s_waitcnt vmcnt(9)
	v_mfma_f32_16x16x32_f16 v[178:181], v[42:45], v[26:29], 0
	v_mfma_f32_16x16x32_f16 v[194:197], v[38:41], v[26:29], 0
	s_waitcnt vmcnt(8)
	v_mfma_f32_16x16x32_f16 v[182:185], v[42:45], v[18:21], 0
	v_mfma_f32_16x16x32_f16 v[198:201], v[38:41], v[18:21], 0
	v_pk_add_f32 v[202:203], v[170:171], v[212:213] op_sel_hi:[1,0]
	v_pk_add_f32 v[204:205], v[172:173], v[212:213] op_sel_hi:[1,0]
	v_pk_add_f32 v[222:223], v[186:187], v[212:213] op_sel_hi:[1,0]
	v_pk_add_f32 v[224:225], v[188:189], v[212:213] op_sel_hi:[1,0]
	v_pk_add_f32 v[232:233], v[174:175], v[214:215] op_sel_hi:[1,0]
	v_pk_add_f32 v[234:235], v[176:177], v[214:215] op_sel_hi:[1,0]
	v_pk_add_f32 v[242:243], v[190:191], v[214:215] op_sel_hi:[1,0]
	v_pk_add_f32 v[244:245], v[192:193], v[214:215] op_sel_hi:[1,0]
	v_min_f32_e32 v206, 0x42a00000, v202
	v_min_f32_e32 v207, 0x42a00000, v203
	v_min_f32_e32 v208, 0x42a00000, v204
	v_min_f32_e32 v209, 0x42a00000, v205
	v_min_f32_e32 v226, 0x42a00000, v222
	v_min_f32_e32 v227, 0x42a00000, v223
	v_min_f32_e32 v228, 0x42a00000, v224
	v_min_f32_e32 v229, 0x42a00000, v225
	v_min_f32_e32 v236, 0x42a00000, v232
	v_min_f32_e32 v237, 0x42a00000, v233
	v_min_f32_e32 v238, 0x42a00000, v234
	v_min_f32_e32 v239, 0x42a00000, v235
	v_min_f32_e32 v246, 0x42a00000, v242
	v_min_f32_e32 v247, 0x42a00000, v243
	v_min_f32_e32 v248, 0x42a00000, v244
	v_min_f32_e32 v249, 0x42a00000, v245
	v_pk_mul_f32 v[206:207], v[206:207], v[164:165]
	v_pk_mul_f32 v[208:209], v[208:209], v[164:165]
	v_pk_mul_f32 v[226:227], v[226:227], v[164:165]
	v_pk_mul_f32 v[228:229], v[228:229], v[164:165]
	v_pk_mul_f32 v[236:237], v[236:237], v[164:165]
	v_pk_mul_f32 v[238:239], v[238:239], v[164:165]
	v_pk_mul_f32 v[246:247], v[246:247], v[164:165]
	v_pk_mul_f32 v[248:249], v[248:249], v[164:165]
	v_exp_f32_e32 v206, v206
	v_exp_f32_e32 v207, v207
	v_exp_f32_e32 v208, v208
	v_exp_f32_e32 v209, v209
	v_exp_f32_e32 v226, v226
	v_exp_f32_e32 v227, v227
	v_exp_f32_e32 v228, v228
	v_exp_f32_e32 v229, v229
	v_exp_f32_e32 v236, v236
	v_exp_f32_e32 v237, v237
	v_exp_f32_e32 v238, v238
	v_exp_f32_e32 v239, v239
	v_exp_f32_e32 v246, v246
	v_exp_f32_e32 v247, v247
	v_exp_f32_e32 v248, v248
	v_exp_f32_e32 v249, v249
	v_pk_add_f32 v[206:207], v[206:207], v[168:169]
	v_pk_add_f32 v[208:209], v[208:209], v[168:169]
	v_pk_add_f32 v[226:227], v[226:227], v[168:169]
	v_pk_add_f32 v[228:229], v[228:229], v[168:169]
	v_pk_add_f32 v[236:237], v[236:237], v[168:169]
	v_pk_add_f32 v[238:239], v[238:239], v[168:169]
	v_pk_add_f32 v[246:247], v[246:247], v[168:169]
	v_pk_add_f32 v[248:249], v[248:249], v[168:169]
	v_log_f32_e32 v206, v206
	v_log_f32_e32 v207, v207
	v_log_f32_e32 v208, v208
	v_log_f32_e32 v209, v209
	v_log_f32_e32 v226, v226
	v_log_f32_e32 v227, v227
	v_log_f32_e32 v228, v228
	v_log_f32_e32 v229, v229
	v_log_f32_e32 v236, v236
	v_log_f32_e32 v237, v237
	v_log_f32_e32 v238, v238
	v_log_f32_e32 v239, v239
	v_log_f32_e32 v246, v246
	v_log_f32_e32 v247, v247
	v_log_f32_e32 v248, v248
	v_log_f32_e32 v249, v249
	v_pk_mul_f32 v[206:207], v[206:207], v[166:167]
	v_pk_mul_f32 v[208:209], v[208:209], v[166:167]
	v_pk_mul_f32 v[226:227], v[226:227], v[166:167]
	v_pk_mul_f32 v[228:229], v[228:229], v[166:167]
	v_pk_mul_f32 v[236:237], v[236:237], v[166:167]
	v_pk_mul_f32 v[238:239], v[238:239], v[166:167]
	v_pk_mul_f32 v[246:247], v[246:247], v[166:167]
	v_pk_mul_f32 v[248:249], v[248:249], v[166:167]
	v_max_f32_e32 v202, v202, v206
	v_max_f32_e32 v203, v203, v207
	v_max_f32_e32 v204, v204, v208
	v_max_f32_e32 v205, v205, v209
	v_max_f32_e32 v222, v222, v226
	v_max_f32_e32 v223, v223, v227
	v_max_f32_e32 v224, v224, v228
	v_max_f32_e32 v225, v225, v229
	v_max_f32_e32 v232, v232, v236
	v_max_f32_e32 v233, v233, v237
	v_max_f32_e32 v234, v234, v238
	v_max_f32_e32 v235, v235, v239
	v_max_f32_e32 v242, v242, v246
	v_max_f32_e32 v243, v243, v247
	v_max_f32_e32 v244, v244, v248
	v_max_f32_e32 v245, v245, v249
	v_cvt_pk_f16_f32 v210, v202, v203
	v_cvt_pk_f16_f32 v211, v204, v205
	v_cvt_pk_f16_f32 v230, v222, v223
	v_cvt_pk_f16_f32 v231, v224, v225
	v_cvt_pk_f16_f32 v240, v232, v233
	v_cvt_pk_f16_f32 v241, v234, v235
	v_cvt_pk_f16_f32 v250, v242, v243
	v_cvt_pk_f16_f32 v251, v244, v245
	ds_write_b64 v24, v[210:211]
	ds_write_b64 v24, v[230:231] offset:32
	ds_write_b64 v24, v[240:241] offset:1280
	ds_write_b64 v24, v[250:251] offset:1312
	v_pk_add_f32 v[202:203], v[178:179], v[216:217] op_sel_hi:[1,0]
	v_pk_add_f32 v[204:205], v[180:181], v[216:217] op_sel_hi:[1,0]
	v_pk_add_f32 v[222:223], v[194:195], v[216:217] op_sel_hi:[1,0]
	v_pk_add_f32 v[224:225], v[196:197], v[216:217] op_sel_hi:[1,0]
	v_pk_add_f32 v[232:233], v[182:183], v[220:221] op_sel_hi:[1,0]
	v_pk_add_f32 v[234:235], v[184:185], v[220:221] op_sel_hi:[1,0]
	v_pk_add_f32 v[242:243], v[198:199], v[220:221] op_sel_hi:[1,0]
	v_pk_add_f32 v[244:245], v[200:201], v[220:221] op_sel_hi:[1,0]
	v_min_f32_e32 v206, 0x42a00000, v202
	v_min_f32_e32 v207, 0x42a00000, v203
	v_min_f32_e32 v208, 0x42a00000, v204
	v_min_f32_e32 v209, 0x42a00000, v205
	v_min_f32_e32 v226, 0x42a00000, v222
	v_min_f32_e32 v227, 0x42a00000, v223
	v_min_f32_e32 v228, 0x42a00000, v224
	v_min_f32_e32 v229, 0x42a00000, v225
	v_min_f32_e32 v236, 0x42a00000, v232
	v_min_f32_e32 v237, 0x42a00000, v233
	v_min_f32_e32 v238, 0x42a00000, v234
	v_min_f32_e32 v239, 0x42a00000, v235
	v_min_f32_e32 v246, 0x42a00000, v242
	v_min_f32_e32 v247, 0x42a00000, v243
	v_min_f32_e32 v248, 0x42a00000, v244
	v_min_f32_e32 v249, 0x42a00000, v245
	v_pk_mul_f32 v[206:207], v[206:207], v[164:165]
	v_pk_mul_f32 v[208:209], v[208:209], v[164:165]
	v_pk_mul_f32 v[226:227], v[226:227], v[164:165]
	v_pk_mul_f32 v[228:229], v[228:229], v[164:165]
	v_pk_mul_f32 v[236:237], v[236:237], v[164:165]
	v_pk_mul_f32 v[238:239], v[238:239], v[164:165]
	v_pk_mul_f32 v[246:247], v[246:247], v[164:165]
	v_pk_mul_f32 v[248:249], v[248:249], v[164:165]
	v_exp_f32_e32 v206, v206
	v_exp_f32_e32 v207, v207
	v_exp_f32_e32 v208, v208
	v_exp_f32_e32 v209, v209
	v_exp_f32_e32 v226, v226
	v_exp_f32_e32 v227, v227
	v_exp_f32_e32 v228, v228
	v_exp_f32_e32 v229, v229
	v_exp_f32_e32 v236, v236
	v_exp_f32_e32 v237, v237
	v_exp_f32_e32 v238, v238
	v_exp_f32_e32 v239, v239
	v_exp_f32_e32 v246, v246
	v_exp_f32_e32 v247, v247
	v_exp_f32_e32 v248, v248
	v_exp_f32_e32 v249, v249
	v_pk_add_f32 v[206:207], v[206:207], v[168:169]
	v_pk_add_f32 v[208:209], v[208:209], v[168:169]
	v_pk_add_f32 v[226:227], v[226:227], v[168:169]
	v_pk_add_f32 v[228:229], v[228:229], v[168:169]
	v_pk_add_f32 v[236:237], v[236:237], v[168:169]
	v_pk_add_f32 v[238:239], v[238:239], v[168:169]
	v_pk_add_f32 v[246:247], v[246:247], v[168:169]
	v_pk_add_f32 v[248:249], v[248:249], v[168:169]
	v_log_f32_e32 v206, v206
	v_log_f32_e32 v207, v207
	v_log_f32_e32 v208, v208
	v_log_f32_e32 v209, v209
	v_log_f32_e32 v226, v226
	v_log_f32_e32 v227, v227
	v_log_f32_e32 v228, v228
	v_log_f32_e32 v229, v229
	v_log_f32_e32 v236, v236
	v_log_f32_e32 v237, v237
	v_log_f32_e32 v238, v238
	v_log_f32_e32 v239, v239
	v_log_f32_e32 v246, v246
	v_log_f32_e32 v247, v247
	v_log_f32_e32 v248, v248
	v_log_f32_e32 v249, v249
	v_pk_mul_f32 v[206:207], v[206:207], v[166:167]
	v_pk_mul_f32 v[208:209], v[208:209], v[166:167]
	v_pk_mul_f32 v[226:227], v[226:227], v[166:167]
	v_pk_mul_f32 v[228:229], v[228:229], v[166:167]
	v_pk_mul_f32 v[236:237], v[236:237], v[166:167]
	v_pk_mul_f32 v[238:239], v[238:239], v[166:167]
	v_pk_mul_f32 v[246:247], v[246:247], v[166:167]
	v_pk_mul_f32 v[248:249], v[248:249], v[166:167]
	v_max_f32_e32 v202, v202, v206
	v_max_f32_e32 v203, v203, v207
	v_max_f32_e32 v204, v204, v208
	v_max_f32_e32 v205, v205, v209
	v_max_f32_e32 v222, v222, v226
	v_max_f32_e32 v223, v223, v227
	v_max_f32_e32 v224, v224, v228
	v_max_f32_e32 v225, v225, v229
	v_max_f32_e32 v232, v232, v236
	v_max_f32_e32 v233, v233, v237
	v_max_f32_e32 v234, v234, v238
	v_max_f32_e32 v235, v235, v239
	v_max_f32_e32 v242, v242, v246
	v_max_f32_e32 v243, v243, v247
	v_max_f32_e32 v244, v244, v248
	v_max_f32_e32 v245, v245, v249
	v_cvt_pk_f16_f32 v210, v202, v203
	v_cvt_pk_f16_f32 v211, v204, v205
	v_cvt_pk_f16_f32 v230, v222, v223
	v_cvt_pk_f16_f32 v231, v224, v225
	v_cvt_pk_f16_f32 v240, v232, v233
	v_cvt_pk_f16_f32 v241, v234, v235
	v_cvt_pk_f16_f32 v250, v242, v243
	v_cvt_pk_f16_f32 v251, v244, v245
	ds_write_b64 v24, v[210:211] offset:2560
	ds_write_b64 v24, v[230:231] offset:2592
	ds_write_b64 v218, v[240:241]
	ds_write_b64 v218, v[250:251] offset:32
	v_mul_u32_u24_e32 v18, 0x50, v0
	s_waitcnt lgkmcnt(0)
	s_barrier
	ds_read_b128 v[92:95], v18
	v_cvt_f32_f16_e32 v55, v111
	v_cvt_f32_f16_e32 v59, v110
	v_cvt_f32_f16_e32 v79, v105
	v_cvt_f32_f16_e32 v82, v104
	v_cvt_f32_f16_e32 v84, v103
	v_cvt_f32_f16_e32 v86, v102
	ds_read_b128 v[96:99], v18 offset:16
	ds_read_b128 v[100:103], v18 offset:32
	ds_read_b128 v[108:111], v18 offset:48
	v_lshl_add_u64 v[104:105], s[8:9], 0, v[118:119]
	v_cvt_f32_f16_e32 v47, v113
	v_cvt_f32_f16_e32 v51, v112
	v_lshl_add_u64 v[112:113], v[104:105], 0, s[6:7]
	s_waitcnt lgkmcnt(3)
	v_cvt_f32_f16_e32 v26, v94
	v_cvt_f32_f16_sdwa v28, v94 dst_sel:DWORD dst_unused:UNUSED_PAD src0_sel:WORD_1
	v_cvt_f32_f16_e32 v30, v95
	v_cvt_f32_f16_sdwa v32, v95 dst_sel:DWORD dst_unused:UNUSED_PAD src0_sel:WORD_1
	global_store_dwordx4 v[112:113], v[92:95], off sc0 sc1
	v_cvt_f32_f16_e32 v53, v122
	v_cvt_f32_f16_e32 v57, v125
	v_lshl_add_u64 v[94:95], v[104:105], 0, s[14:15]
	s_waitcnt lgkmcnt(2)
	global_store_dwordx4 v[94:95], v[96:99], off sc0 sc1
	v_lshl_add_u64 v[94:95], v[104:105], 0, s[16:17]
	s_waitcnt lgkmcnt(1)
	global_store_dwordx4 v[94:95], v[100:103], off sc0 sc1
	v_lshl_add_u64 v[94:95], v[104:105], 0, s[18:19]
	v_cvt_f32_f16_e32 v61, v124
	v_cvt_f32_f16_e32 v63, v117
	v_cvt_f32_f16_e32 v65, v147
	v_cvt_f32_f16_e32 v67, v116
	v_cvt_f32_f16_e32 v69, v145
	v_cvt_f32_f16_e32 v71, v115
	v_cvt_f32_f16_e32 v73, v127
	v_cvt_f32_f16_e32 v75, v114
	v_cvt_f32_f16_e32 v77, v126
	v_cvt_f32_f16_e32 v81, v142
	v_cvt_f32_f16_e32 v83, v141
	v_cvt_f32_f16_e32 v85, v140
	v_cvt_f32_f16_e32 v87, v139
	v_cvt_f32_f16_e32 v25, v25
	v_cvt_f32_f16_e32 v88, v138
	v_cvt_f32_f16_e32 v90, v137
	v_cvt_f32_f16_e32 v23, v23
	v_cvt_f32_f16_e32 v91, v123
	v_cvt_f32_f16_e32 v19, v22
	v_cvt_f32_f16_sdwa v20, v92 dst_sel:DWORD dst_unused:UNUSED_PAD src0_sel:WORD_1
	v_cvt_f32_f16_e32 v22, v93
	v_cvt_f32_f16_sdwa v24, v93 dst_sel:DWORD dst_unused:UNUSED_PAD src0_sel:WORD_1
	v_cvt_f32_f16_e32 v34, v96
	v_cvt_f32_f16_sdwa v36, v96 dst_sel:DWORD dst_unused:UNUSED_PAD src0_sel:WORD_1
	v_cvt_f32_f16_e32 v38, v97
	v_cvt_f32_f16_sdwa v40, v97 dst_sel:DWORD dst_unused:UNUSED_PAD src0_sel:WORD_1
	v_cvt_f32_f16_e32 v42, v98
	v_cvt_f32_f16_sdwa v44, v98 dst_sel:DWORD dst_unused:UNUSED_PAD src0_sel:WORD_1
	v_cvt_f32_f16_e32 v46, v99
	v_cvt_f32_f16_sdwa v48, v99 dst_sel:DWORD dst_unused:UNUSED_PAD src0_sel:WORD_1
	v_cvt_f32_f16_e32 v50, v100
	v_cvt_f32_f16_sdwa v52, v100 dst_sel:DWORD dst_unused:UNUSED_PAD src0_sel:WORD_1
	v_cvt_f32_f16_e32 v54, v101
	v_cvt_f32_f16_sdwa v56, v101 dst_sel:DWORD dst_unused:UNUSED_PAD src0_sel:WORD_1
	v_cvt_f32_f16_e32 v58, v102
	v_cvt_f32_f16_sdwa v60, v102 dst_sel:DWORD dst_unused:UNUSED_PAD src0_sel:WORD_1
	v_cvt_f32_f16_e32 v62, v103
	v_cvt_f32_f16_sdwa v64, v103 dst_sel:DWORD dst_unused:UNUSED_PAD src0_sel:WORD_1
	s_waitcnt lgkmcnt(0)
	v_cvt_f32_f16_e32 v66, v108
	v_cvt_f32_f16_sdwa v68, v108 dst_sel:DWORD dst_unused:UNUSED_PAD src0_sel:WORD_1
	v_cvt_f32_f16_e32 v70, v109
	v_cvt_f32_f16_sdwa v72, v109 dst_sel:DWORD dst_unused:UNUSED_PAD src0_sel:WORD_1
	v_cvt_f32_f16_e32 v74, v110
	v_cvt_f32_f16_sdwa v76, v110 dst_sel:DWORD dst_unused:UNUSED_PAD src0_sel:WORD_1
	v_cvt_f32_f16_e32 v78, v111
	v_cvt_f32_f16_sdwa v18, v111 dst_sel:DWORD dst_unused:UNUSED_PAD src0_sel:WORD_1
	global_store_dwordx4 v[94:95], v[108:111], off sc0 sc1
	v_cvt_f32_f16_e32 v80, v92
	v_mov_b32_e32 v160, 0
	ds_read_b128 v[92:95], v160 offset:41024
	ds_read_b128 v[96:99], v160 offset:41040
	ds_read_b128 v[100:103], v160 offset:41056
	ds_read_b128 v[108:111], v160 offset:41072
	s_waitcnt lgkmcnt(0)
	ds_read_b128 v[112:115], v160 offset:41232
	ds_read_b128 v[116:119], v160 offset:41248
	ds_read_b128 v[120:123], v160 offset:41264
	ds_read_b128 v[124:127], v160 offset:41280
	s_lshr_b32 s0, s23, 5
	s_waitcnt vmcnt(11)
	v_mul_f32_e32 v104, v80, v19
	v_pk_mul_f32 v[128:129], v[104:105], v[92:93] op_sel_hi:[0,1]
	v_pk_mul_f32 v[130:131], v[104:105], v[94:95] op_sel_hi:[0,1]
	s_waitcnt vmcnt(10)
	v_pk_mul_f32 v[132:133], v[104:105], v[96:97] op_sel_hi:[0,1]
	v_pk_mul_f32 v[134:135], v[104:105], v[98:99] op_sel_hi:[0,1]
	s_waitcnt vmcnt(9)
	v_pk_mul_f32 v[136:137], v[104:105], v[100:101] op_sel_hi:[0,1]
	v_pk_mul_f32 v[138:139], v[104:105], v[102:103] op_sel_hi:[0,1]
	s_waitcnt vmcnt(8)
	v_pk_mul_f32 v[140:141], v[104:105], v[108:109] op_sel_hi:[0,1]
	v_pk_mul_f32 v[104:105], v[104:105], v[110:111] op_sel_hi:[0,1]
	s_waitcnt lgkmcnt(0)
	s_and_b32 s6, s22, 0x7ffffc0
	ds_read_b128 v[92:95], v160 offset:41440
	ds_read_b128 v[96:99], v160 offset:41456
	ds_read_b128 v[100:103], v160 offset:41472
	ds_read_b128 v[108:111], v160 offset:41488
	v_pk_mul_f32 v[142:143], v[20:21], v[14:15] op_sel_hi:[0,1]
	v_exp_f32_e32 v142, v142
	v_exp_f32_e32 v143, v143
	v_mul_f32_e32 v144, v20, v91
	v_pk_mul_f32 v[112:113], v[144:145], v[112:113] op_sel_hi:[0,1]
	v_pk_mul_f32 v[114:115], v[144:145], v[114:115] op_sel_hi:[0,1]
	v_pk_fma_f32 v[128:129], v[128:129], v[142:143], v[112:113]
	v_pk_mul_f32 v[112:113], v[20:21], v[16:17] op_sel_hi:[0,1]
	v_exp_f32_e32 v112, v112
	v_exp_f32_e32 v113, v113
	v_pk_mul_f32 v[116:117], v[144:145], v[116:117] op_sel_hi:[0,1]
	s_or_b32 s0, s0, s6
	s_lshl_b64 s[6:7], s[0:1], 14
	v_pk_fma_f32 v[130:131], v[130:131], v[112:113], v[114:115]
	v_pk_mul_f32 v[112:113], v[20:21], v[10:11] op_sel_hi:[0,1]
	v_exp_f32_e32 v112, v112
	v_exp_f32_e32 v113, v113
	v_pk_mul_f32 v[114:115], v[20:21], v[12:13] op_sel_hi:[0,1]
	v_exp_f32_e32 v114, v114
	v_exp_f32_e32 v115, v115
	v_pk_fma_f32 v[132:133], v[132:133], v[112:113], v[116:117]
	v_pk_mul_f32 v[112:113], v[144:145], v[118:119] op_sel_hi:[0,1]
	v_pk_mul_f32 v[116:117], v[144:145], v[120:121] op_sel_hi:[0,1]
	v_pk_fma_f32 v[134:135], v[134:135], v[114:115], v[112:113]
	v_pk_mul_f32 v[112:113], v[20:21], v[6:7] op_sel_hi:[0,1]
	v_exp_f32_e32 v112, v112
	v_exp_f32_e32 v113, v113
	v_pk_mul_f32 v[114:115], v[20:21], v[8:9] op_sel_hi:[0,1]
	v_exp_f32_e32 v114, v114
	v_exp_f32_e32 v115, v115
	v_pk_fma_f32 v[136:137], v[136:137], v[112:113], v[116:117]
	v_pk_mul_f32 v[112:113], v[144:145], v[122:123] op_sel_hi:[0,1]
	v_pk_mul_f32 v[116:117], v[144:145], v[124:125] op_sel_hi:[0,1]
	v_pk_fma_f32 v[138:139], v[138:139], v[114:115], v[112:113]
	v_pk_mul_f32 v[112:113], v[20:21], v[2:3] op_sel_hi:[0,1]
	v_exp_f32_e32 v112, v112
	v_exp_f32_e32 v113, v113
	v_pk_mul_f32 v[114:115], v[20:21], v[4:5] op_sel_hi:[0,1]
	v_exp_f32_e32 v114, v114
	v_exp_f32_e32 v115, v115
	v_pk_fma_f32 v[140:141], v[140:141], v[112:113], v[116:117]
	v_pk_mul_f32 v[112:113], v[144:145], v[126:127] op_sel_hi:[0,1]
	s_lshl_b64 s[0:1], s[0:1], 11
	v_pk_fma_f32 v[104:105], v[104:105], v[114:115], v[112:113]
	s_add_u32 s0, s2, s0
	s_waitcnt lgkmcnt(0)
	s_addc_u32 s1, s3, s1
	ds_read_b128 v[112:115], v160 offset:41648
	ds_read_b128 v[116:119], v160 offset:41664
	ds_read_b128 v[120:123], v160 offset:41680
	ds_read_b128 v[124:127], v160 offset:41696
	v_pk_mul_f32 v[142:143], v[22:23], v[14:15] op_sel_hi:[0,1]
	v_exp_f32_e32 v142, v142
	v_exp_f32_e32 v143, v143
	v_mul_f32_e32 v144, v22, v23
	v_pk_mul_f32 v[92:93], v[144:145], v[92:93] op_sel_hi:[0,1]
	v_pk_mul_f32 v[94:95], v[144:145], v[94:95] op_sel_hi:[0,1]
	v_pk_fma_f32 v[128:129], v[128:129], v[142:143], v[92:93]
	v_pk_mul_f32 v[92:93], v[22:23], v[16:17] op_sel_hi:[0,1]
	v_exp_f32_e32 v92, v92
	v_exp_f32_e32 v93, v93
	v_pk_mul_f32 v[96:97], v[144:145], v[96:97] op_sel_hi:[0,1]
	v_pk_fma_f32 v[130:131], v[130:131], v[92:93], v[94:95]
	v_pk_mul_f32 v[92:93], v[22:23], v[10:11] op_sel_hi:[0,1]
	v_exp_f32_e32 v92, v92
	v_exp_f32_e32 v93, v93
	v_pk_mul_f32 v[94:95], v[22:23], v[12:13] op_sel_hi:[0,1]
	v_exp_f32_e32 v94, v94
	v_exp_f32_e32 v95, v95
	v_pk_fma_f32 v[132:133], v[132:133], v[92:93], v[96:97]
	v_pk_mul_f32 v[92:93], v[144:145], v[98:99] op_sel_hi:[0,1]
	v_pk_mul_f32 v[96:97], v[144:145], v[100:101] op_sel_hi:[0,1]
	v_pk_fma_f32 v[134:135], v[134:135], v[94:95], v[92:93]
	v_pk_mul_f32 v[92:93], v[22:23], v[6:7] op_sel_hi:[0,1]
	v_exp_f32_e32 v92, v92
	v_exp_f32_e32 v93, v93
	v_pk_mul_f32 v[94:95], v[22:23], v[8:9] op_sel_hi:[0,1]
	v_exp_f32_e32 v94, v94
	v_exp_f32_e32 v95, v95
	v_pk_fma_f32 v[136:137], v[136:137], v[92:93], v[96:97]
	v_pk_mul_f32 v[92:93], v[144:145], v[102:103] op_sel_hi:[0,1]
	v_pk_mul_f32 v[96:97], v[144:145], v[108:109] op_sel_hi:[0,1]
	v_pk_fma_f32 v[138:139], v[138:139], v[94:95], v[92:93]
	v_pk_mul_f32 v[92:93], v[22:23], v[2:3] op_sel_hi:[0,1]
	v_exp_f32_e32 v92, v92
	v_exp_f32_e32 v93, v93
	v_pk_mul_f32 v[94:95], v[22:23], v[4:5] op_sel_hi:[0,1]
	v_exp_f32_e32 v94, v94
	v_exp_f32_e32 v95, v95
	v_pk_fma_f32 v[140:141], v[140:141], v[92:93], v[96:97]
	v_pk_mul_f32 v[92:93], v[144:145], v[110:111] op_sel_hi:[0,1]
	v_pk_fma_f32 v[104:105], v[104:105], v[94:95], v[92:93]
	s_nop 0
	s_waitcnt lgkmcnt(0)
	s_nop 0
	ds_read_b128 v[92:95], v160 offset:41856
	ds_read_b128 v[96:99], v160 offset:41872
	ds_read_b128 v[100:103], v160 offset:41888
	ds_read_b128 v[108:111], v160 offset:41904
	v_pk_mul_f32 v[142:143], v[24:25], v[14:15] op_sel_hi:[0,1]
	v_exp_f32_e32 v142, v142
	v_exp_f32_e32 v143, v143
	v_mul_f32_e32 v90, v24, v90
	v_pk_mul_f32 v[112:113], v[90:91], v[112:113] op_sel_hi:[0,1]
	v_pk_mul_f32 v[114:115], v[90:91], v[114:115] op_sel_hi:[0,1]
	v_pk_fma_f32 v[128:129], v[128:129], v[142:143], v[112:113]
	v_pk_mul_f32 v[112:113], v[24:25], v[16:17] op_sel_hi:[0,1]
	v_exp_f32_e32 v112, v112
	v_exp_f32_e32 v113, v113
	v_pk_mul_f32 v[116:117], v[90:91], v[116:117] op_sel_hi:[0,1]
	v_pk_fma_f32 v[130:131], v[130:131], v[112:113], v[114:115]
	v_pk_mul_f32 v[112:113], v[24:25], v[10:11] op_sel_hi:[0,1]
	v_exp_f32_e32 v112, v112
	v_exp_f32_e32 v113, v113
	v_pk_mul_f32 v[114:115], v[24:25], v[12:13] op_sel_hi:[0,1]
	v_exp_f32_e32 v114, v114
	v_exp_f32_e32 v115, v115
	v_pk_fma_f32 v[132:133], v[132:133], v[112:113], v[116:117]
	v_pk_mul_f32 v[112:113], v[90:91], v[118:119] op_sel_hi:[0,1]
	v_pk_mul_f32 v[116:117], v[90:91], v[120:121] op_sel_hi:[0,1]
	v_pk_fma_f32 v[134:135], v[134:135], v[114:115], v[112:113]
	v_pk_mul_f32 v[112:113], v[24:25], v[6:7] op_sel_hi:[0,1]
	v_exp_f32_e32 v112, v112
	v_exp_f32_e32 v113, v113
	v_pk_mul_f32 v[114:115], v[24:25], v[8:9] op_sel_hi:[0,1]
	v_exp_f32_e32 v114, v114
	v_exp_f32_e32 v115, v115
	v_pk_fma_f32 v[136:137], v[136:137], v[112:113], v[116:117]
	v_pk_mul_f32 v[112:113], v[90:91], v[122:123] op_sel_hi:[0,1]
	v_pk_mul_f32 v[116:117], v[90:91], v[124:125] op_sel_hi:[0,1]
	v_pk_fma_f32 v[138:139], v[138:139], v[114:115], v[112:113]
	v_pk_mul_f32 v[112:113], v[24:25], v[2:3] op_sel_hi:[0,1]
	v_pk_mul_f32 v[114:115], v[24:25], v[4:5] op_sel_hi:[0,1]
	v_exp_f32_e32 v112, v112
	v_exp_f32_e32 v113, v113
	v_exp_f32_e32 v114, v114
	v_exp_f32_e32 v115, v115
	v_pk_mul_f32 v[90:91], v[90:91], v[126:127] op_sel_hi:[0,1]
	v_pk_fma_f32 v[140:141], v[140:141], v[112:113], v[116:117]
	v_pk_fma_f32 v[90:91], v[104:105], v[114:115], v[90:91]
	s_nop 0
	s_waitcnt lgkmcnt(0)
	s_nop 0
	ds_read_b128 v[112:115], v160 offset:42064
	ds_read_b128 v[116:119], v160 offset:42080
	ds_read_b128 v[120:123], v160 offset:42096
	ds_read_b128 v[124:127], v160 offset:42112
	v_pk_mul_f32 v[104:105], v[26:27], v[14:15] op_sel_hi:[0,1]
	v_exp_f32_e32 v104, v104
	v_exp_f32_e32 v105, v105
	v_mul_f32_e32 v142, v26, v89
	v_pk_mul_f32 v[92:93], v[142:143], v[92:93] op_sel_hi:[0,1]
	v_pk_mul_f32 v[94:95], v[142:143], v[94:95] op_sel_hi:[0,1]
	v_pk_fma_f32 v[128:129], v[128:129], v[104:105], v[92:93]
	v_pk_mul_f32 v[92:93], v[26:27], v[16:17] op_sel_hi:[0,1]
	v_exp_f32_e32 v92, v92
	v_exp_f32_e32 v93, v93
	v_pk_mul_f32 v[96:97], v[142:143], v[96:97] op_sel_hi:[0,1]
	v_pk_fma_f32 v[130:131], v[130:131], v[92:93], v[94:95]
	v_pk_mul_f32 v[92:93], v[26:27], v[10:11] op_sel_hi:[0,1]
	v_exp_f32_e32 v92, v92
	v_exp_f32_e32 v93, v93
	v_pk_mul_f32 v[94:95], v[26:27], v[12:13] op_sel_hi:[0,1]
	v_exp_f32_e32 v94, v94
	v_exp_f32_e32 v95, v95
	v_pk_fma_f32 v[132:133], v[132:133], v[92:93], v[96:97]
	v_pk_mul_f32 v[92:93], v[142:143], v[98:99] op_sel_hi:[0,1]
	v_pk_mul_f32 v[96:97], v[142:143], v[100:101] op_sel_hi:[0,1]
	v_pk_fma_f32 v[134:135], v[134:135], v[94:95], v[92:93]
	v_pk_mul_f32 v[92:93], v[26:27], v[6:7] op_sel_hi:[0,1]
	v_exp_f32_e32 v92, v92
	v_exp_f32_e32 v93, v93
	v_pk_mul_f32 v[94:95], v[26:27], v[8:9] op_sel_hi:[0,1]
	v_exp_f32_e32 v94, v94
	v_exp_f32_e32 v95, v95
	v_pk_fma_f32 v[136:137], v[136:137], v[92:93], v[96:97]
	v_pk_mul_f32 v[92:93], v[142:143], v[102:103] op_sel_hi:[0,1]
	v_pk_mul_f32 v[96:97], v[142:143], v[108:109] op_sel_hi:[0,1]
	v_pk_fma_f32 v[138:139], v[138:139], v[94:95], v[92:93]
	v_pk_mul_f32 v[92:93], v[26:27], v[2:3] op_sel_hi:[0,1]
	v_exp_f32_e32 v92, v92
	v_exp_f32_e32 v93, v93
	v_pk_mul_f32 v[94:95], v[26:27], v[4:5] op_sel_hi:[0,1]
	v_exp_f32_e32 v94, v94
	v_exp_f32_e32 v95, v95
	v_pk_fma_f32 v[108:109], v[140:141], v[92:93], v[96:97]
	v_pk_mul_f32 v[92:93], v[142:143], v[110:111] op_sel_hi:[0,1]
	v_pk_fma_f32 v[110:111], v[90:91], v[94:95], v[92:93]
	s_nop 0
	s_waitcnt lgkmcnt(0)
	s_nop 0
	ds_read_b128 v[90:93], v160 offset:42272
	ds_read_b128 v[94:97], v160 offset:42288
	ds_read_b128 v[98:101], v160 offset:42304
	ds_read_b128 v[102:105], v160 offset:42320
	v_pk_mul_f32 v[140:141], v[28:29], v[14:15] op_sel_hi:[0,1]
	v_exp_f32_e32 v140, v140
	v_exp_f32_e32 v141, v141
	v_pk_mul_f32 v[142:143], v[28:29], v[16:17] op_sel_hi:[0,1]
	v_exp_f32_e32 v142, v142
	v_exp_f32_e32 v143, v143
	v_mul_f32_e32 v88, v28, v88
	v_pk_mul_f32 v[112:113], v[88:89], v[112:113] op_sel_hi:[0,1]
	v_pk_fma_f32 v[128:129], v[128:129], v[140:141], v[112:113]
	v_pk_mul_f32 v[112:113], v[88:89], v[114:115] op_sel_hi:[0,1]
	v_pk_fma_f32 v[130:131], v[130:131], v[142:143], v[112:113]
	v_pk_mul_f32 v[112:113], v[28:29], v[10:11] op_sel_hi:[0,1]
	v_exp_f32_e32 v112, v112
	v_exp_f32_e32 v113, v113
	v_pk_mul_f32 v[114:115], v[28:29], v[12:13] op_sel_hi:[0,1]
	v_exp_f32_e32 v114, v114
	v_exp_f32_e32 v115, v115
	v_pk_mul_f32 v[116:117], v[88:89], v[116:117] op_sel_hi:[0,1]
	v_pk_fma_f32 v[132:133], v[132:133], v[112:113], v[116:117]
	v_pk_mul_f32 v[112:113], v[88:89], v[118:119] op_sel_hi:[0,1]
	v_pk_fma_f32 v[134:135], v[134:135], v[114:115], v[112:113]
	v_pk_mul_f32 v[112:113], v[28:29], v[6:7] op_sel_hi:[0,1]
	v_exp_f32_e32 v112, v112
	v_exp_f32_e32 v113, v113
	v_pk_mul_f32 v[114:115], v[28:29], v[8:9] op_sel_hi:[0,1]
	v_exp_f32_e32 v114, v114
	v_exp_f32_e32 v115, v115
	v_pk_mul_f32 v[116:117], v[88:89], v[120:121] op_sel_hi:[0,1]
	v_pk_fma_f32 v[136:137], v[136:137], v[112:113], v[116:117]
	v_pk_mul_f32 v[112:113], v[88:89], v[122:123] op_sel_hi:[0,1]
	v_pk_fma_f32 v[138:139], v[138:139], v[114:115], v[112:113]
	v_pk_mul_f32 v[112:113], v[28:29], v[2:3] op_sel_hi:[0,1]
	v_pk_mul_f32 v[114:115], v[28:29], v[4:5] op_sel_hi:[0,1]
	v_exp_f32_e32 v112, v112
	v_exp_f32_e32 v113, v113
	v_exp_f32_e32 v114, v114
	v_exp_f32_e32 v115, v115
	v_pk_mul_f32 v[116:117], v[88:89], v[124:125] op_sel_hi:[0,1]
	v_pk_mul_f32 v[88:89], v[88:89], v[126:127] op_sel_hi:[0,1]
	v_pk_fma_f32 v[124:125], v[108:109], v[112:113], v[116:117]
	v_pk_fma_f32 v[88:89], v[110:111], v[114:115], v[88:89]
	s_nop 0
	s_waitcnt lgkmcnt(0)
	s_nop 0
	ds_read_b128 v[108:111], v160 offset:42480
	ds_read_b128 v[112:115], v160 offset:42496
	ds_read_b128 v[116:119], v160 offset:42512
	ds_read_b128 v[120:123], v160 offset:42528
	v_pk_mul_f32 v[140:141], v[30:31], v[14:15] op_sel_hi:[0,1]
	v_exp_f32_e32 v140, v140
	v_exp_f32_e32 v141, v141
	v_pk_mul_f32 v[142:143], v[30:31], v[16:17] op_sel_hi:[0,1]
	v_exp_f32_e32 v142, v142
	v_exp_f32_e32 v143, v143
	v_mul_f32_e32 v126, v30, v25
	v_pk_mul_f32 v[90:91], v[126:127], v[90:91] op_sel_hi:[0,1]
	v_pk_fma_f32 v[128:129], v[128:129], v[140:141], v[90:91]
	v_pk_mul_f32 v[90:91], v[126:127], v[92:93] op_sel_hi:[0,1]
	v_pk_fma_f32 v[130:131], v[130:131], v[142:143], v[90:91]
	v_pk_mul_f32 v[90:91], v[30:31], v[10:11] op_sel_hi:[0,1]
	v_exp_f32_e32 v90, v90
	v_exp_f32_e32 v91, v91
	v_pk_mul_f32 v[92:93], v[30:31], v[12:13] op_sel_hi:[0,1]
	v_exp_f32_e32 v92, v92
	v_exp_f32_e32 v93, v93
	v_pk_mul_f32 v[94:95], v[126:127], v[94:95] op_sel_hi:[0,1]
	v_pk_fma_f32 v[132:133], v[132:133], v[90:91], v[94:95]
	v_pk_mul_f32 v[90:91], v[126:127], v[96:97] op_sel_hi:[0,1]
	v_pk_fma_f32 v[134:135], v[134:135], v[92:93], v[90:91]
	v_pk_mul_f32 v[90:91], v[30:31], v[6:7] op_sel_hi:[0,1]
	v_exp_f32_e32 v90, v90
	v_exp_f32_e32 v91, v91
	v_pk_mul_f32 v[92:93], v[30:31], v[8:9] op_sel_hi:[0,1]
	v_exp_f32_e32 v92, v92
	v_exp_f32_e32 v93, v93
	v_pk_mul_f32 v[94:95], v[126:127], v[98:99] op_sel_hi:[0,1]
	v_pk_fma_f32 v[136:137], v[136:137], v[90:91], v[94:95]
	v_pk_mul_f32 v[90:91], v[126:127], v[100:101] op_sel_hi:[0,1]
	v_pk_fma_f32 v[138:139], v[138:139], v[92:93], v[90:91]
	v_pk_mul_f32 v[90:91], v[30:31], v[2:3] op_sel_hi:[0,1]
	v_exp_f32_e32 v90, v90
	v_exp_f32_e32 v91, v91
	v_pk_mul_f32 v[92:93], v[30:31], v[4:5] op_sel_hi:[0,1]
	v_exp_f32_e32 v92, v92
	v_exp_f32_e32 v93, v93
	v_pk_mul_f32 v[94:95], v[126:127], v[102:103] op_sel_hi:[0,1]
	v_pk_fma_f32 v[124:125], v[124:125], v[90:91], v[94:95]
	v_pk_mul_f32 v[90:91], v[126:127], v[104:105] op_sel_hi:[0,1]
	v_pk_fma_f32 v[104:105], v[88:89], v[92:93], v[90:91]
	s_nop 0
	s_waitcnt lgkmcnt(0)
	s_nop 0
	ds_read_b128 v[88:91], v160 offset:42688
	ds_read_b128 v[92:95], v160 offset:42704
	ds_read_b128 v[96:99], v160 offset:42720
	ds_read_b128 v[100:103], v160 offset:42736
	v_pk_mul_f32 v[140:141], v[32:33], v[14:15] op_sel_hi:[0,1]
	v_exp_f32_e32 v140, v140
	v_exp_f32_e32 v141, v141
	v_pk_mul_f32 v[142:143], v[32:33], v[16:17] op_sel_hi:[0,1]
	v_exp_f32_e32 v142, v142
	v_exp_f32_e32 v143, v143
	v_mul_f32_e32 v126, v32, v87
	v_pk_mul_f32 v[108:109], v[126:127], v[108:109] op_sel_hi:[0,1]
	v_pk_fma_f32 v[128:129], v[128:129], v[140:141], v[108:109]
	v_pk_mul_f32 v[108:109], v[126:127], v[110:111] op_sel_hi:[0,1]
	v_pk_fma_f32 v[130:131], v[130:131], v[142:143], v[108:109]
	v_pk_mul_f32 v[108:109], v[32:33], v[10:11] op_sel_hi:[0,1]
	v_exp_f32_e32 v108, v108
	v_exp_f32_e32 v109, v109
	v_pk_mul_f32 v[110:111], v[32:33], v[12:13] op_sel_hi:[0,1]
	v_exp_f32_e32 v110, v110
	v_exp_f32_e32 v111, v111
	v_pk_mul_f32 v[112:113], v[126:127], v[112:113] op_sel_hi:[0,1]
	v_pk_fma_f32 v[132:133], v[132:133], v[108:109], v[112:113]
	v_pk_mul_f32 v[108:109], v[126:127], v[114:115] op_sel_hi:[0,1]
	v_pk_fma_f32 v[134:135], v[134:135], v[110:111], v[108:109]
	v_pk_mul_f32 v[108:109], v[32:33], v[6:7] op_sel_hi:[0,1]
	v_exp_f32_e32 v108, v108
	v_exp_f32_e32 v109, v109
	v_pk_mul_f32 v[110:111], v[32:33], v[8:9] op_sel_hi:[0,1]
	v_exp_f32_e32 v110, v110
	v_exp_f32_e32 v111, v111
	v_pk_mul_f32 v[112:113], v[126:127], v[116:117] op_sel_hi:[0,1]
	v_pk_fma_f32 v[136:137], v[136:137], v[108:109], v[112:113]
	v_pk_mul_f32 v[108:109], v[126:127], v[118:119] op_sel_hi:[0,1]
	v_pk_fma_f32 v[138:139], v[138:139], v[110:111], v[108:109]
	v_pk_mul_f32 v[108:109], v[32:33], v[2:3] op_sel_hi:[0,1]
	v_exp_f32_e32 v108, v108
	v_exp_f32_e32 v109, v109
	v_pk_mul_f32 v[110:111], v[32:33], v[4:5] op_sel_hi:[0,1]
	v_exp_f32_e32 v110, v110
	v_exp_f32_e32 v111, v111
	v_pk_mul_f32 v[112:113], v[126:127], v[120:121] op_sel_hi:[0,1]
	v_pk_fma_f32 v[124:125], v[124:125], v[108:109], v[112:113]
	v_pk_mul_f32 v[108:109], v[126:127], v[122:123] op_sel_hi:[0,1]
	v_pk_fma_f32 v[104:105], v[104:105], v[110:111], v[108:109]
	s_nop 0
	s_waitcnt lgkmcnt(0)
	s_nop 0
	ds_read_b128 v[108:111], v160 offset:42896
	ds_read_b128 v[112:115], v160 offset:42912
	ds_read_b128 v[116:119], v160 offset:42928
	ds_read_b128 v[120:123], v160 offset:42944
	v_pk_mul_f32 v[126:127], v[34:35], v[14:15] op_sel_hi:[0,1]
	v_exp_f32_e32 v126, v126
	v_exp_f32_e32 v127, v127
	v_pk_mul_f32 v[140:141], v[34:35], v[16:17] op_sel_hi:[0,1]
	v_exp_f32_e32 v140, v140
	v_exp_f32_e32 v141, v141
	v_mul_f32_e32 v86, v34, v86
	v_pk_mul_f32 v[88:89], v[86:87], v[88:89] op_sel_hi:[0,1]
	v_pk_fma_f32 v[126:127], v[128:129], v[126:127], v[88:89]
	v_pk_mul_f32 v[88:89], v[86:87], v[90:91] op_sel_hi:[0,1]
	v_pk_fma_f32 v[128:129], v[130:131], v[140:141], v[88:89]
	v_pk_mul_f32 v[88:89], v[34:35], v[10:11] op_sel_hi:[0,1]
	v_exp_f32_e32 v88, v88
	v_exp_f32_e32 v89, v89
	v_pk_mul_f32 v[90:91], v[34:35], v[12:13] op_sel_hi:[0,1]
	v_exp_f32_e32 v90, v90
	v_exp_f32_e32 v91, v91
	v_pk_mul_f32 v[92:93], v[86:87], v[92:93] op_sel_hi:[0,1]
	v_pk_fma_f32 v[130:131], v[132:133], v[88:89], v[92:93]
	v_pk_mul_f32 v[88:89], v[86:87], v[94:95] op_sel_hi:[0,1]
	v_pk_fma_f32 v[132:133], v[134:135], v[90:91], v[88:89]
	v_pk_mul_f32 v[88:89], v[34:35], v[6:7] op_sel_hi:[0,1]
	v_exp_f32_e32 v88, v88
	v_exp_f32_e32 v89, v89
	v_pk_mul_f32 v[90:91], v[34:35], v[8:9] op_sel_hi:[0,1]
	v_exp_f32_e32 v90, v90
	v_exp_f32_e32 v91, v91
	v_pk_mul_f32 v[92:93], v[86:87], v[96:97] op_sel_hi:[0,1]
	v_pk_fma_f32 v[134:135], v[136:137], v[88:89], v[92:93]
	v_pk_mul_f32 v[88:89], v[86:87], v[98:99] op_sel_hi:[0,1]
	v_pk_fma_f32 v[136:137], v[138:139], v[90:91], v[88:89]
	v_pk_mul_f32 v[88:89], v[34:35], v[2:3] op_sel_hi:[0,1]
	v_pk_mul_f32 v[90:91], v[34:35], v[4:5] op_sel_hi:[0,1]
	v_exp_f32_e32 v88, v88
	v_exp_f32_e32 v89, v89
	v_exp_f32_e32 v90, v90
	v_exp_f32_e32 v91, v91
	v_pk_mul_f32 v[92:93], v[86:87], v[100:101] op_sel_hi:[0,1]
	v_pk_mul_f32 v[86:87], v[86:87], v[102:103] op_sel_hi:[0,1]
	v_pk_fma_f32 v[124:125], v[124:125], v[88:89], v[92:93]
	v_pk_fma_f32 v[102:103], v[104:105], v[90:91], v[86:87]
	s_nop 0
	s_waitcnt lgkmcnt(0)
	s_nop 0
	ds_read_b128 v[86:89], v160 offset:43104
	ds_read_b128 v[90:93], v160 offset:43120
	ds_read_b128 v[94:97], v160 offset:43136
	ds_read_b128 v[98:101], v160 offset:43152
	v_pk_mul_f32 v[138:139], v[36:37], v[14:15] op_sel_hi:[0,1]
	v_exp_f32_e32 v138, v138
	v_exp_f32_e32 v139, v139
	v_pk_mul_f32 v[140:141], v[36:37], v[16:17] op_sel_hi:[0,1]
	v_exp_f32_e32 v140, v140
	v_exp_f32_e32 v141, v141
	v_mul_f32_e32 v104, v36, v85
	v_pk_mul_f32 v[108:109], v[104:105], v[108:109] op_sel_hi:[0,1]
	v_pk_fma_f32 v[126:127], v[126:127], v[138:139], v[108:109]
	v_pk_mul_f32 v[108:109], v[104:105], v[110:111] op_sel_hi:[0,1]
	v_pk_fma_f32 v[128:129], v[128:129], v[140:141], v[108:109]
	v_pk_mul_f32 v[108:109], v[36:37], v[10:11] op_sel_hi:[0,1]
	v_exp_f32_e32 v108, v108
	v_exp_f32_e32 v109, v109
	v_pk_mul_f32 v[110:111], v[36:37], v[12:13] op_sel_hi:[0,1]
	v_exp_f32_e32 v110, v110
	v_exp_f32_e32 v111, v111
	v_pk_mul_f32 v[112:113], v[104:105], v[112:113] op_sel_hi:[0,1]
	v_pk_fma_f32 v[130:131], v[130:131], v[108:109], v[112:113]
	v_pk_mul_f32 v[108:109], v[104:105], v[114:115] op_sel_hi:[0,1]
	v_pk_fma_f32 v[132:133], v[132:133], v[110:111], v[108:109]
	v_pk_mul_f32 v[108:109], v[36:37], v[6:7] op_sel_hi:[0,1]
	v_exp_f32_e32 v108, v108
	v_exp_f32_e32 v109, v109
	v_pk_mul_f32 v[110:111], v[36:37], v[8:9] op_sel_hi:[0,1]
	v_exp_f32_e32 v110, v110
	v_exp_f32_e32 v111, v111
	v_pk_mul_f32 v[112:113], v[104:105], v[116:117] op_sel_hi:[0,1]
	v_pk_fma_f32 v[134:135], v[134:135], v[108:109], v[112:113]
	v_pk_mul_f32 v[108:109], v[104:105], v[118:119] op_sel_hi:[0,1]
	v_pk_fma_f32 v[136:137], v[136:137], v[110:111], v[108:109]
	v_pk_mul_f32 v[108:109], v[36:37], v[2:3] op_sel_hi:[0,1]
	v_pk_mul_f32 v[110:111], v[36:37], v[4:5] op_sel_hi:[0,1]
	v_exp_f32_e32 v108, v108
	v_exp_f32_e32 v109, v109
	v_exp_f32_e32 v110, v110
	v_exp_f32_e32 v111, v111
	v_pk_mul_f32 v[112:113], v[104:105], v[120:121] op_sel_hi:[0,1]
	v_pk_mul_f32 v[104:105], v[104:105], v[122:123] op_sel_hi:[0,1]
	v_pk_fma_f32 v[120:121], v[124:125], v[108:109], v[112:113]
	v_pk_fma_f32 v[122:123], v[102:103], v[110:111], v[104:105]
	s_nop 0
	s_waitcnt lgkmcnt(0)
	s_nop 0
	ds_read_b128 v[102:105], v160 offset:43312
	ds_read_b128 v[108:111], v160 offset:43328
	ds_read_b128 v[112:115], v160 offset:43344
	ds_read_b128 v[116:119], v160 offset:43360
	v_pk_mul_f32 v[124:125], v[38:39], v[14:15] op_sel_hi:[0,1]
	v_exp_f32_e32 v124, v124
	v_exp_f32_e32 v125, v125
	v_pk_mul_f32 v[138:139], v[38:39], v[16:17] op_sel_hi:[0,1]
	v_exp_f32_e32 v138, v138
	v_exp_f32_e32 v139, v139
	v_mul_f32_e32 v84, v38, v84
	v_pk_mul_f32 v[86:87], v[84:85], v[86:87] op_sel_hi:[0,1]
	v_pk_fma_f32 v[124:125], v[126:127], v[124:125], v[86:87]
	v_pk_mul_f32 v[86:87], v[84:85], v[88:89] op_sel_hi:[0,1]
	v_pk_fma_f32 v[126:127], v[128:129], v[138:139], v[86:87]
	v_pk_mul_f32 v[86:87], v[38:39], v[10:11] op_sel_hi:[0,1]
	v_exp_f32_e32 v86, v86
	v_exp_f32_e32 v87, v87
	v_pk_mul_f32 v[88:89], v[38:39], v[12:13] op_sel_hi:[0,1]
	v_exp_f32_e32 v88, v88
	v_exp_f32_e32 v89, v89
	v_pk_mul_f32 v[90:91], v[84:85], v[90:91] op_sel_hi:[0,1]
	v_pk_fma_f32 v[128:129], v[130:131], v[86:87], v[90:91]
	v_pk_mul_f32 v[86:87], v[84:85], v[92:93] op_sel_hi:[0,1]
	v_pk_fma_f32 v[130:131], v[132:133], v[88:89], v[86:87]
	v_pk_mul_f32 v[86:87], v[38:39], v[6:7] op_sel_hi:[0,1]
	v_exp_f32_e32 v86, v86
	v_exp_f32_e32 v87, v87
	v_pk_mul_f32 v[88:89], v[38:39], v[8:9] op_sel_hi:[0,1]
	v_exp_f32_e32 v88, v88
	v_exp_f32_e32 v89, v89
	v_pk_mul_f32 v[90:91], v[84:85], v[94:95] op_sel_hi:[0,1]
	v_pk_fma_f32 v[132:133], v[134:135], v[86:87], v[90:91]
	v_pk_mul_f32 v[86:87], v[84:85], v[96:97] op_sel_hi:[0,1]
	v_pk_fma_f32 v[134:135], v[136:137], v[88:89], v[86:87]
	v_pk_mul_f32 v[86:87], v[38:39], v[2:3] op_sel_hi:[0,1]
	v_pk_mul_f32 v[88:89], v[38:39], v[4:5] op_sel_hi:[0,1]
	v_exp_f32_e32 v86, v86
	v_exp_f32_e32 v87, v87
	v_exp_f32_e32 v88, v88
	v_exp_f32_e32 v89, v89
	v_pk_mul_f32 v[90:91], v[84:85], v[98:99] op_sel_hi:[0,1]
	v_pk_mul_f32 v[84:85], v[84:85], v[100:101] op_sel_hi:[0,1]
	v_pk_fma_f32 v[120:121], v[120:121], v[86:87], v[90:91]
	v_pk_fma_f32 v[100:101], v[122:123], v[88:89], v[84:85]
	s_nop 0
	s_waitcnt lgkmcnt(0)
	s_nop 0
	ds_read_b128 v[84:87], v160 offset:43520
	ds_read_b128 v[88:91], v160 offset:43536
	ds_read_b128 v[92:95], v160 offset:43552
	ds_read_b128 v[96:99], v160 offset:43568
	v_pk_mul_f32 v[136:137], v[40:41], v[14:15] op_sel_hi:[0,1]
	v_exp_f32_e32 v136, v136
	v_exp_f32_e32 v137, v137
	v_pk_mul_f32 v[138:139], v[40:41], v[16:17] op_sel_hi:[0,1]
	v_exp_f32_e32 v138, v138
	v_exp_f32_e32 v139, v139
	v_mul_f32_e32 v122, v40, v83
	v_pk_mul_f32 v[102:103], v[122:123], v[102:103] op_sel_hi:[0,1]
	v_pk_fma_f32 v[124:125], v[124:125], v[136:137], v[102:103]
	v_pk_mul_f32 v[102:103], v[122:123], v[104:105] op_sel_hi:[0,1]
	v_pk_fma_f32 v[104:105], v[126:127], v[138:139], v[102:103]
	v_pk_mul_f32 v[102:103], v[40:41], v[10:11] op_sel_hi:[0,1]
	v_exp_f32_e32 v102, v102
	v_exp_f32_e32 v103, v103
	v_pk_mul_f32 v[126:127], v[40:41], v[12:13] op_sel_hi:[0,1]
	v_exp_f32_e32 v126, v126
	v_exp_f32_e32 v127, v127
	v_pk_mul_f32 v[108:109], v[122:123], v[108:109] op_sel_hi:[0,1]
	v_pk_fma_f32 v[128:129], v[128:129], v[102:103], v[108:109]
	v_pk_mul_f32 v[102:103], v[122:123], v[110:111] op_sel_hi:[0,1]
	v_pk_fma_f32 v[126:127], v[130:131], v[126:127], v[102:103]
	v_pk_mul_f32 v[102:103], v[40:41], v[6:7] op_sel_hi:[0,1]
	v_exp_f32_e32 v102, v102
	v_exp_f32_e32 v103, v103
	v_pk_mul_f32 v[108:109], v[40:41], v[8:9] op_sel_hi:[0,1]
	v_exp_f32_e32 v108, v108
	v_exp_f32_e32 v109, v109
	v_pk_mul_f32 v[110:111], v[122:123], v[112:113] op_sel_hi:[0,1]
	v_pk_fma_f32 v[130:131], v[132:133], v[102:103], v[110:111]
	v_pk_mul_f32 v[102:103], v[122:123], v[114:115] op_sel_hi:[0,1]
	v_pk_fma_f32 v[132:133], v[134:135], v[108:109], v[102:103]
	v_pk_mul_f32 v[102:103], v[40:41], v[2:3] op_sel_hi:[0,1]
	v_exp_f32_e32 v102, v102
	v_exp_f32_e32 v103, v103
	v_pk_mul_f32 v[108:109], v[40:41], v[4:5] op_sel_hi:[0,1]
	v_exp_f32_e32 v108, v108
	v_exp_f32_e32 v109, v109
	v_pk_mul_f32 v[110:111], v[122:123], v[116:117] op_sel_hi:[0,1]
	v_pk_fma_f32 v[120:121], v[120:121], v[102:103], v[110:111]
	v_pk_mul_f32 v[102:103], v[122:123], v[118:119] op_sel_hi:[0,1]
	v_pk_fma_f32 v[122:123], v[100:101], v[108:109], v[102:103]
	s_nop 0
	s_waitcnt lgkmcnt(0)
	s_nop 0
	ds_read_b128 v[100:103], v160 offset:43728
	ds_read_b128 v[108:111], v160 offset:43744
	ds_read_b128 v[112:115], v160 offset:43760
	ds_read_b128 v[116:119], v160 offset:43776
	v_pk_mul_f32 v[134:135], v[42:43], v[14:15] op_sel_hi:[0,1]
	v_exp_f32_e32 v134, v134
	v_exp_f32_e32 v135, v135
	v_pk_mul_f32 v[136:137], v[42:43], v[16:17] op_sel_hi:[0,1]
	v_exp_f32_e32 v136, v136
	v_exp_f32_e32 v137, v137
	v_mul_f32_e32 v82, v42, v82
	v_pk_mul_f32 v[84:85], v[82:83], v[84:85] op_sel_hi:[0,1]
	v_pk_fma_f32 v[124:125], v[124:125], v[134:135], v[84:85]
	v_pk_mul_f32 v[84:85], v[82:83], v[86:87] op_sel_hi:[0,1]
	v_pk_fma_f32 v[104:105], v[104:105], v[136:137], v[84:85]
	v_pk_mul_f32 v[84:85], v[42:43], v[10:11] op_sel_hi:[0,1]
	v_exp_f32_e32 v84, v84
	v_exp_f32_e32 v85, v85
	v_pk_mul_f32 v[86:87], v[42:43], v[12:13] op_sel_hi:[0,1]
	v_exp_f32_e32 v86, v86
	v_exp_f32_e32 v87, v87
	v_pk_mul_f32 v[88:89], v[82:83], v[88:89] op_sel_hi:[0,1]
	v_pk_fma_f32 v[128:129], v[128:129], v[84:85], v[88:89]
	v_pk_mul_f32 v[84:85], v[82:83], v[90:91] op_sel_hi:[0,1]
	v_pk_fma_f32 v[126:127], v[126:127], v[86:87], v[84:85]
	v_pk_mul_f32 v[84:85], v[42:43], v[6:7] op_sel_hi:[0,1]
	v_exp_f32_e32 v84, v84
	v_exp_f32_e32 v85, v85
	v_pk_mul_f32 v[86:87], v[42:43], v[8:9] op_sel_hi:[0,1]
	v_exp_f32_e32 v86, v86
	v_exp_f32_e32 v87, v87
	v_pk_mul_f32 v[88:89], v[82:83], v[92:93] op_sel_hi:[0,1]
	v_pk_fma_f32 v[130:131], v[130:131], v[84:85], v[88:89]
	v_pk_mul_f32 v[84:85], v[82:83], v[94:95] op_sel_hi:[0,1]
	v_pk_fma_f32 v[132:133], v[132:133], v[86:87], v[84:85]
	v_pk_mul_f32 v[84:85], v[42:43], v[2:3] op_sel_hi:[0,1]
	v_pk_mul_f32 v[86:87], v[42:43], v[4:5] op_sel_hi:[0,1]
	v_exp_f32_e32 v84, v84
	v_exp_f32_e32 v85, v85
	v_exp_f32_e32 v86, v86
	v_exp_f32_e32 v87, v87
	v_pk_mul_f32 v[88:89], v[82:83], v[96:97] op_sel_hi:[0,1]
	v_pk_mul_f32 v[82:83], v[82:83], v[98:99] op_sel_hi:[0,1]
	v_pk_fma_f32 v[120:121], v[120:121], v[84:85], v[88:89]
	v_pk_fma_f32 v[98:99], v[122:123], v[86:87], v[82:83]
	s_nop 0
	s_waitcnt lgkmcnt(0)
	s_nop 0
	ds_read_b128 v[82:85], v160 offset:43936
	ds_read_b128 v[86:89], v160 offset:43952
	ds_read_b128 v[90:93], v160 offset:43968
	ds_read_b128 v[94:97], v160 offset:43984
	v_pk_mul_f32 v[134:135], v[44:45], v[14:15] op_sel_hi:[0,1]
	v_exp_f32_e32 v134, v134
	v_exp_f32_e32 v135, v135
	v_pk_mul_f32 v[136:137], v[44:45], v[16:17] op_sel_hi:[0,1]
	v_exp_f32_e32 v136, v136
	v_exp_f32_e32 v137, v137
	v_mul_f32_e32 v122, v44, v81
	v_pk_mul_f32 v[100:101], v[122:123], v[100:101] op_sel_hi:[0,1]
	v_pk_fma_f32 v[124:125], v[124:125], v[134:135], v[100:101]
	v_pk_mul_f32 v[100:101], v[122:123], v[102:103] op_sel_hi:[0,1]
	v_pk_fma_f32 v[134:135], v[104:105], v[136:137], v[100:101]
	v_pk_mul_f32 v[100:101], v[44:45], v[10:11] op_sel_hi:[0,1]
	v_exp_f32_e32 v100, v100
	v_exp_f32_e32 v101, v101
	v_pk_mul_f32 v[102:103], v[44:45], v[12:13] op_sel_hi:[0,1]
	v_exp_f32_e32 v102, v102
	v_exp_f32_e32 v103, v103
	v_pk_mul_f32 v[104:105], v[122:123], v[108:109] op_sel_hi:[0,1]
	v_pk_fma_f32 v[128:129], v[128:129], v[100:101], v[104:105]
	v_pk_mul_f32 v[100:101], v[122:123], v[110:111] op_sel_hi:[0,1]
	v_pk_fma_f32 v[126:127], v[126:127], v[102:103], v[100:101]
	v_pk_mul_f32 v[100:101], v[44:45], v[6:7] op_sel_hi:[0,1]
	v_exp_f32_e32 v100, v100
	v_exp_f32_e32 v101, v101
	v_pk_mul_f32 v[102:103], v[44:45], v[8:9] op_sel_hi:[0,1]
	v_exp_f32_e32 v102, v102
	v_exp_f32_e32 v103, v103
	v_pk_mul_f32 v[104:105], v[122:123], v[112:113] op_sel_hi:[0,1]
	v_pk_fma_f32 v[130:131], v[130:131], v[100:101], v[104:105]
	v_pk_mul_f32 v[100:101], v[122:123], v[114:115] op_sel_hi:[0,1]
	v_pk_fma_f32 v[132:133], v[132:133], v[102:103], v[100:101]
	v_pk_mul_f32 v[100:101], v[44:45], v[2:3] op_sel_hi:[0,1]
	v_exp_f32_e32 v100, v100
	v_exp_f32_e32 v101, v101
	v_pk_mul_f32 v[102:103], v[44:45], v[4:5] op_sel_hi:[0,1]
	v_exp_f32_e32 v102, v102
	v_exp_f32_e32 v103, v103
	v_pk_mul_f32 v[104:105], v[122:123], v[116:117] op_sel_hi:[0,1]
	v_pk_fma_f32 v[116:117], v[120:121], v[100:101], v[104:105]
	v_pk_mul_f32 v[100:101], v[122:123], v[118:119] op_sel_hi:[0,1]
	v_pk_fma_f32 v[118:119], v[98:99], v[102:103], v[100:101]
	s_nop 0
	s_waitcnt lgkmcnt(0)
	s_nop 0
	ds_read_b128 v[98:101], v160 offset:44144
	ds_read_b128 v[102:105], v160 offset:44160
	ds_read_b128 v[108:111], v160 offset:44176
	ds_read_b128 v[112:115], v160 offset:44192
	v_pk_mul_f32 v[122:123], v[46:47], v[14:15] op_sel_hi:[0,1]
	v_exp_f32_e32 v122, v122
	v_exp_f32_e32 v123, v123
	v_pk_mul_f32 v[136:137], v[46:47], v[16:17] op_sel_hi:[0,1]
	v_exp_f32_e32 v136, v136
	v_exp_f32_e32 v137, v137
	v_mul_f32_e32 v120, v46, v79
	v_pk_mul_f32 v[82:83], v[120:121], v[82:83] op_sel_hi:[0,1]
	v_pk_fma_f32 v[122:123], v[124:125], v[122:123], v[82:83]
	v_pk_mul_f32 v[82:83], v[120:121], v[84:85] op_sel_hi:[0,1]
	v_pk_fma_f32 v[124:125], v[134:135], v[136:137], v[82:83]
	v_pk_mul_f32 v[82:83], v[46:47], v[10:11] op_sel_hi:[0,1]
	v_exp_f32_e32 v82, v82
	v_exp_f32_e32 v83, v83
	v_pk_mul_f32 v[84:85], v[46:47], v[12:13] op_sel_hi:[0,1]
	v_exp_f32_e32 v84, v84
	v_exp_f32_e32 v85, v85
	v_pk_mul_f32 v[86:87], v[120:121], v[86:87] op_sel_hi:[0,1]
	v_pk_fma_f32 v[128:129], v[128:129], v[82:83], v[86:87]
	v_pk_mul_f32 v[82:83], v[120:121], v[88:89] op_sel_hi:[0,1]
	v_pk_fma_f32 v[126:127], v[126:127], v[84:85], v[82:83]
	v_pk_mul_f32 v[82:83], v[46:47], v[6:7] op_sel_hi:[0,1]
	v_exp_f32_e32 v82, v82
	v_exp_f32_e32 v83, v83
	v_pk_mul_f32 v[84:85], v[46:47], v[8:9] op_sel_hi:[0,1]
	v_exp_f32_e32 v84, v84
	v_exp_f32_e32 v85, v85
	v_pk_mul_f32 v[86:87], v[120:121], v[90:91] op_sel_hi:[0,1]
	v_pk_fma_f32 v[130:131], v[130:131], v[82:83], v[86:87]
	v_pk_mul_f32 v[82:83], v[120:121], v[92:93] op_sel_hi:[0,1]
	v_pk_fma_f32 v[132:133], v[132:133], v[84:85], v[82:83]
	v_pk_mul_f32 v[82:83], v[46:47], v[2:3] op_sel_hi:[0,1]
	v_exp_f32_e32 v82, v82
	v_exp_f32_e32 v83, v83
	v_pk_mul_f32 v[84:85], v[46:47], v[4:5] op_sel_hi:[0,1]
	v_exp_f32_e32 v84, v84
	v_exp_f32_e32 v85, v85
	v_pk_mul_f32 v[86:87], v[120:121], v[94:95] op_sel_hi:[0,1]
	v_pk_fma_f32 v[116:117], v[116:117], v[82:83], v[86:87]
	v_pk_mul_f32 v[82:83], v[120:121], v[96:97] op_sel_hi:[0,1]
	v_pk_fma_f32 v[118:119], v[118:119], v[84:85], v[82:83]
	s_nop 0
	s_waitcnt lgkmcnt(0)
	s_nop 0
	ds_read_b128 v[82:85], v160 offset:44352
	ds_read_b128 v[86:89], v160 offset:44368
	ds_read_b128 v[90:93], v160 offset:44384
	ds_read_b128 v[94:97], v160 offset:44400
	v_pk_mul_f32 v[134:135], v[48:49], v[14:15] op_sel_hi:[0,1]
	v_exp_f32_e32 v134, v134
	v_exp_f32_e32 v135, v135
	v_pk_mul_f32 v[136:137], v[48:49], v[16:17] op_sel_hi:[0,1]
	v_exp_f32_e32 v136, v136
	v_exp_f32_e32 v137, v137
	v_mul_f32_e32 v120, v48, v77
	v_pk_mul_f32 v[98:99], v[120:121], v[98:99] op_sel_hi:[0,1]
	v_pk_fma_f32 v[122:123], v[122:123], v[134:135], v[98:99]
	v_pk_mul_f32 v[98:99], v[120:121], v[100:101] op_sel_hi:[0,1]
	v_pk_fma_f32 v[124:125], v[124:125], v[136:137], v[98:99]
	v_pk_mul_f32 v[98:99], v[48:49], v[10:11] op_sel_hi:[0,1]
	v_exp_f32_e32 v98, v98
	v_exp_f32_e32 v99, v99
	v_pk_mul_f32 v[100:101], v[48:49], v[12:13] op_sel_hi:[0,1]
	v_exp_f32_e32 v100, v100
	v_exp_f32_e32 v101, v101
	v_pk_mul_f32 v[102:103], v[120:121], v[102:103] op_sel_hi:[0,1]
	v_pk_fma_f32 v[128:129], v[128:129], v[98:99], v[102:103]
	v_pk_mul_f32 v[98:99], v[120:121], v[104:105] op_sel_hi:[0,1]
	v_pk_fma_f32 v[126:127], v[126:127], v[100:101], v[98:99]
	v_pk_mul_f32 v[98:99], v[48:49], v[6:7] op_sel_hi:[0,1]
	v_exp_f32_e32 v98, v98
	v_exp_f32_e32 v99, v99
	v_pk_mul_f32 v[100:101], v[48:49], v[8:9] op_sel_hi:[0,1]
	v_exp_f32_e32 v100, v100
	v_exp_f32_e32 v101, v101
	v_pk_mul_f32 v[102:103], v[120:121], v[108:109] op_sel_hi:[0,1]
	v_pk_fma_f32 v[130:131], v[130:131], v[98:99], v[102:103]
	v_pk_mul_f32 v[98:99], v[120:121], v[110:111] op_sel_hi:[0,1]
	v_pk_fma_f32 v[132:133], v[132:133], v[100:101], v[98:99]
	v_pk_mul_f32 v[98:99], v[48:49], v[2:3] op_sel_hi:[0,1]
	v_exp_f32_e32 v98, v98
	v_exp_f32_e32 v99, v99
	v_pk_mul_f32 v[100:101], v[48:49], v[4:5] op_sel_hi:[0,1]
	v_exp_f32_e32 v100, v100
	v_exp_f32_e32 v101, v101
	v_pk_mul_f32 v[102:103], v[120:121], v[112:113] op_sel_hi:[0,1]
	v_pk_fma_f32 v[116:117], v[116:117], v[98:99], v[102:103]
	v_pk_mul_f32 v[98:99], v[120:121], v[114:115] op_sel_hi:[0,1]
	v_pk_fma_f32 v[118:119], v[118:119], v[100:101], v[98:99]
	s_nop 0
	s_waitcnt lgkmcnt(0)
	s_nop 0
	ds_read_b128 v[98:101], v160 offset:44560
	ds_read_b128 v[102:105], v160 offset:44576
	ds_read_b128 v[108:111], v160 offset:44592
	ds_read_b128 v[112:115], v160 offset:44608
	v_pk_mul_f32 v[134:135], v[50:51], v[14:15] op_sel_hi:[0,1]
	v_exp_f32_e32 v134, v134
	v_exp_f32_e32 v135, v135
	v_pk_mul_f32 v[136:137], v[50:51], v[16:17] op_sel_hi:[0,1]
	v_exp_f32_e32 v136, v136
	v_exp_f32_e32 v137, v137
	v_mul_f32_e32 v120, v50, v75
	v_pk_mul_f32 v[82:83], v[120:121], v[82:83] op_sel_hi:[0,1]
	v_pk_fma_f32 v[122:123], v[122:123], v[134:135], v[82:83]
	v_pk_mul_f32 v[82:83], v[120:121], v[84:85] op_sel_hi:[0,1]
	v_pk_fma_f32 v[124:125], v[124:125], v[136:137], v[82:83]
	v_pk_mul_f32 v[82:83], v[50:51], v[10:11] op_sel_hi:[0,1]
	v_exp_f32_e32 v82, v82
	v_exp_f32_e32 v83, v83
	v_pk_mul_f32 v[84:85], v[50:51], v[12:13] op_sel_hi:[0,1]
	v_exp_f32_e32 v84, v84
	v_exp_f32_e32 v85, v85
	v_pk_mul_f32 v[86:87], v[120:121], v[86:87] op_sel_hi:[0,1]
	v_pk_fma_f32 v[128:129], v[128:129], v[82:83], v[86:87]
	v_pk_mul_f32 v[82:83], v[120:121], v[88:89] op_sel_hi:[0,1]
	v_pk_fma_f32 v[126:127], v[126:127], v[84:85], v[82:83]
	v_pk_mul_f32 v[82:83], v[50:51], v[6:7] op_sel_hi:[0,1]
	v_exp_f32_e32 v82, v82
	v_exp_f32_e32 v83, v83
	v_pk_mul_f32 v[84:85], v[50:51], v[8:9] op_sel_hi:[0,1]
	v_exp_f32_e32 v84, v84
	v_exp_f32_e32 v85, v85
	v_pk_mul_f32 v[86:87], v[120:121], v[90:91] op_sel_hi:[0,1]
	v_pk_fma_f32 v[130:131], v[130:131], v[82:83], v[86:87]
	v_pk_mul_f32 v[82:83], v[120:121], v[92:93] op_sel_hi:[0,1]
	v_pk_fma_f32 v[132:133], v[132:133], v[84:85], v[82:83]
	v_pk_mul_f32 v[82:83], v[50:51], v[2:3] op_sel_hi:[0,1]
	v_exp_f32_e32 v82, v82
	v_exp_f32_e32 v83, v83
	v_pk_mul_f32 v[84:85], v[50:51], v[4:5] op_sel_hi:[0,1]
	v_exp_f32_e32 v84, v84
	v_exp_f32_e32 v85, v85
	v_pk_mul_f32 v[86:87], v[120:121], v[94:95] op_sel_hi:[0,1]
	v_pk_fma_f32 v[116:117], v[116:117], v[82:83], v[86:87]
	v_pk_mul_f32 v[82:83], v[120:121], v[96:97] op_sel_hi:[0,1]
	v_pk_fma_f32 v[118:119], v[118:119], v[84:85], v[82:83]
	s_nop 0
	s_waitcnt lgkmcnt(0)
	s_nop 0
	ds_read_b128 v[82:85], v160 offset:44768
	ds_read_b128 v[86:89], v160 offset:44784
	ds_read_b128 v[90:93], v160 offset:44800
	ds_read_b128 v[94:97], v160 offset:44816
	v_pk_mul_f32 v[134:135], v[52:53], v[14:15] op_sel_hi:[0,1]
	v_exp_f32_e32 v134, v134
	v_exp_f32_e32 v135, v135
	v_pk_mul_f32 v[136:137], v[52:53], v[16:17] op_sel_hi:[0,1]
	v_exp_f32_e32 v136, v136
	v_exp_f32_e32 v137, v137
	v_mul_f32_e32 v120, v52, v73
	v_pk_mul_f32 v[98:99], v[120:121], v[98:99] op_sel_hi:[0,1]
	v_pk_fma_f32 v[122:123], v[122:123], v[134:135], v[98:99]
	v_pk_mul_f32 v[98:99], v[120:121], v[100:101] op_sel_hi:[0,1]
	v_pk_fma_f32 v[124:125], v[124:125], v[136:137], v[98:99]
	v_pk_mul_f32 v[98:99], v[52:53], v[10:11] op_sel_hi:[0,1]
	v_exp_f32_e32 v98, v98
	v_exp_f32_e32 v99, v99
	v_pk_mul_f32 v[100:101], v[52:53], v[12:13] op_sel_hi:[0,1]
	v_exp_f32_e32 v100, v100
	v_exp_f32_e32 v101, v101
	v_pk_mul_f32 v[102:103], v[120:121], v[102:103] op_sel_hi:[0,1]
	v_pk_fma_f32 v[128:129], v[128:129], v[98:99], v[102:103]
	v_pk_mul_f32 v[98:99], v[120:121], v[104:105] op_sel_hi:[0,1]
	v_pk_fma_f32 v[126:127], v[126:127], v[100:101], v[98:99]
	v_pk_mul_f32 v[98:99], v[52:53], v[6:7] op_sel_hi:[0,1]
	v_exp_f32_e32 v98, v98
	v_exp_f32_e32 v99, v99
	v_pk_mul_f32 v[100:101], v[52:53], v[8:9] op_sel_hi:[0,1]
	v_exp_f32_e32 v100, v100
	v_exp_f32_e32 v101, v101
	v_pk_mul_f32 v[102:103], v[120:121], v[108:109] op_sel_hi:[0,1]
	v_pk_fma_f32 v[130:131], v[130:131], v[98:99], v[102:103]
	v_pk_mul_f32 v[98:99], v[120:121], v[110:111] op_sel_hi:[0,1]
	v_pk_fma_f32 v[132:133], v[132:133], v[100:101], v[98:99]
	v_pk_mul_f32 v[98:99], v[52:53], v[2:3] op_sel_hi:[0,1]
	v_exp_f32_e32 v98, v98
	v_exp_f32_e32 v99, v99
	v_pk_mul_f32 v[100:101], v[52:53], v[4:5] op_sel_hi:[0,1]
	v_exp_f32_e32 v100, v100
	v_exp_f32_e32 v101, v101
	v_pk_mul_f32 v[102:103], v[120:121], v[112:113] op_sel_hi:[0,1]
	v_pk_fma_f32 v[116:117], v[116:117], v[98:99], v[102:103]
	v_pk_mul_f32 v[98:99], v[120:121], v[114:115] op_sel_hi:[0,1]
	v_pk_fma_f32 v[118:119], v[118:119], v[100:101], v[98:99]
	s_nop 0
	s_waitcnt lgkmcnt(0)
	s_nop 0
	ds_read_b128 v[98:101], v160 offset:44976
	ds_read_b128 v[102:105], v160 offset:44992
	ds_read_b128 v[108:111], v160 offset:45008
	ds_read_b128 v[112:115], v160 offset:45024
	v_pk_mul_f32 v[134:135], v[54:55], v[14:15] op_sel_hi:[0,1]
	v_exp_f32_e32 v134, v134
	v_exp_f32_e32 v135, v135
	v_pk_mul_f32 v[136:137], v[54:55], v[16:17] op_sel_hi:[0,1]
	v_exp_f32_e32 v136, v136
	v_exp_f32_e32 v137, v137
	v_mul_f32_e32 v120, v54, v71
	v_pk_mul_f32 v[82:83], v[120:121], v[82:83] op_sel_hi:[0,1]
	v_pk_fma_f32 v[122:123], v[122:123], v[134:135], v[82:83]
	v_pk_mul_f32 v[82:83], v[120:121], v[84:85] op_sel_hi:[0,1]
	v_pk_fma_f32 v[124:125], v[124:125], v[136:137], v[82:83]
	v_pk_mul_f32 v[82:83], v[54:55], v[10:11] op_sel_hi:[0,1]
	v_exp_f32_e32 v82, v82
	v_exp_f32_e32 v83, v83
	v_pk_mul_f32 v[84:85], v[54:55], v[12:13] op_sel_hi:[0,1]
	v_exp_f32_e32 v84, v84
	v_exp_f32_e32 v85, v85
	v_pk_mul_f32 v[86:87], v[120:121], v[86:87] op_sel_hi:[0,1]
	v_pk_fma_f32 v[128:129], v[128:129], v[82:83], v[86:87]
	v_pk_mul_f32 v[82:83], v[120:121], v[88:89] op_sel_hi:[0,1]
	v_pk_fma_f32 v[126:127], v[126:127], v[84:85], v[82:83]
	v_pk_mul_f32 v[82:83], v[54:55], v[6:7] op_sel_hi:[0,1]
	v_exp_f32_e32 v82, v82
	v_exp_f32_e32 v83, v83
	v_pk_mul_f32 v[84:85], v[54:55], v[8:9] op_sel_hi:[0,1]
	v_exp_f32_e32 v84, v84
	v_exp_f32_e32 v85, v85
	v_pk_mul_f32 v[86:87], v[120:121], v[90:91] op_sel_hi:[0,1]
	v_pk_fma_f32 v[130:131], v[130:131], v[82:83], v[86:87]
	v_pk_mul_f32 v[82:83], v[120:121], v[92:93] op_sel_hi:[0,1]
	v_pk_fma_f32 v[132:133], v[132:133], v[84:85], v[82:83]
	v_pk_mul_f32 v[82:83], v[54:55], v[2:3] op_sel_hi:[0,1]
	v_exp_f32_e32 v82, v82
	v_exp_f32_e32 v83, v83
	v_pk_mul_f32 v[84:85], v[54:55], v[4:5] op_sel_hi:[0,1]
	v_exp_f32_e32 v84, v84
	v_exp_f32_e32 v85, v85
	v_pk_mul_f32 v[86:87], v[120:121], v[94:95] op_sel_hi:[0,1]
	v_pk_fma_f32 v[116:117], v[116:117], v[82:83], v[86:87]
	v_pk_mul_f32 v[82:83], v[120:121], v[96:97] op_sel_hi:[0,1]
	v_pk_fma_f32 v[118:119], v[118:119], v[84:85], v[82:83]
	s_nop 0
	s_waitcnt lgkmcnt(0)
	s_nop 0
	ds_read_b128 v[82:85], v160 offset:45184
	ds_read_b128 v[86:89], v160 offset:45200
	ds_read_b128 v[90:93], v160 offset:45216
	ds_read_b128 v[94:97], v160 offset:45232
	v_pk_mul_f32 v[134:135], v[56:57], v[14:15] op_sel_hi:[0,1]
	v_exp_f32_e32 v134, v134
	v_exp_f32_e32 v135, v135
	v_pk_mul_f32 v[136:137], v[56:57], v[16:17] op_sel_hi:[0,1]
	v_exp_f32_e32 v136, v136
	v_exp_f32_e32 v137, v137
	v_mul_f32_e32 v120, v56, v69
	v_pk_mul_f32 v[98:99], v[120:121], v[98:99] op_sel_hi:[0,1]
	v_pk_fma_f32 v[122:123], v[122:123], v[134:135], v[98:99]
	v_pk_mul_f32 v[98:99], v[120:121], v[100:101] op_sel_hi:[0,1]
	v_pk_fma_f32 v[124:125], v[124:125], v[136:137], v[98:99]
	v_pk_mul_f32 v[98:99], v[56:57], v[10:11] op_sel_hi:[0,1]
	v_exp_f32_e32 v98, v98
	v_exp_f32_e32 v99, v99
	v_pk_mul_f32 v[100:101], v[56:57], v[12:13] op_sel_hi:[0,1]
	v_exp_f32_e32 v100, v100
	v_exp_f32_e32 v101, v101
	v_pk_mul_f32 v[102:103], v[120:121], v[102:103] op_sel_hi:[0,1]
	v_pk_fma_f32 v[128:129], v[128:129], v[98:99], v[102:103]
	v_pk_mul_f32 v[98:99], v[120:121], v[104:105] op_sel_hi:[0,1]
	v_pk_fma_f32 v[126:127], v[126:127], v[100:101], v[98:99]
	v_pk_mul_f32 v[98:99], v[56:57], v[6:7] op_sel_hi:[0,1]
	v_exp_f32_e32 v98, v98
	v_exp_f32_e32 v99, v99
	v_pk_mul_f32 v[100:101], v[56:57], v[8:9] op_sel_hi:[0,1]
	v_exp_f32_e32 v100, v100
	v_exp_f32_e32 v101, v101
	v_pk_mul_f32 v[102:103], v[120:121], v[108:109] op_sel_hi:[0,1]
	v_pk_fma_f32 v[130:131], v[130:131], v[98:99], v[102:103]
	v_pk_mul_f32 v[98:99], v[120:121], v[110:111] op_sel_hi:[0,1]
	v_pk_fma_f32 v[132:133], v[132:133], v[100:101], v[98:99]
	v_pk_mul_f32 v[98:99], v[56:57], v[2:3] op_sel_hi:[0,1]
	v_exp_f32_e32 v98, v98
	v_exp_f32_e32 v99, v99
	v_pk_mul_f32 v[100:101], v[56:57], v[4:5] op_sel_hi:[0,1]
	v_exp_f32_e32 v100, v100
	v_exp_f32_e32 v101, v101
	v_pk_mul_f32 v[102:103], v[120:121], v[112:113] op_sel_hi:[0,1]
	v_pk_fma_f32 v[116:117], v[116:117], v[98:99], v[102:103]
	v_pk_mul_f32 v[98:99], v[120:121], v[114:115] op_sel_hi:[0,1]
	v_pk_fma_f32 v[118:119], v[118:119], v[100:101], v[98:99]
	s_nop 0
	s_waitcnt lgkmcnt(0)
	s_nop 0
	ds_read_b128 v[98:101], v160 offset:45392
	ds_read_b128 v[102:105], v160 offset:45408
	ds_read_b128 v[108:111], v160 offset:45424
	ds_read_b128 v[112:115], v160 offset:45440
	v_pk_mul_f32 v[134:135], v[58:59], v[14:15] op_sel_hi:[0,1]
	v_exp_f32_e32 v134, v134
	v_exp_f32_e32 v135, v135
	v_pk_mul_f32 v[136:137], v[58:59], v[16:17] op_sel_hi:[0,1]
	v_exp_f32_e32 v136, v136
	v_exp_f32_e32 v137, v137
	v_mul_f32_e32 v120, v58, v67
	v_pk_mul_f32 v[82:83], v[120:121], v[82:83] op_sel_hi:[0,1]
	v_pk_fma_f32 v[122:123], v[122:123], v[134:135], v[82:83]
	v_pk_mul_f32 v[82:83], v[120:121], v[84:85] op_sel_hi:[0,1]
	v_pk_fma_f32 v[124:125], v[124:125], v[136:137], v[82:83]
	v_pk_mul_f32 v[82:83], v[58:59], v[10:11] op_sel_hi:[0,1]
	v_exp_f32_e32 v82, v82
	v_exp_f32_e32 v83, v83
	v_pk_mul_f32 v[84:85], v[58:59], v[12:13] op_sel_hi:[0,1]
	v_exp_f32_e32 v84, v84
	v_exp_f32_e32 v85, v85
	v_pk_mul_f32 v[86:87], v[120:121], v[86:87] op_sel_hi:[0,1]
	v_pk_fma_f32 v[128:129], v[128:129], v[82:83], v[86:87]
	v_pk_mul_f32 v[82:83], v[120:121], v[88:89] op_sel_hi:[0,1]
	v_pk_fma_f32 v[126:127], v[126:127], v[84:85], v[82:83]
	v_pk_mul_f32 v[82:83], v[58:59], v[6:7] op_sel_hi:[0,1]
	v_exp_f32_e32 v82, v82
	v_exp_f32_e32 v83, v83
	v_pk_mul_f32 v[84:85], v[58:59], v[8:9] op_sel_hi:[0,1]
	v_exp_f32_e32 v84, v84
	v_exp_f32_e32 v85, v85
	v_pk_mul_f32 v[86:87], v[120:121], v[90:91] op_sel_hi:[0,1]
	v_pk_fma_f32 v[130:131], v[130:131], v[82:83], v[86:87]
	v_pk_mul_f32 v[82:83], v[120:121], v[92:93] op_sel_hi:[0,1]
	v_pk_fma_f32 v[132:133], v[132:133], v[84:85], v[82:83]
	v_pk_mul_f32 v[82:83], v[58:59], v[2:3] op_sel_hi:[0,1]
	v_exp_f32_e32 v82, v82
	v_exp_f32_e32 v83, v83
	v_pk_mul_f32 v[84:85], v[58:59], v[4:5] op_sel_hi:[0,1]
	v_exp_f32_e32 v84, v84
	v_exp_f32_e32 v85, v85
	v_pk_mul_f32 v[86:87], v[120:121], v[94:95] op_sel_hi:[0,1]
	v_pk_fma_f32 v[116:117], v[116:117], v[82:83], v[86:87]
	v_pk_mul_f32 v[82:83], v[120:121], v[96:97] op_sel_hi:[0,1]
	v_pk_fma_f32 v[118:119], v[118:119], v[84:85], v[82:83]
	s_nop 0
	s_waitcnt lgkmcnt(0)
	s_nop 0
	ds_read_b128 v[82:85], v160 offset:45600
	ds_read_b128 v[86:89], v160 offset:45616
	ds_read_b128 v[90:93], v160 offset:45632
	ds_read_b128 v[94:97], v160 offset:45648
	v_pk_mul_f32 v[134:135], v[60:61], v[14:15] op_sel_hi:[0,1]
	v_exp_f32_e32 v134, v134
	v_exp_f32_e32 v135, v135
	v_pk_mul_f32 v[136:137], v[60:61], v[16:17] op_sel_hi:[0,1]
	v_exp_f32_e32 v136, v136
	v_exp_f32_e32 v137, v137
	v_mul_f32_e32 v120, v60, v65
	v_pk_mul_f32 v[98:99], v[120:121], v[98:99] op_sel_hi:[0,1]
	v_pk_fma_f32 v[122:123], v[122:123], v[134:135], v[98:99]
	v_pk_mul_f32 v[98:99], v[120:121], v[100:101] op_sel_hi:[0,1]
	v_pk_fma_f32 v[124:125], v[124:125], v[136:137], v[98:99]
	v_pk_mul_f32 v[98:99], v[60:61], v[10:11] op_sel_hi:[0,1]
	v_exp_f32_e32 v98, v98
	v_exp_f32_e32 v99, v99
	v_pk_mul_f32 v[100:101], v[60:61], v[12:13] op_sel_hi:[0,1]
	v_exp_f32_e32 v100, v100
	v_exp_f32_e32 v101, v101
	v_pk_mul_f32 v[102:103], v[120:121], v[102:103] op_sel_hi:[0,1]
	v_pk_fma_f32 v[128:129], v[128:129], v[98:99], v[102:103]
	v_pk_mul_f32 v[98:99], v[120:121], v[104:105] op_sel_hi:[0,1]
	v_pk_fma_f32 v[126:127], v[126:127], v[100:101], v[98:99]
	v_pk_mul_f32 v[98:99], v[60:61], v[6:7] op_sel_hi:[0,1]
	v_exp_f32_e32 v98, v98
	v_exp_f32_e32 v99, v99
	v_pk_mul_f32 v[100:101], v[60:61], v[8:9] op_sel_hi:[0,1]
	v_exp_f32_e32 v100, v100
	v_exp_f32_e32 v101, v101
	v_pk_mul_f32 v[102:103], v[120:121], v[108:109] op_sel_hi:[0,1]
	v_pk_fma_f32 v[130:131], v[130:131], v[98:99], v[102:103]
	v_pk_mul_f32 v[98:99], v[120:121], v[110:111] op_sel_hi:[0,1]
	v_pk_fma_f32 v[132:133], v[132:133], v[100:101], v[98:99]
	v_pk_mul_f32 v[98:99], v[60:61], v[2:3] op_sel_hi:[0,1]
	v_exp_f32_e32 v98, v98
	v_exp_f32_e32 v99, v99
	v_pk_mul_f32 v[100:101], v[60:61], v[4:5] op_sel_hi:[0,1]
	v_exp_f32_e32 v100, v100
	v_exp_f32_e32 v101, v101
	v_pk_mul_f32 v[102:103], v[120:121], v[112:113] op_sel_hi:[0,1]
	v_pk_fma_f32 v[116:117], v[116:117], v[98:99], v[102:103]
	v_pk_mul_f32 v[98:99], v[120:121], v[114:115] op_sel_hi:[0,1]
	v_pk_fma_f32 v[118:119], v[118:119], v[100:101], v[98:99]
	s_nop 0
	s_waitcnt lgkmcnt(0)
	s_nop 0
	ds_read_b128 v[98:101], v160 offset:45808
	ds_read_b128 v[102:105], v160 offset:45824
	ds_read_b128 v[108:111], v160 offset:45840
	ds_read_b128 v[112:115], v160 offset:45856
	v_pk_mul_f32 v[134:135], v[62:63], v[14:15] op_sel_hi:[0,1]
	v_exp_f32_e32 v134, v134
	v_exp_f32_e32 v135, v135
	v_pk_mul_f32 v[136:137], v[62:63], v[16:17] op_sel_hi:[0,1]
	v_exp_f32_e32 v136, v136
	v_exp_f32_e32 v137, v137
	v_mul_f32_e32 v120, v62, v63
	v_pk_mul_f32 v[82:83], v[120:121], v[82:83] op_sel_hi:[0,1]
	v_pk_fma_f32 v[122:123], v[122:123], v[134:135], v[82:83]
	v_pk_mul_f32 v[82:83], v[120:121], v[84:85] op_sel_hi:[0,1]
	v_pk_fma_f32 v[124:125], v[124:125], v[136:137], v[82:83]
	v_pk_mul_f32 v[82:83], v[62:63], v[10:11] op_sel_hi:[0,1]
	v_exp_f32_e32 v82, v82
	v_exp_f32_e32 v83, v83
	v_pk_mul_f32 v[84:85], v[62:63], v[12:13] op_sel_hi:[0,1]
	v_exp_f32_e32 v84, v84
	v_exp_f32_e32 v85, v85
	v_pk_mul_f32 v[86:87], v[120:121], v[86:87] op_sel_hi:[0,1]
	v_pk_fma_f32 v[128:129], v[128:129], v[82:83], v[86:87]
	v_pk_mul_f32 v[82:83], v[120:121], v[88:89] op_sel_hi:[0,1]
	v_pk_fma_f32 v[126:127], v[126:127], v[84:85], v[82:83]
	v_pk_mul_f32 v[82:83], v[62:63], v[6:7] op_sel_hi:[0,1]
	v_exp_f32_e32 v82, v82
	v_exp_f32_e32 v83, v83
	v_pk_mul_f32 v[84:85], v[62:63], v[8:9] op_sel_hi:[0,1]
	v_exp_f32_e32 v84, v84
	v_exp_f32_e32 v85, v85
	v_pk_mul_f32 v[86:87], v[120:121], v[90:91] op_sel_hi:[0,1]
	v_pk_fma_f32 v[130:131], v[130:131], v[82:83], v[86:87]
	v_pk_mul_f32 v[82:83], v[120:121], v[92:93] op_sel_hi:[0,1]
	v_pk_fma_f32 v[132:133], v[132:133], v[84:85], v[82:83]
	v_pk_mul_f32 v[82:83], v[62:63], v[2:3] op_sel_hi:[0,1]
	v_exp_f32_e32 v82, v82
	v_exp_f32_e32 v83, v83
	v_pk_mul_f32 v[84:85], v[62:63], v[4:5] op_sel_hi:[0,1]
	v_exp_f32_e32 v84, v84
	v_exp_f32_e32 v85, v85
	v_pk_mul_f32 v[86:87], v[120:121], v[94:95] op_sel_hi:[0,1]
	v_pk_fma_f32 v[116:117], v[116:117], v[82:83], v[86:87]
	v_pk_mul_f32 v[82:83], v[120:121], v[96:97] op_sel_hi:[0,1]
	v_pk_fma_f32 v[118:119], v[118:119], v[84:85], v[82:83]
	s_nop 0
	s_waitcnt lgkmcnt(0)
	s_nop 0
	ds_read_b128 v[82:85], v160 offset:46016
	ds_read_b128 v[86:89], v160 offset:46032
	ds_read_b128 v[90:93], v160 offset:46048
	ds_read_b128 v[94:97], v160 offset:46064
	v_pk_mul_f32 v[134:135], v[64:65], v[14:15] op_sel_hi:[0,1]
	v_exp_f32_e32 v134, v134
	v_exp_f32_e32 v135, v135
	v_pk_mul_f32 v[136:137], v[64:65], v[16:17] op_sel_hi:[0,1]
	v_exp_f32_e32 v136, v136
	v_exp_f32_e32 v137, v137
	v_mul_f32_e32 v120, v64, v61
	v_pk_mul_f32 v[98:99], v[120:121], v[98:99] op_sel_hi:[0,1]
	v_pk_fma_f32 v[122:123], v[122:123], v[134:135], v[98:99]
	v_pk_mul_f32 v[98:99], v[120:121], v[100:101] op_sel_hi:[0,1]
	v_pk_fma_f32 v[124:125], v[124:125], v[136:137], v[98:99]
	v_pk_mul_f32 v[98:99], v[64:65], v[10:11] op_sel_hi:[0,1]
	v_exp_f32_e32 v98, v98
	v_exp_f32_e32 v99, v99
	v_pk_mul_f32 v[100:101], v[64:65], v[12:13] op_sel_hi:[0,1]
	v_exp_f32_e32 v100, v100
	v_exp_f32_e32 v101, v101
	v_pk_mul_f32 v[102:103], v[120:121], v[102:103] op_sel_hi:[0,1]
	v_pk_fma_f32 v[128:129], v[128:129], v[98:99], v[102:103]
	v_pk_mul_f32 v[98:99], v[120:121], v[104:105] op_sel_hi:[0,1]
	v_pk_fma_f32 v[126:127], v[126:127], v[100:101], v[98:99]
	v_pk_mul_f32 v[98:99], v[64:65], v[6:7] op_sel_hi:[0,1]
	v_exp_f32_e32 v98, v98
	v_exp_f32_e32 v99, v99
	v_pk_mul_f32 v[100:101], v[64:65], v[8:9] op_sel_hi:[0,1]
	v_exp_f32_e32 v100, v100
	v_exp_f32_e32 v101, v101
	v_pk_mul_f32 v[102:103], v[120:121], v[108:109] op_sel_hi:[0,1]
	v_pk_fma_f32 v[130:131], v[130:131], v[98:99], v[102:103]
	v_pk_mul_f32 v[98:99], v[120:121], v[110:111] op_sel_hi:[0,1]
	v_pk_fma_f32 v[132:133], v[132:133], v[100:101], v[98:99]
	v_pk_mul_f32 v[98:99], v[64:65], v[2:3] op_sel_hi:[0,1]
	v_exp_f32_e32 v98, v98
	v_exp_f32_e32 v99, v99
	v_pk_mul_f32 v[100:101], v[64:65], v[4:5] op_sel_hi:[0,1]
	v_exp_f32_e32 v100, v100
	v_exp_f32_e32 v101, v101
	v_pk_mul_f32 v[102:103], v[120:121], v[112:113] op_sel_hi:[0,1]
	v_pk_fma_f32 v[116:117], v[116:117], v[98:99], v[102:103]
	v_pk_mul_f32 v[98:99], v[120:121], v[114:115] op_sel_hi:[0,1]
	v_pk_fma_f32 v[118:119], v[118:119], v[100:101], v[98:99]
	s_nop 0
	s_waitcnt lgkmcnt(0)
	s_nop 0
	ds_read_b128 v[98:101], v160 offset:46224
	ds_read_b128 v[102:105], v160 offset:46240
	ds_read_b128 v[108:111], v160 offset:46256
	ds_read_b128 v[112:115], v160 offset:46272
	v_pk_mul_f32 v[134:135], v[66:67], v[14:15] op_sel_hi:[0,1]
	v_exp_f32_e32 v134, v134
	v_exp_f32_e32 v135, v135
	v_pk_mul_f32 v[136:137], v[66:67], v[16:17] op_sel_hi:[0,1]
	v_exp_f32_e32 v136, v136
	v_exp_f32_e32 v137, v137
	v_mul_f32_e32 v120, v66, v59
	v_pk_mul_f32 v[82:83], v[120:121], v[82:83] op_sel_hi:[0,1]
	v_pk_fma_f32 v[122:123], v[122:123], v[134:135], v[82:83]
	v_pk_mul_f32 v[82:83], v[120:121], v[84:85] op_sel_hi:[0,1]
	v_pk_fma_f32 v[124:125], v[124:125], v[136:137], v[82:83]
	v_pk_mul_f32 v[82:83], v[66:67], v[10:11] op_sel_hi:[0,1]
	v_exp_f32_e32 v82, v82
	v_exp_f32_e32 v83, v83
	v_pk_mul_f32 v[84:85], v[66:67], v[12:13] op_sel_hi:[0,1]
	v_exp_f32_e32 v84, v84
	v_exp_f32_e32 v85, v85
	v_pk_mul_f32 v[86:87], v[120:121], v[86:87] op_sel_hi:[0,1]
	v_pk_fma_f32 v[128:129], v[128:129], v[82:83], v[86:87]
	v_pk_mul_f32 v[82:83], v[120:121], v[88:89] op_sel_hi:[0,1]
	v_pk_fma_f32 v[126:127], v[126:127], v[84:85], v[82:83]
	v_pk_mul_f32 v[82:83], v[66:67], v[6:7] op_sel_hi:[0,1]
	v_exp_f32_e32 v82, v82
	v_exp_f32_e32 v83, v83
	v_pk_mul_f32 v[84:85], v[66:67], v[8:9] op_sel_hi:[0,1]
	v_exp_f32_e32 v84, v84
	v_exp_f32_e32 v85, v85
	v_pk_mul_f32 v[86:87], v[120:121], v[90:91] op_sel_hi:[0,1]
	v_pk_fma_f32 v[130:131], v[130:131], v[82:83], v[86:87]
	v_pk_mul_f32 v[82:83], v[120:121], v[92:93] op_sel_hi:[0,1]
	v_pk_fma_f32 v[132:133], v[132:133], v[84:85], v[82:83]
	v_pk_mul_f32 v[82:83], v[66:67], v[2:3] op_sel_hi:[0,1]
	v_exp_f32_e32 v82, v82
	v_exp_f32_e32 v83, v83
	v_pk_mul_f32 v[84:85], v[66:67], v[4:5] op_sel_hi:[0,1]
	v_exp_f32_e32 v84, v84
	v_exp_f32_e32 v85, v85
	v_pk_mul_f32 v[86:87], v[120:121], v[94:95] op_sel_hi:[0,1]
	v_pk_fma_f32 v[116:117], v[116:117], v[82:83], v[86:87]
	v_pk_mul_f32 v[82:83], v[120:121], v[96:97] op_sel_hi:[0,1]
	v_pk_fma_f32 v[118:119], v[118:119], v[84:85], v[82:83]
	s_nop 0
	s_waitcnt lgkmcnt(0)
	s_nop 0
	ds_read_b128 v[82:85], v160 offset:46432
	ds_read_b128 v[86:89], v160 offset:46448
	ds_read_b128 v[90:93], v160 offset:46464
	ds_read_b128 v[94:97], v160 offset:46480
	v_pk_mul_f32 v[134:135], v[68:69], v[14:15] op_sel_hi:[0,1]
	v_exp_f32_e32 v134, v134
	v_exp_f32_e32 v135, v135
	v_pk_mul_f32 v[136:137], v[68:69], v[16:17] op_sel_hi:[0,1]
	v_exp_f32_e32 v136, v136
	v_exp_f32_e32 v137, v137
	v_mul_f32_e32 v120, v68, v57
	v_pk_mul_f32 v[98:99], v[120:121], v[98:99] op_sel_hi:[0,1]
	v_pk_fma_f32 v[122:123], v[122:123], v[134:135], v[98:99]
	v_pk_mul_f32 v[98:99], v[120:121], v[100:101] op_sel_hi:[0,1]
	v_pk_fma_f32 v[124:125], v[124:125], v[136:137], v[98:99]
	v_pk_mul_f32 v[98:99], v[68:69], v[10:11] op_sel_hi:[0,1]
	v_exp_f32_e32 v98, v98
	v_exp_f32_e32 v99, v99
	v_pk_mul_f32 v[100:101], v[68:69], v[12:13] op_sel_hi:[0,1]
	v_exp_f32_e32 v100, v100
	v_exp_f32_e32 v101, v101
	v_pk_mul_f32 v[102:103], v[120:121], v[102:103] op_sel_hi:[0,1]
	v_pk_fma_f32 v[128:129], v[128:129], v[98:99], v[102:103]
	v_pk_mul_f32 v[98:99], v[120:121], v[104:105] op_sel_hi:[0,1]
	v_pk_fma_f32 v[126:127], v[126:127], v[100:101], v[98:99]
	v_pk_mul_f32 v[98:99], v[68:69], v[6:7] op_sel_hi:[0,1]
	v_exp_f32_e32 v98, v98
	v_exp_f32_e32 v99, v99
	v_pk_mul_f32 v[100:101], v[68:69], v[8:9] op_sel_hi:[0,1]
	v_exp_f32_e32 v100, v100
	v_exp_f32_e32 v101, v101
	v_pk_mul_f32 v[102:103], v[120:121], v[108:109] op_sel_hi:[0,1]
	v_pk_fma_f32 v[130:131], v[130:131], v[98:99], v[102:103]
	v_pk_mul_f32 v[98:99], v[120:121], v[110:111] op_sel_hi:[0,1]
	v_pk_fma_f32 v[132:133], v[132:133], v[100:101], v[98:99]
	v_pk_mul_f32 v[98:99], v[68:69], v[2:3] op_sel_hi:[0,1]
	v_exp_f32_e32 v98, v98
	v_exp_f32_e32 v99, v99
	v_pk_mul_f32 v[100:101], v[68:69], v[4:5] op_sel_hi:[0,1]
	v_exp_f32_e32 v100, v100
	v_exp_f32_e32 v101, v101
	v_pk_mul_f32 v[102:103], v[120:121], v[112:113] op_sel_hi:[0,1]
	v_pk_fma_f32 v[116:117], v[116:117], v[98:99], v[102:103]
	v_pk_mul_f32 v[98:99], v[120:121], v[114:115] op_sel_hi:[0,1]
	v_pk_fma_f32 v[118:119], v[118:119], v[100:101], v[98:99]
	s_nop 0
	s_waitcnt lgkmcnt(0)
	s_nop 0
	ds_read_b128 v[98:101], v160 offset:46640
	ds_read_b128 v[102:105], v160 offset:46656
	ds_read_b128 v[108:111], v160 offset:46672
	ds_read_b128 v[112:115], v160 offset:46688
	v_pk_mul_f32 v[134:135], v[70:71], v[14:15] op_sel_hi:[0,1]
	v_exp_f32_e32 v134, v134
	v_exp_f32_e32 v135, v135
	v_pk_mul_f32 v[136:137], v[70:71], v[16:17] op_sel_hi:[0,1]
	v_exp_f32_e32 v136, v136
	v_exp_f32_e32 v137, v137
	v_mul_f32_e32 v120, v70, v55
	v_pk_mul_f32 v[82:83], v[120:121], v[82:83] op_sel_hi:[0,1]
	v_pk_fma_f32 v[122:123], v[122:123], v[134:135], v[82:83]
	v_pk_mul_f32 v[82:83], v[120:121], v[84:85] op_sel_hi:[0,1]
	v_pk_fma_f32 v[124:125], v[124:125], v[136:137], v[82:83]
	v_pk_mul_f32 v[82:83], v[70:71], v[10:11] op_sel_hi:[0,1]
	v_exp_f32_e32 v82, v82
	v_exp_f32_e32 v83, v83
	v_pk_mul_f32 v[84:85], v[70:71], v[12:13] op_sel_hi:[0,1]
	v_exp_f32_e32 v84, v84
	v_exp_f32_e32 v85, v85
	v_pk_mul_f32 v[86:87], v[120:121], v[86:87] op_sel_hi:[0,1]
	v_pk_fma_f32 v[128:129], v[128:129], v[82:83], v[86:87]
	v_pk_mul_f32 v[82:83], v[120:121], v[88:89] op_sel_hi:[0,1]
	v_pk_fma_f32 v[126:127], v[126:127], v[84:85], v[82:83]
	v_pk_mul_f32 v[82:83], v[70:71], v[6:7] op_sel_hi:[0,1]
	v_exp_f32_e32 v82, v82
	v_exp_f32_e32 v83, v83
	v_pk_mul_f32 v[84:85], v[70:71], v[8:9] op_sel_hi:[0,1]
	v_exp_f32_e32 v84, v84
	v_exp_f32_e32 v85, v85
	v_pk_mul_f32 v[86:87], v[120:121], v[90:91] op_sel_hi:[0,1]
	v_pk_fma_f32 v[130:131], v[130:131], v[82:83], v[86:87]
	v_pk_mul_f32 v[82:83], v[120:121], v[92:93] op_sel_hi:[0,1]
	v_pk_fma_f32 v[132:133], v[132:133], v[84:85], v[82:83]
	v_pk_mul_f32 v[82:83], v[70:71], v[2:3] op_sel_hi:[0,1]
	v_exp_f32_e32 v82, v82
	v_exp_f32_e32 v83, v83
	v_pk_mul_f32 v[84:85], v[70:71], v[4:5] op_sel_hi:[0,1]
	v_exp_f32_e32 v84, v84
	v_exp_f32_e32 v85, v85
	v_pk_mul_f32 v[86:87], v[120:121], v[94:95] op_sel_hi:[0,1]
	v_pk_fma_f32 v[116:117], v[116:117], v[82:83], v[86:87]
	v_pk_mul_f32 v[82:83], v[120:121], v[96:97] op_sel_hi:[0,1]
	v_pk_fma_f32 v[118:119], v[118:119], v[84:85], v[82:83]
	s_nop 0
	s_waitcnt lgkmcnt(0)
	s_nop 0
	ds_read_b128 v[82:85], v160 offset:46848
	ds_read_b128 v[86:89], v160 offset:46864
	ds_read_b128 v[90:93], v160 offset:46880
	ds_read_b128 v[94:97], v160 offset:46896
	v_pk_mul_f32 v[134:135], v[72:73], v[14:15] op_sel_hi:[0,1]
	v_exp_f32_e32 v134, v134
	v_exp_f32_e32 v135, v135
	v_pk_mul_f32 v[136:137], v[72:73], v[16:17] op_sel_hi:[0,1]
	v_exp_f32_e32 v136, v136
	v_exp_f32_e32 v137, v137
	v_mul_f32_e32 v120, v72, v53
	v_pk_mul_f32 v[98:99], v[120:121], v[98:99] op_sel_hi:[0,1]
	v_pk_fma_f32 v[122:123], v[122:123], v[134:135], v[98:99]
	v_pk_mul_f32 v[98:99], v[120:121], v[100:101] op_sel_hi:[0,1]
	v_pk_fma_f32 v[124:125], v[124:125], v[136:137], v[98:99]
	v_pk_mul_f32 v[98:99], v[72:73], v[10:11] op_sel_hi:[0,1]
	v_exp_f32_e32 v98, v98
	v_exp_f32_e32 v99, v99
	v_pk_mul_f32 v[100:101], v[72:73], v[12:13] op_sel_hi:[0,1]
	v_exp_f32_e32 v100, v100
	v_exp_f32_e32 v101, v101
	v_pk_mul_f32 v[102:103], v[120:121], v[102:103] op_sel_hi:[0,1]
	v_pk_fma_f32 v[128:129], v[128:129], v[98:99], v[102:103]
	v_pk_mul_f32 v[98:99], v[120:121], v[104:105] op_sel_hi:[0,1]
	v_pk_fma_f32 v[126:127], v[126:127], v[100:101], v[98:99]
	v_pk_mul_f32 v[98:99], v[72:73], v[6:7] op_sel_hi:[0,1]
	v_exp_f32_e32 v98, v98
	v_exp_f32_e32 v99, v99
	v_pk_mul_f32 v[100:101], v[72:73], v[8:9] op_sel_hi:[0,1]
	v_exp_f32_e32 v100, v100
	v_exp_f32_e32 v101, v101
	v_pk_mul_f32 v[102:103], v[120:121], v[108:109] op_sel_hi:[0,1]
	v_pk_fma_f32 v[130:131], v[130:131], v[98:99], v[102:103]
	v_pk_mul_f32 v[98:99], v[120:121], v[110:111] op_sel_hi:[0,1]
	v_pk_fma_f32 v[132:133], v[132:133], v[100:101], v[98:99]
	v_pk_mul_f32 v[98:99], v[72:73], v[2:3] op_sel_hi:[0,1]
	v_exp_f32_e32 v98, v98
	v_exp_f32_e32 v99, v99
	v_pk_mul_f32 v[100:101], v[72:73], v[4:5] op_sel_hi:[0,1]
	v_exp_f32_e32 v100, v100
	v_exp_f32_e32 v101, v101
	v_pk_mul_f32 v[102:103], v[120:121], v[112:113] op_sel_hi:[0,1]
	v_pk_fma_f32 v[116:117], v[116:117], v[98:99], v[102:103]
	v_pk_mul_f32 v[98:99], v[120:121], v[114:115] op_sel_hi:[0,1]
	v_pk_fma_f32 v[118:119], v[118:119], v[100:101], v[98:99]
	s_nop 0
	s_waitcnt lgkmcnt(0)
	s_nop 0
	ds_read_b128 v[98:101], v160 offset:47056
	ds_read_b128 v[102:105], v160 offset:47072
	ds_read_b128 v[108:111], v160 offset:47088
	ds_read_b128 v[112:115], v160 offset:47104
	v_pk_mul_f32 v[134:135], v[74:75], v[14:15] op_sel_hi:[0,1]
	v_exp_f32_e32 v134, v134
	v_exp_f32_e32 v135, v135
	v_pk_mul_f32 v[136:137], v[74:75], v[16:17] op_sel_hi:[0,1]
	v_exp_f32_e32 v136, v136
	v_exp_f32_e32 v137, v137
	v_mul_f32_e32 v120, v74, v51
	v_pk_mul_f32 v[82:83], v[120:121], v[82:83] op_sel_hi:[0,1]
	v_pk_fma_f32 v[122:123], v[122:123], v[134:135], v[82:83]
	v_pk_mul_f32 v[82:83], v[120:121], v[84:85] op_sel_hi:[0,1]
	v_pk_fma_f32 v[124:125], v[124:125], v[136:137], v[82:83]
	v_pk_mul_f32 v[82:83], v[74:75], v[10:11] op_sel_hi:[0,1]
	v_exp_f32_e32 v82, v82
	v_exp_f32_e32 v83, v83
	v_pk_mul_f32 v[84:85], v[74:75], v[12:13] op_sel_hi:[0,1]
	v_exp_f32_e32 v84, v84
	v_exp_f32_e32 v85, v85
	v_pk_mul_f32 v[86:87], v[120:121], v[86:87] op_sel_hi:[0,1]
	v_pk_fma_f32 v[128:129], v[128:129], v[82:83], v[86:87]
	v_pk_mul_f32 v[82:83], v[120:121], v[88:89] op_sel_hi:[0,1]
	v_pk_fma_f32 v[126:127], v[126:127], v[84:85], v[82:83]
	v_pk_mul_f32 v[82:83], v[74:75], v[6:7] op_sel_hi:[0,1]
	v_exp_f32_e32 v82, v82
	v_exp_f32_e32 v83, v83
	v_pk_mul_f32 v[84:85], v[74:75], v[8:9] op_sel_hi:[0,1]
	v_exp_f32_e32 v84, v84
	v_exp_f32_e32 v85, v85
	v_pk_mul_f32 v[86:87], v[120:121], v[90:91] op_sel_hi:[0,1]
	v_pk_fma_f32 v[130:131], v[130:131], v[82:83], v[86:87]
	v_pk_mul_f32 v[82:83], v[120:121], v[92:93] op_sel_hi:[0,1]
	v_pk_fma_f32 v[132:133], v[132:133], v[84:85], v[82:83]
	v_pk_mul_f32 v[82:83], v[74:75], v[2:3] op_sel_hi:[0,1]
	v_exp_f32_e32 v82, v82
	v_exp_f32_e32 v83, v83
	v_pk_mul_f32 v[84:85], v[74:75], v[4:5] op_sel_hi:[0,1]
	v_exp_f32_e32 v84, v84
	v_exp_f32_e32 v85, v85
	v_pk_mul_f32 v[86:87], v[120:121], v[94:95] op_sel_hi:[0,1]
	v_pk_fma_f32 v[116:117], v[116:117], v[82:83], v[86:87]
	v_pk_mul_f32 v[82:83], v[120:121], v[96:97] op_sel_hi:[0,1]
	v_pk_fma_f32 v[118:119], v[118:119], v[84:85], v[82:83]
	s_nop 0
	s_waitcnt lgkmcnt(0)
	s_nop 0
	ds_read_b128 v[82:85], v160 offset:47264
	ds_read_b128 v[86:89], v160 offset:47280
	ds_read_b128 v[90:93], v160 offset:47296
	ds_read_b128 v[94:97], v160 offset:47312
	v_pk_mul_f32 v[134:135], v[76:77], v[14:15] op_sel_hi:[0,1]
	v_exp_f32_e32 v134, v134
	v_exp_f32_e32 v135, v135
	v_pk_mul_f32 v[136:137], v[76:77], v[16:17] op_sel_hi:[0,1]
	v_exp_f32_e32 v136, v136
	v_exp_f32_e32 v137, v137
	v_mul_f32_e32 v120, v76, v49
	v_pk_mul_f32 v[98:99], v[120:121], v[98:99] op_sel_hi:[0,1]
	v_pk_fma_f32 v[122:123], v[122:123], v[134:135], v[98:99]
	v_pk_mul_f32 v[98:99], v[120:121], v[100:101] op_sel_hi:[0,1]
	v_pk_fma_f32 v[124:125], v[124:125], v[136:137], v[98:99]
	v_pk_mul_f32 v[98:99], v[76:77], v[10:11] op_sel_hi:[0,1]
	v_exp_f32_e32 v98, v98
	v_exp_f32_e32 v99, v99
	v_pk_mul_f32 v[100:101], v[76:77], v[12:13] op_sel_hi:[0,1]
	v_exp_f32_e32 v100, v100
	v_exp_f32_e32 v101, v101
	v_pk_mul_f32 v[102:103], v[120:121], v[102:103] op_sel_hi:[0,1]
	v_pk_fma_f32 v[128:129], v[128:129], v[98:99], v[102:103]
	v_pk_mul_f32 v[98:99], v[120:121], v[104:105] op_sel_hi:[0,1]
	v_pk_fma_f32 v[126:127], v[126:127], v[100:101], v[98:99]
	v_pk_mul_f32 v[98:99], v[76:77], v[6:7] op_sel_hi:[0,1]
	v_exp_f32_e32 v98, v98
	v_exp_f32_e32 v99, v99
	v_pk_mul_f32 v[100:101], v[76:77], v[8:9] op_sel_hi:[0,1]
	v_exp_f32_e32 v100, v100
	v_exp_f32_e32 v101, v101
	v_pk_mul_f32 v[102:103], v[120:121], v[108:109] op_sel_hi:[0,1]
	v_pk_fma_f32 v[130:131], v[130:131], v[98:99], v[102:103]
	v_pk_mul_f32 v[98:99], v[120:121], v[110:111] op_sel_hi:[0,1]
	v_pk_fma_f32 v[132:133], v[132:133], v[100:101], v[98:99]
	v_pk_mul_f32 v[98:99], v[76:77], v[2:3] op_sel_hi:[0,1]
	v_exp_f32_e32 v98, v98
	v_exp_f32_e32 v99, v99
	v_pk_mul_f32 v[100:101], v[76:77], v[4:5] op_sel_hi:[0,1]
	v_exp_f32_e32 v100, v100
	v_exp_f32_e32 v101, v101
	v_pk_mul_f32 v[102:103], v[120:121], v[112:113] op_sel_hi:[0,1]
	v_pk_fma_f32 v[116:117], v[116:117], v[98:99], v[102:103]
	v_pk_mul_f32 v[98:99], v[120:121], v[114:115] op_sel_hi:[0,1]
	v_pk_fma_f32 v[118:119], v[118:119], v[100:101], v[98:99]
	s_nop 0
	s_waitcnt lgkmcnt(0)
	s_nop 0
	ds_read_b128 v[98:101], v160 offset:47472
	ds_read_b128 v[102:105], v160 offset:47488
	ds_read_b128 v[108:111], v160 offset:47504
	ds_read_b128 v[112:115], v160 offset:47520
	v_add_f32_e32 v19, 0, v80
	v_add_f32_e32 v19, v19, v20
	v_add_f32_e32 v19, v19, v22
	v_add_f32_e32 v19, v19, v24
	v_add_f32_e32 v19, v19, v26
	v_add_f32_e32 v19, v19, v28
	v_add_f32_e32 v19, v19, v30
	v_add_f32_e32 v19, v19, v32
	v_add_f32_e32 v19, v19, v34
	v_add_f32_e32 v19, v19, v36
	v_pk_mul_f32 v[134:135], v[78:79], v[14:15] op_sel_hi:[0,1]
	v_pk_mul_f32 v[136:137], v[78:79], v[16:17] op_sel_hi:[0,1]
	v_add_f32_e32 v19, v19, v38
	v_exp_f32_e32 v134, v134
	v_exp_f32_e32 v135, v135
	v_exp_f32_e32 v136, v136
	v_exp_f32_e32 v137, v137
	v_add_f32_e32 v19, v19, v40
	v_add_f32_e32 v19, v19, v42
	v_mul_f32_e32 v120, v78, v47
	v_add_f32_e32 v19, v19, v44
	v_pk_mul_f32 v[82:83], v[120:121], v[82:83] op_sel_hi:[0,1]
	v_pk_mul_f32 v[84:85], v[120:121], v[84:85] op_sel_hi:[0,1]
	v_add_f32_e32 v19, v19, v46
	v_pk_fma_f32 v[82:83], v[122:123], v[134:135], v[82:83]
	v_pk_fma_f32 v[84:85], v[124:125], v[136:137], v[84:85]
	v_pk_mul_f32 v[122:123], v[78:79], v[10:11] op_sel_hi:[0,1]
	v_pk_mul_f32 v[124:125], v[78:79], v[12:13] op_sel_hi:[0,1]
	v_add_f32_e32 v19, v19, v48
	v_exp_f32_e32 v122, v122
	v_exp_f32_e32 v123, v123
	v_exp_f32_e32 v124, v124
	v_exp_f32_e32 v125, v125
	v_add_f32_e32 v19, v19, v50
	v_add_f32_e32 v19, v19, v52
	v_add_f32_e32 v19, v19, v54
	v_pk_mul_f32 v[86:87], v[120:121], v[86:87] op_sel_hi:[0,1]
	v_pk_mul_f32 v[88:89], v[120:121], v[88:89] op_sel_hi:[0,1]
	v_add_f32_e32 v19, v19, v56
	v_pk_fma_f32 v[86:87], v[128:129], v[122:123], v[86:87]
	v_pk_fma_f32 v[88:89], v[126:127], v[124:125], v[88:89]
	v_pk_mul_f32 v[122:123], v[78:79], v[6:7] op_sel_hi:[0,1]
	v_pk_mul_f32 v[124:125], v[78:79], v[8:9] op_sel_hi:[0,1]
	v_add_f32_e32 v19, v19, v58
	v_exp_f32_e32 v122, v122
	v_exp_f32_e32 v123, v123
	v_exp_f32_e32 v124, v124
	v_exp_f32_e32 v125, v125
	v_add_f32_e32 v19, v19, v60
	v_add_f32_e32 v19, v19, v62
	v_add_f32_e32 v19, v19, v64
	v_pk_mul_f32 v[90:91], v[120:121], v[90:91] op_sel_hi:[0,1]
	v_pk_mul_f32 v[92:93], v[120:121], v[92:93] op_sel_hi:[0,1]
	v_add_f32_e32 v19, v19, v66
	v_pk_fma_f32 v[90:91], v[130:131], v[122:123], v[90:91]
	v_pk_fma_f32 v[92:93], v[132:133], v[124:125], v[92:93]
	v_pk_mul_f32 v[122:123], v[78:79], v[2:3] op_sel_hi:[0,1]
	v_pk_mul_f32 v[124:125], v[78:79], v[4:5] op_sel_hi:[0,1]
	v_add_f32_e32 v19, v19, v68
	v_exp_f32_e32 v122, v122
	v_exp_f32_e32 v123, v123
	v_exp_f32_e32 v124, v124
	v_exp_f32_e32 v125, v125
	v_add_f32_e32 v19, v19, v70
	v_add_f32_e32 v19, v19, v72
	v_add_f32_e32 v19, v19, v74
	v_pk_mul_f32 v[94:95], v[120:121], v[94:95] op_sel_hi:[0,1]
	v_pk_mul_f32 v[96:97], v[120:121], v[96:97] op_sel_hi:[0,1]
	v_add_f32_e32 v19, v19, v76
	v_pk_fma_f32 v[94:95], v[116:117], v[122:123], v[94:95]
	v_pk_fma_f32 v[96:97], v[118:119], v[124:125], v[96:97]
	v_add_f32_e32 v19, v19, v78
	s_waitcnt lgkmcnt(0)
	v_cvt_f32_f16_e32 v20, v106
	v_add_f32_e32 v19, v19, v18
	v_pk_mul_f32 v[4:5], v[18:19], v[4:5] op_sel_hi:[0,1]
	v_exp_f32_e32 v4, v4
	v_exp_f32_e32 v5, v5
	v_pk_mul_f32 v[14:15], v[18:19], v[14:15] op_sel_hi:[0,1]
	v_exp_f32_e32 v14, v14
	v_exp_f32_e32 v15, v15
	v_mul_f32_e32 v20, v18, v20
	v_pk_mul_f32 v[22:23], v[20:21], v[114:115] op_sel_hi:[0,1]
	v_pk_fma_f32 v[22:23], v[96:97], v[4:5], v[22:23]
	v_pk_mul_f32 v[4:5], v[20:21], v[98:99] op_sel_hi:[0,1]
	v_pk_fma_f32 v[14:15], v[82:83], v[14:15], v[4:5]
	v_pk_mul_f32 v[4:5], v[18:19], v[16:17] op_sel_hi:[0,1]
	v_exp_f32_e32 v4, v4
	v_exp_f32_e32 v5, v5
	v_pk_mul_f32 v[10:11], v[18:19], v[10:11] op_sel_hi:[0,1]
	v_exp_f32_e32 v10, v10
	v_exp_f32_e32 v11, v11
	v_pk_mul_f32 v[16:17], v[20:21], v[100:101] op_sel_hi:[0,1]
	v_pk_fma_f32 v[16:17], v[84:85], v[4:5], v[16:17]
	v_pk_mul_f32 v[4:5], v[20:21], v[102:103] op_sel_hi:[0,1]
	v_pk_fma_f32 v[10:11], v[86:87], v[10:11], v[4:5]
	v_pk_mul_f32 v[4:5], v[18:19], v[12:13] op_sel_hi:[0,1]
	v_exp_f32_e32 v4, v4
	v_exp_f32_e32 v5, v5
	v_pk_mul_f32 v[6:7], v[18:19], v[6:7] op_sel_hi:[0,1]
	v_exp_f32_e32 v6, v6
	v_exp_f32_e32 v7, v7
	v_pk_mul_f32 v[8:9], v[18:19], v[8:9] op_sel_hi:[0,1]
	v_exp_f32_e32 v8, v8
	v_exp_f32_e32 v9, v9
	v_pk_mul_f32 v[2:3], v[18:19], v[2:3] op_sel_hi:[0,1]
	v_pk_mul_f32 v[12:13], v[20:21], v[104:105] op_sel_hi:[0,1]
	v_exp_f32_e32 v2, v2
	v_exp_f32_e32 v3, v3
	v_pk_fma_f32 v[4:5], v[88:89], v[4:5], v[12:13]
	v_pk_mul_f32 v[12:13], v[20:21], v[108:109] op_sel_hi:[0,1]
	v_pk_fma_f32 v[6:7], v[90:91], v[6:7], v[12:13]
	v_pk_mul_f32 v[12:13], v[20:21], v[110:111] op_sel_hi:[0,1]
	v_pk_fma_f32 v[8:9], v[92:93], v[8:9], v[12:13]
	v_pk_mul_f32 v[12:13], v[20:21], v[112:113] op_sel_hi:[0,1]
	v_cvt_pk_f16_f32 v5, v4, v5
	v_cvt_pk_f16_f32 v4, v10, v11
	v_lshl_or_b32 v10, v0, 4, s6
	v_mov_b32_e32 v11, s7
	v_pk_fma_f32 v[12:13], v[94:95], v[2:3], v[12:13]
	v_cvt_pk_f16_f32 v3, v16, v17
	v_cvt_pk_f16_f32 v2, v14, v15
	v_lshl_add_u64 v[10:11], s[4:5], 0, v[10:11]
	s_movk_i32 s4, 0x2000
	global_store_dwordx4 v[10:11], v[2:5], off sc0 sc1
	global_store_dword v1, v19, s[0:1] sc0 sc1
	s_nop 0
	v_cvt_pk_f16_f32 v2, v6, v7
	v_add_co_u32_e32 v6, vcc, s4, v10
	v_cvt_pk_f16_f32 v5, v22, v23
	v_cvt_pk_f16_f32 v4, v12, v13
	v_cvt_pk_f16_f32 v3, v8, v9
	v_addc_co_u32_e32 v7, vcc, 0, v11, vcc
	global_store_dwordx4 v[6:7], v[2:5], off sc0 sc1
	s_endpgm

	.amdhsa_kernel _Z12k_conv_xprojPKDF16_PKfS2_S0_S0_S2_PDF16_S3_PfS2_S3_S4_
		.amdhsa_group_segment_fixed_size 47616
		.amdhsa_private_segment_fixed_size 0
		.amdhsa_kernarg_size 96
		.amdhsa_user_sgpr_count 2
		.amdhsa_user_sgpr_dispatch_ptr 0
		.amdhsa_user_sgpr_queue_ptr 0
		.amdhsa_user_sgpr_kernarg_segment_ptr 1
		.amdhsa_user_sgpr_dispatch_id 0
		.amdhsa_user_sgpr_kernarg_preload_length 0
		.amdhsa_user_sgpr_kernarg_preload_offset 0
		.amdhsa_user_sgpr_private_segment_size 0
		.amdhsa_uses_dynamic_stack 0
		.amdhsa_enable_private_segment 0
		.amdhsa_system_sgpr_workgroup_id_x 1
		.amdhsa_system_sgpr_workgroup_id_y 0
		.amdhsa_system_sgpr_workgroup_id_z 0
		.amdhsa_system_sgpr_workgroup_info 0
		.amdhsa_system_vgpr_workitem_id 0
		.amdhsa_next_free_vgpr 252
		.amdhsa_next_free_sgpr 91
		.amdhsa_accum_offset 252
		.amdhsa_reserve_vcc 1
		.amdhsa_float_round_mode_32 0
		.amdhsa_float_round_mode_16_64 0
		.amdhsa_float_denorm_mode_32 3
		.amdhsa_float_denorm_mode_16_64 3
		.amdhsa_dx10_clamp 1
		.amdhsa_ieee_mode 1
		.amdhsa_fp16_overflow 0
		.amdhsa_tg_split 0
		.amdhsa_exception_fp_ieee_invalid_op 0
		.amdhsa_exception_fp_denorm_src 0
		.amdhsa_exception_fp_ieee_div_zero 0
		.amdhsa_exception_fp_ieee_overflow 0
		.amdhsa_exception_fp_ieee_underflow 0
		.amdhsa_exception_fp_ieee_inexact 0
		.amdhsa_exception_int_div_zero 0
	.end_amdhsa_kernel

_Z4k_k2ILb0EEvPKDF16_S1_PKfS3_S3_S1_S1_PfS3_S3_S1_PDF16_PKiS4_S4_:
	s_load_dwordx2 s[24:25], s[0:1], 0x58
	s_load_dwordx8 s[4:11], s[0:1], 0x38
	s_load_dwordx4 s[20:23], s[0:1], 0x0
	s_load_dwordx8 s[12:19], s[0:1], 0x18
	s_load_dwordx2 s[54:55], s[0:1], 0x10
	s_lshl_b32 s3, s2, 5
	s_and_b32 s3, s3, 0xe0
	s_lshr_b32 s26, s2, 3
	s_or_b32 s3, s3, s26
	s_movk_i32 s26, 0x100
	s_lshl_b32 s28, s3, 5
	v_cmp_gt_u32_e32 vcc, s26, v0
	v_mov_b32_e32 v67, 0
	v_lshlrev_b32_e32 v66, 4, v0
	s_lshl_b32 s0, s3, 1
	s_and_b32 s26, s0, 0xffffffe
	s_mov_b32 s27, 0
	s_waitcnt lgkmcnt(0)
	v_lshl_add_u64 v[2:3], s[16:17], 0, v[66:67]
	s_lshl_b64 s[0:1], s[26:27], 13
	s_or_b32 s26, s26, 1
	v_lshl_add_u64 v[4:5], v[2:3], 0, s[0:1]
	s_lshl_b64 s[0:1], s[26:27], 13
	v_lshl_add_u64 v[2:3], v[2:3], 0, s[0:1]
	global_load_dwordx4 v[68:71], v[4:5], off
	global_load_dwordx4 v[72:75], v[2:3], off
	v_lshl_add_u64 v[2:3], s[12:13], 0, v[66:67]
	s_movk_i32 s29, 0x2000
	v_add_co_u32_e32 v4, vcc, s29, v2
	s_movk_i32 s52, 0x4000
	s_nop 0
	v_addc_co_u32_e32 v5, vcc, 0, v3, vcc
	v_add_co_u32_e32 v18, vcc, s52, v2
	s_movk_i32 s33, 0x6000
	s_nop 0
	v_addc_co_u32_e32 v19, vcc, 0, v3, vcc
	s_lshl_b32 s26, s3, 2
	global_load_dwordx4 v[14:17], v66, s[12:13]
	global_load_dwordx4 v[10:13], v[4:5], off
	global_load_dwordx4 v[6:9], v[18:19], off
	v_add_co_u32_e32 v18, vcc, s33, v2
	s_add_u32 s0, s24, 0x800000
	s_nop 0
	v_addc_co_u32_e32 v19, vcc, 0, v3, vcc
	s_addc_u32 s1, s25, 0
	s_lshl_b64 s[12:13], s[26:27], 13
	v_lshlrev_b32_e32 v20, 2, v0
	global_load_dwordx4 v[2:5], v[18:19], off
	global_load_dword v1, v20, s[14:15]
	v_or_b32_e32 v18, s12, v66
	v_mov_b32_e32 v19, s13
	s_or_b32 s12, s26, 1
	s_mov_b32 s13, s27
	s_lshl_b64 s[12:13], s[12:13], 13
	v_lshl_add_u64 v[76:77], s[22:23], 0, v[18:19]
	v_lshl_add_u64 v[78:79], s[20:21], 0, v[18:19]
	v_lshl_add_u64 v[80:81], s[0:1], 0, v[18:19]
	v_or_b32_e32 v18, s12, v66
	v_mov_b32_e32 v19, s13
	s_or_b32 s12, s26, 2
	s_mov_b32 s13, s27
	s_lshl_b64 s[12:13], s[12:13], 13
	s_or_b32 s26, s26, 3
	v_lshl_add_u64 v[82:83], s[22:23], 0, v[18:19]
	v_lshl_add_u64 v[84:85], s[20:21], 0, v[18:19]
	v_lshl_add_u64 v[86:87], s[0:1], 0, v[18:19]
	v_or_b32_e32 v18, s12, v66
	v_mov_b32_e32 v19, s13
	s_lshl_b64 s[12:13], s[26:27], 13
	v_lshl_add_u64 v[88:89], s[22:23], 0, v[18:19]
	v_lshl_add_u64 v[90:91], s[20:21], 0, v[18:19]
	v_lshl_add_u64 v[92:93], s[0:1], 0, v[18:19]
	v_or_b32_e32 v18, s12, v66
	v_mov_b32_e32 v19, s13
	v_lshl_add_u64 v[94:95], s[22:23], 0, v[18:19]
	v_lshl_add_u64 v[96:97], s[20:21], 0, v[18:19]
	v_lshl_add_u64 v[98:99], s[0:1], 0, v[18:19]
	global_load_dwordx4 v[62:65], v[76:77], off
	global_load_dwordx4 v[54:57], v[78:79], off
	global_load_dwordx4 v[58:61], v[80:81], off
	v_mov_b64_e32 v[212:213], v[82:83]
	v_mov_b64_e32 v[214:215], v[84:85]
	v_mov_b64_e32 v[216:217], v[86:87]
	v_mov_b64_e32 v[218:219], v[88:89]
	v_mov_b64_e32 v[220:221], v[90:91]
	v_mov_b64_e32 v[222:223], v[92:93]
	v_mov_b64_e32 v[224:225], v[94:95]
	v_mov_b64_e32 v[226:227], v[96:97]
	v_mov_b64_e32 v[228:229], v[98:99]
	s_lshl_b32 s30, s28, 7
	s_add_u32 s54, s54, s30
	s_addc_u32 s55, s55, 0
	s_load_dwordx16 s[36:51], s[54:55], 0x0
	s_load_dwordx16 s[72:87], s[54:55], 0x40
	s_load_dwordx16 s[56:71], s[54:55], 0x80
	s_load_dwordx8 s[88:95], s[54:55], 0xc0
	s_load_dwordx4 s[96:99], s[54:55], 0xe0
	s_load_dwordx4 s[20:23], s[54:55], 0xf0
	v_lshrrev_b32_e32 v196, 6, v0
	s_nop 1
	v_readfirstlane_b32 s16, v196
	s_nop 3
	s_lshl_b32 s16, s16, 9
	s_add_u32 s16, s54, s16
	s_addc_u32 s17, s55, 0
	s_load_dword s30, s[16:17], 0x0
	s_load_dword s30, s[16:17], 0x40
	s_load_dword s30, s[16:17], 0x80
	s_load_dword s30, s[16:17], 0xc0
	s_load_dword s30, s[16:17], 0x100
	s_load_dword s30, s[16:17], 0x140
	s_load_dword s30, s[16:17], 0x180
	s_load_dword s30, s[16:17], 0x1c0
	s_waitcnt vmcnt(9)
	v_cvt_f32_f16_e32 v134, v68
	v_cvt_f32_f16_sdwa v135, v68 dst_sel:DWORD dst_unused:UNUSED_PAD src0_sel:WORD_1
	v_cvt_f32_f16_e32 v136, v69
	v_cvt_f32_f16_sdwa v137, v69 dst_sel:DWORD dst_unused:UNUSED_PAD src0_sel:WORD_1
	v_cvt_f32_f16_e32 v138, v70
	v_cvt_f32_f16_sdwa v139, v70 dst_sel:DWORD dst_unused:UNUSED_PAD src0_sel:WORD_1
	v_cvt_f32_f16_e32 v140, v71
	v_cvt_f32_f16_sdwa v141, v71 dst_sel:DWORD dst_unused:UNUSED_PAD src0_sel:WORD_1
	s_waitcnt vmcnt(8)
	v_cvt_f32_f16_e32 v142, v72
	v_cvt_f32_f16_sdwa v143, v72 dst_sel:DWORD dst_unused:UNUSED_PAD src0_sel:WORD_1
	v_cvt_f32_f16_e32 v144, v73
	v_cvt_f32_f16_sdwa v145, v73 dst_sel:DWORD dst_unused:UNUSED_PAD src0_sel:WORD_1
	v_cvt_f32_f16_e32 v146, v74
	v_cvt_f32_f16_sdwa v147, v74 dst_sel:DWORD dst_unused:UNUSED_PAD src0_sel:WORD_1
	v_cvt_f32_f16_e32 v148, v75
	v_cvt_f32_f16_sdwa v149, v75 dst_sel:DWORD dst_unused:UNUSED_PAD src0_sel:WORD_1
	s_waitcnt lgkmcnt(0)
	v_lshlrev_b32_e32 v68, 1, v0
	s_waitcnt vmcnt(2)
	v_cvt_f32_f16_e32 v150, v62
	s_waitcnt vmcnt(1)
	v_pk_mul_f32 v[154:155], v[150:151], v[14:15] op_sel_hi:[0,1]
	v_exp_f32_e32 v154, v154
	v_exp_f32_e32 v155, v155
	v_pk_mul_f32 v[156:157], v[150:151], v[16:17] op_sel_hi:[0,1]
	v_exp_f32_e32 v156, v156
	v_exp_f32_e32 v157, v157
	v_fma_mix_f32 v152, v150, v54, 0 op_sel_hi:[0,1,0]
	v_pk_mul_f32 v[134:135], v[154:155], v[134:135]
	v_pk_fma_f32 v[134:135], v[152:153], s[36:37], v[134:135] op_sel_hi:[0, 1, 1]
	v_pk_fma_f32 v[70:71], s[72:73], v[134:135], 0 op_sel_hi:[1, 1, 0]
	v_pk_mul_f32 v[86:87], v[156:157], v[136:137]
	s_nop 0
	v_pk_fma_f32 v[136:137], v[152:153], s[38:39], v[86:87] op_sel_hi:[0, 1, 1]
	v_pk_mul_f32 v[72:73], v[150:151], v[10:11] op_sel_hi:[0,1]
	v_exp_f32_e32 v72, v72
	v_exp_f32_e32 v73, v73
	v_pk_mul_f32 v[86:87], v[150:151], v[12:13] op_sel_hi:[0,1]
	v_exp_f32_e32 v86, v86
	v_exp_f32_e32 v87, v87
	v_pk_mul_f32 v[72:73], v[72:73], v[138:139]
	v_pk_fma_f32 v[70:71], s[74:75], v[136:137], v[70:71]
	v_pk_fma_f32 v[138:139], v[152:153], s[40:41], v[72:73] op_sel_hi:[0, 1, 1]
	v_pk_mul_f32 v[72:73], v[86:87], v[140:141]
	v_pk_mul_f32 v[74:75], v[150:151], v[8:9] op_sel_hi:[0,1]
	v_pk_fma_f32 v[140:141], v[152:153], s[42:43], v[72:73] op_sel_hi:[0, 1, 1]
	v_pk_mul_f32 v[72:73], v[150:151], v[6:7] op_sel_hi:[0,1]
	v_exp_f32_e32 v72, v72
	v_exp_f32_e32 v73, v73
	v_exp_f32_e32 v74, v74
	v_exp_f32_e32 v75, v75
	v_pk_fma_f32 v[70:71], s[76:77], v[138:139], v[70:71]
	v_pk_mul_f32 v[72:73], v[72:73], v[142:143]
	v_pk_fma_f32 v[70:71], s[78:79], v[140:141], v[70:71]
	v_pk_fma_f32 v[142:143], v[152:153], s[44:45], v[72:73] op_sel_hi:[0, 1, 1]
	v_pk_mul_f32 v[72:73], v[74:75], v[144:145]
	v_pk_mul_f32 v[74:75], v[150:151], v[4:5] op_sel_hi:[0,1]
	v_pk_fma_f32 v[144:145], v[152:153], s[46:47], v[72:73] op_sel_hi:[0, 1, 1]
	v_pk_mul_f32 v[72:73], v[150:151], v[2:3] op_sel_hi:[0,1]
	v_exp_f32_e32 v72, v72
	v_exp_f32_e32 v73, v73
	v_exp_f32_e32 v74, v74
	v_exp_f32_e32 v75, v75
	v_pk_fma_f32 v[70:71], s[80:81], v[142:143], v[70:71]
	v_pk_mul_f32 v[72:73], v[72:73], v[146:147]
	v_pk_fma_f32 v[70:71], s[82:83], v[144:145], v[70:71]
	v_pk_fma_f32 v[146:147], v[152:153], s[48:49], v[72:73] op_sel_hi:[0, 1, 1]
	v_pk_mul_f32 v[72:73], v[74:75], v[148:149]
	v_pk_fma_f32 v[70:71], s[84:85], v[146:147], v[70:71]
	v_pk_fma_f32 v[148:149], v[152:153], s[50:51], v[72:73] op_sel_hi:[0, 1, 1]
	v_pk_fma_f32 v[70:71], s[86:87], v[148:149], v[70:71]
	s_nop 0
	v_add_f32_e32 v69, v70, v71
	v_fma_mix_f32 v69, v1, v54, v69 op_sel_hi:[0,1,0]
	s_waitcnt vmcnt(0)
	v_fma_mixlo_f16 v69, v69, v58, 0 op_sel_hi:[0,1,0]
	ds_write_b16 v68, v69 offset:4096
	global_load_dwordx4 v[50:53], v[212:213], off
	global_load_dwordx4 v[42:45], v[214:215], off
	global_load_dwordx4 v[46:49], v[216:217], off
	global_load_dwordx4 v[38:41], v[218:219], off
	global_load_dwordx4 v[30:33], v[220:221], off
	global_load_dwordx4 v[34:37], v[222:223], off
	global_load_dwordx4 v[26:29], v[224:225], off
	global_load_dwordx4 v[18:21], v[226:227], off
	global_load_dwordx4 v[22:25], v[228:229], off
	s_waitcnt lgkmcnt(0)
	s_load_dwordx16 s[36:51], s[54:55], 0x100
	s_load_dwordx16 s[72:87], s[54:55], 0x140
	v_cvt_f32_f16_sdwa v62, v62 dst_sel:DWORD dst_unused:UNUSED_PAD src0_sel:WORD_1
	v_pk_mul_f32 v[152:153], v[62:63], v[14:15] op_sel_hi:[0,1]
	v_exp_f32_e32 v152, v152
	v_exp_f32_e32 v153, v153
	v_pk_mul_f32 v[154:155], v[62:63], v[16:17] op_sel_hi:[0,1]
	v_exp_f32_e32 v154, v154
	v_exp_f32_e32 v155, v155
	v_fma_mix_f32 v150, v62, v54, 0 op_sel:[0,1,0] op_sel_hi:[0,1,0]
	v_pk_mul_f32 v[134:135], v[152:153], v[134:135]
	v_pk_fma_f32 v[134:135], v[150:151], s[56:57], v[134:135] op_sel_hi:[0, 1, 1]
	v_pk_fma_f32 v[102:103], s[88:89], v[134:135], 0 op_sel_hi:[1, 1, 0]
	v_pk_mul_f32 v[118:119], v[154:155], v[136:137]
	s_nop 0
	v_pk_fma_f32 v[136:137], v[150:151], s[58:59], v[118:119] op_sel_hi:[0, 1, 1]
	v_pk_mul_f32 v[104:105], v[62:63], v[10:11] op_sel_hi:[0,1]
	v_exp_f32_e32 v104, v104
	v_exp_f32_e32 v105, v105
	v_pk_mul_f32 v[118:119], v[62:63], v[12:13] op_sel_hi:[0,1]
	v_exp_f32_e32 v118, v118
	v_exp_f32_e32 v119, v119
	v_pk_mul_f32 v[104:105], v[104:105], v[138:139]
	v_pk_fma_f32 v[102:103], s[90:91], v[136:137], v[102:103]
	v_pk_fma_f32 v[138:139], v[150:151], s[60:61], v[104:105] op_sel_hi:[0, 1, 1]
	v_pk_mul_f32 v[104:105], v[118:119], v[140:141]
	v_pk_mul_f32 v[106:107], v[62:63], v[8:9] op_sel_hi:[0,1]
	v_pk_fma_f32 v[140:141], v[150:151], s[62:63], v[104:105] op_sel_hi:[0, 1, 1]
	v_pk_mul_f32 v[104:105], v[62:63], v[6:7] op_sel_hi:[0,1]
	v_exp_f32_e32 v104, v104
	v_exp_f32_e32 v105, v105
	v_exp_f32_e32 v106, v106
	v_exp_f32_e32 v107, v107
	v_pk_fma_f32 v[102:103], s[92:93], v[138:139], v[102:103]
	v_pk_mul_f32 v[104:105], v[104:105], v[142:143]
	v_pk_fma_f32 v[102:103], s[94:95], v[140:141], v[102:103]
	v_pk_fma_f32 v[142:143], v[150:151], s[64:65], v[104:105] op_sel_hi:[0, 1, 1]
	v_pk_mul_f32 v[104:105], v[106:107], v[144:145]
	v_pk_mul_f32 v[106:107], v[62:63], v[4:5] op_sel_hi:[0,1]
	v_pk_fma_f32 v[144:145], v[150:151], s[66:67], v[104:105] op_sel_hi:[0, 1, 1]
	v_pk_mul_f32 v[104:105], v[62:63], v[2:3] op_sel_hi:[0,1]
	v_exp_f32_e32 v104, v104
	v_exp_f32_e32 v105, v105
	v_exp_f32_e32 v106, v106
	v_exp_f32_e32 v107, v107
	v_pk_fma_f32 v[102:103], s[96:97], v[142:143], v[102:103]
	v_pk_mul_f32 v[104:105], v[104:105], v[146:147]
	v_pk_fma_f32 v[102:103], s[98:99], v[144:145], v[102:103]
	v_pk_fma_f32 v[146:147], v[150:151], s[68:69], v[104:105] op_sel_hi:[0, 1, 1]
	v_pk_mul_f32 v[104:105], v[106:107], v[148:149]
	v_pk_fma_f32 v[102:103], s[20:21], v[146:147], v[102:103]
	v_pk_fma_f32 v[148:149], v[150:151], s[70:71], v[104:105] op_sel_hi:[0, 1, 1]
	v_pk_fma_f32 v[102:103], s[22:23], v[148:149], v[102:103]
	s_nop 0
	v_add_f32_e32 v62, v102, v103
	v_fma_mix_f32 v54, v1, v54, v62 op_sel:[0,1,0] op_sel_hi:[0,1,0]
	v_fma_mixlo_f16 v54, v54, v58, 0 op_sel:[0,1,0] op_sel_hi:[0,1,0]
	ds_write_b16 v68, v54 offset:5136
	s_waitcnt lgkmcnt(0)
	s_load_dwordx16 s[56:71], s[54:55], 0x180
	s_load_dwordx8 s[88:95], s[54:55], 0x1c0
	s_load_dwordx4 s[96:99], s[54:55], 0x1e0
	s_load_dwordx4 s[20:23], s[54:55], 0x1f0
	v_cvt_f32_f16_e32 v54, v63
	v_pk_mul_f32 v[150:151], v[54:55], v[14:15] op_sel_hi:[0,1]
	v_exp_f32_e32 v150, v150
	v_exp_f32_e32 v151, v151
	v_pk_mul_f32 v[152:153], v[54:55], v[16:17] op_sel_hi:[0,1]
	v_exp_f32_e32 v152, v152
	v_exp_f32_e32 v153, v153
	v_fma_mix_f32 v58, v54, v55, 0 op_sel_hi:[0,1,0]
	v_pk_mul_f32 v[134:135], v[150:151], v[134:135]
	v_pk_fma_f32 v[134:135], v[58:59], s[36:37], v[134:135] op_sel_hi:[0, 1, 1]
	v_pk_fma_f32 v[70:71], s[72:73], v[134:135], 0 op_sel_hi:[1, 1, 0]
	v_pk_mul_f32 v[86:87], v[152:153], v[136:137]
	s_nop 0
	v_pk_fma_f32 v[136:137], v[58:59], s[38:39], v[86:87] op_sel_hi:[0, 1, 1]
	v_pk_mul_f32 v[72:73], v[54:55], v[10:11] op_sel_hi:[0,1]
	v_exp_f32_e32 v72, v72
	v_exp_f32_e32 v73, v73
	v_pk_mul_f32 v[86:87], v[54:55], v[12:13] op_sel_hi:[0,1]
	v_exp_f32_e32 v86, v86
	v_exp_f32_e32 v87, v87
	v_pk_mul_f32 v[72:73], v[72:73], v[138:139]
	v_pk_fma_f32 v[70:71], s[74:75], v[136:137], v[70:71]
	v_pk_fma_f32 v[138:139], v[58:59], s[40:41], v[72:73] op_sel_hi:[0, 1, 1]
	v_pk_mul_f32 v[72:73], v[86:87], v[140:141]
	v_pk_mul_f32 v[74:75], v[54:55], v[8:9] op_sel_hi:[0,1]
	v_pk_fma_f32 v[140:141], v[58:59], s[42:43], v[72:73] op_sel_hi:[0, 1, 1]
	v_pk_mul_f32 v[72:73], v[54:55], v[6:7] op_sel_hi:[0,1]
	v_exp_f32_e32 v72, v72
	v_exp_f32_e32 v73, v73
	v_exp_f32_e32 v74, v74
	v_exp_f32_e32 v75, v75
	v_pk_fma_f32 v[70:71], s[76:77], v[138:139], v[70:71]
	v_pk_mul_f32 v[72:73], v[72:73], v[142:143]
	v_pk_fma_f32 v[70:71], s[78:79], v[140:141], v[70:71]
	v_pk_fma_f32 v[142:143], v[58:59], s[44:45], v[72:73] op_sel_hi:[0, 1, 1]
	v_pk_mul_f32 v[72:73], v[74:75], v[144:145]
	v_pk_mul_f32 v[74:75], v[54:55], v[4:5] op_sel_hi:[0,1]
	v_pk_fma_f32 v[144:145], v[58:59], s[46:47], v[72:73] op_sel_hi:[0, 1, 1]
	v_pk_mul_f32 v[72:73], v[54:55], v[2:3] op_sel_hi:[0,1]
	v_exp_f32_e32 v72, v72
	v_exp_f32_e32 v73, v73
	v_exp_f32_e32 v74, v74
	v_exp_f32_e32 v75, v75
	v_pk_fma_f32 v[70:71], s[80:81], v[142:143], v[70:71]
	v_pk_mul_f32 v[72:73], v[72:73], v[146:147]
	v_pk_fma_f32 v[70:71], s[82:83], v[144:145], v[70:71]
	v_pk_fma_f32 v[146:147], v[58:59], s[48:49], v[72:73] op_sel_hi:[0, 1, 1]
	v_pk_mul_f32 v[72:73], v[74:75], v[148:149]
	v_pk_fma_f32 v[70:71], s[84:85], v[146:147], v[70:71]
	v_pk_fma_f32 v[148:149], v[58:59], s[50:51], v[72:73] op_sel_hi:[0, 1, 1]
	v_pk_fma_f32 v[70:71], s[86:87], v[148:149], v[70:71]
	s_nop 0
	v_add_f32_e32 v54, v70, v71
	v_fma_mix_f32 v54, v1, v55, v54 op_sel_hi:[0,1,0]
	v_fma_mixlo_f16 v54, v54, v59, 0 op_sel_hi:[0,1,0]
	ds_write_b16 v68, v54 offset:6176
	s_waitcnt lgkmcnt(0)
	s_load_dwordx16 s[36:51], s[54:55], 0x200
	s_load_dwordx16 s[72:87], s[54:55], 0x240
	v_cvt_f32_f16_sdwa v54, v63 dst_sel:DWORD dst_unused:UNUSED_PAD src0_sel:WORD_1
	v_pk_mul_f32 v[62:63], v[54:55], v[14:15] op_sel_hi:[0,1]
	v_exp_f32_e32 v62, v62
	v_exp_f32_e32 v63, v63
	v_pk_mul_f32 v[150:151], v[54:55], v[16:17] op_sel_hi:[0,1]
	v_exp_f32_e32 v150, v150
	v_exp_f32_e32 v151, v151
	v_fma_mix_f32 v58, v54, v55, 0 op_sel:[0,1,0] op_sel_hi:[0,1,0]
	v_pk_mul_f32 v[62:63], v[62:63], v[134:135]
	v_pk_fma_f32 v[62:63], v[58:59], s[56:57], v[62:63] op_sel_hi:[0, 1, 1]
	v_pk_fma_f32 v[102:103], s[88:89], v[62:63], 0 op_sel_hi:[1, 1, 0]
	v_pk_mul_f32 v[118:119], v[150:151], v[136:137]
	s_nop 0
	v_pk_fma_f32 v[134:135], v[58:59], s[58:59], v[118:119] op_sel_hi:[0, 1, 1]
	v_pk_mul_f32 v[104:105], v[54:55], v[10:11] op_sel_hi:[0,1]
	v_exp_f32_e32 v104, v104
	v_exp_f32_e32 v105, v105
	v_pk_mul_f32 v[118:119], v[54:55], v[12:13] op_sel_hi:[0,1]
	v_exp_f32_e32 v118, v118
	v_exp_f32_e32 v119, v119
	v_pk_mul_f32 v[104:105], v[104:105], v[138:139]
	v_pk_fma_f32 v[102:103], s[90:91], v[134:135], v[102:103]
	v_pk_fma_f32 v[136:137], v[58:59], s[60:61], v[104:105] op_sel_hi:[0, 1, 1]
	v_pk_mul_f32 v[104:105], v[118:119], v[140:141]
	v_pk_mul_f32 v[106:107], v[54:55], v[8:9] op_sel_hi:[0,1]
	v_pk_fma_f32 v[138:139], v[58:59], s[62:63], v[104:105] op_sel_hi:[0, 1, 1]
	v_pk_mul_f32 v[104:105], v[54:55], v[6:7] op_sel_hi:[0,1]
	v_exp_f32_e32 v104, v104
	v_exp_f32_e32 v105, v105
	v_exp_f32_e32 v106, v106
	v_exp_f32_e32 v107, v107
	v_pk_fma_f32 v[102:103], s[92:93], v[136:137], v[102:103]
	v_pk_mul_f32 v[104:105], v[104:105], v[142:143]
	v_pk_fma_f32 v[102:103], s[94:95], v[138:139], v[102:103]
	v_pk_fma_f32 v[140:141], v[58:59], s[64:65], v[104:105] op_sel_hi:[0, 1, 1]
	v_pk_mul_f32 v[104:105], v[106:107], v[144:145]
	v_pk_mul_f32 v[106:107], v[54:55], v[4:5] op_sel_hi:[0,1]
	v_pk_fma_f32 v[142:143], v[58:59], s[66:67], v[104:105] op_sel_hi:[0, 1, 1]
	v_pk_mul_f32 v[104:105], v[54:55], v[2:3] op_sel_hi:[0,1]
	v_exp_f32_e32 v104, v104
	v_exp_f32_e32 v105, v105
	v_exp_f32_e32 v106, v106
	v_exp_f32_e32 v107, v107
	v_pk_fma_f32 v[102:103], s[96:97], v[140:141], v[102:103]
	v_pk_mul_f32 v[104:105], v[104:105], v[146:147]
	v_pk_fma_f32 v[102:103], s[98:99], v[142:143], v[102:103]
	v_pk_fma_f32 v[144:145], v[58:59], s[68:69], v[104:105] op_sel_hi:[0, 1, 1]
	v_pk_mul_f32 v[104:105], v[106:107], v[148:149]
	v_pk_fma_f32 v[102:103], s[20:21], v[144:145], v[102:103]
	v_pk_fma_f32 v[146:147], v[58:59], s[70:71], v[104:105] op_sel_hi:[0, 1, 1]
	v_pk_fma_f32 v[102:103], s[22:23], v[146:147], v[102:103]
	s_nop 0
	v_add_f32_e32 v54, v102, v103
	v_fma_mix_f32 v54, v1, v55, v54 op_sel:[0,1,0] op_sel_hi:[0,1,0]
	v_fma_mixlo_f16 v54, v54, v59, 0 op_sel:[0,1,0] op_sel_hi:[0,1,0]
	ds_write_b16 v68, v54 offset:7216
	s_waitcnt lgkmcnt(0)
	s_load_dwordx16 s[56:71], s[54:55], 0x280
	s_load_dwordx8 s[88:95], s[54:55], 0x2c0
	s_load_dwordx4 s[96:99], s[54:55], 0x2e0
	s_load_dwordx4 s[20:23], s[54:55], 0x2f0
	v_cvt_f32_f16_e32 v54, v64
	v_pk_mul_f32 v[148:149], v[54:55], v[14:15] op_sel_hi:[0,1]
	v_exp_f32_e32 v148, v148
	v_exp_f32_e32 v149, v149
	v_pk_mul_f32 v[150:151], v[54:55], v[16:17] op_sel_hi:[0,1]
	v_exp_f32_e32 v150, v150
	v_exp_f32_e32 v151, v151
	v_fma_mix_f32 v58, v54, v56, 0 op_sel_hi:[0,1,0]
	v_pk_mul_f32 v[62:63], v[148:149], v[62:63]
	v_pk_fma_f32 v[62:63], v[58:59], s[36:37], v[62:63] op_sel_hi:[0, 1, 1]
	v_pk_fma_f32 v[70:71], s[72:73], v[62:63], 0 op_sel_hi:[1, 1, 0]
	v_pk_mul_f32 v[86:87], v[150:151], v[134:135]
	s_nop 0
	v_pk_fma_f32 v[134:135], v[58:59], s[38:39], v[86:87] op_sel_hi:[0, 1, 1]
	v_pk_mul_f32 v[72:73], v[54:55], v[10:11] op_sel_hi:[0,1]
	v_exp_f32_e32 v72, v72
	v_exp_f32_e32 v73, v73
	v_pk_mul_f32 v[86:87], v[54:55], v[12:13] op_sel_hi:[0,1]
	v_exp_f32_e32 v86, v86
	v_exp_f32_e32 v87, v87
	v_pk_mul_f32 v[72:73], v[72:73], v[136:137]
	v_pk_fma_f32 v[70:71], s[74:75], v[134:135], v[70:71]
	v_pk_fma_f32 v[136:137], v[58:59], s[40:41], v[72:73] op_sel_hi:[0, 1, 1]
	v_pk_mul_f32 v[72:73], v[86:87], v[138:139]
	v_pk_mul_f32 v[74:75], v[54:55], v[8:9] op_sel_hi:[0,1]
	v_pk_fma_f32 v[138:139], v[58:59], s[42:43], v[72:73] op_sel_hi:[0, 1, 1]
	v_pk_mul_f32 v[72:73], v[54:55], v[6:7] op_sel_hi:[0,1]
	v_exp_f32_e32 v72, v72
	v_exp_f32_e32 v73, v73
	v_exp_f32_e32 v74, v74
	v_exp_f32_e32 v75, v75
	v_pk_fma_f32 v[70:71], s[76:77], v[136:137], v[70:71]
	v_pk_mul_f32 v[72:73], v[72:73], v[140:141]
	v_pk_fma_f32 v[70:71], s[78:79], v[138:139], v[70:71]
	v_pk_fma_f32 v[140:141], v[58:59], s[44:45], v[72:73] op_sel_hi:[0, 1, 1]
	v_pk_mul_f32 v[72:73], v[74:75], v[142:143]
	v_pk_fma_f32 v[70:71], s[80:81], v[140:141], v[70:71]
	v_pk_fma_f32 v[142:143], v[58:59], s[46:47], v[72:73] op_sel_hi:[0, 1, 1]
	v_pk_mul_f32 v[72:73], v[54:55], v[2:3] op_sel_hi:[0,1]
	v_exp_f32_e32 v72, v72
	v_exp_f32_e32 v73, v73
	v_pk_mul_f32 v[54:55], v[54:55], v[4:5] op_sel_hi:[0,1]
	v_exp_f32_e32 v54, v54
	v_exp_f32_e32 v55, v55
	v_pk_mul_f32 v[72:73], v[72:73], v[144:145]
	v_pk_fma_f32 v[70:71], s[82:83], v[142:143], v[70:71]
	v_pk_fma_f32 v[144:145], v[58:59], s[48:49], v[72:73] op_sel_hi:[0, 1, 1]
	v_pk_mul_f32 v[54:55], v[54:55], v[146:147]
	v_pk_fma_f32 v[70:71], s[84:85], v[144:145], v[70:71]
	v_pk_fma_f32 v[54:55], v[58:59], s[50:51], v[54:55] op_sel_hi:[0, 1, 1]
	v_pk_fma_f32 v[58:59], s[86:87], v[54:55], v[70:71]
	s_nop 0
	v_add_f32_e32 v58, v58, v59
	v_fma_mix_f32 v58, v1, v56, v58 op_sel_hi:[0,1,0]
	v_fma_mixlo_f16 v58, v58, v60, 0 op_sel_hi:[0,1,0]
	ds_write_b16 v68, v58 offset:8256
	s_waitcnt lgkmcnt(0)
	s_load_dwordx16 s[36:51], s[54:55], 0x300
	s_load_dwordx16 s[72:87], s[54:55], 0x340
	v_cvt_f32_f16_sdwa v58, v64 dst_sel:DWORD dst_unused:UNUSED_PAD src0_sel:WORD_1
	v_pk_mul_f32 v[146:147], v[58:59], v[14:15] op_sel_hi:[0,1]
	v_exp_f32_e32 v146, v146
	v_exp_f32_e32 v147, v147
	v_pk_mul_f32 v[148:149], v[58:59], v[16:17] op_sel_hi:[0,1]
	v_exp_f32_e32 v148, v148
	v_exp_f32_e32 v149, v149
	v_fma_mix_f32 v64, v58, v56, 0 op_sel:[0,1,0] op_sel_hi:[0,1,0]
	v_pk_mul_f32 v[62:63], v[146:147], v[62:63]
	v_pk_fma_f32 v[62:63], v[64:65], s[56:57], v[62:63] op_sel_hi:[0, 1, 1]
	v_pk_fma_f32 v[102:103], s[88:89], v[62:63], 0 op_sel_hi:[1, 1, 0]
	v_pk_mul_f32 v[118:119], v[148:149], v[134:135]
	s_nop 0
	v_pk_fma_f32 v[134:135], v[64:65], s[58:59], v[118:119] op_sel_hi:[0, 1, 1]
	v_pk_mul_f32 v[104:105], v[58:59], v[10:11] op_sel_hi:[0,1]
	v_exp_f32_e32 v104, v104
	v_exp_f32_e32 v105, v105
	v_pk_mul_f32 v[118:119], v[58:59], v[12:13] op_sel_hi:[0,1]
	v_exp_f32_e32 v118, v118
	v_exp_f32_e32 v119, v119
	v_pk_mul_f32 v[104:105], v[104:105], v[136:137]
	v_pk_fma_f32 v[102:103], s[90:91], v[134:135], v[102:103]
	v_pk_fma_f32 v[136:137], v[64:65], s[60:61], v[104:105] op_sel_hi:[0, 1, 1]
	v_pk_mul_f32 v[104:105], v[118:119], v[138:139]
	v_pk_mul_f32 v[106:107], v[58:59], v[8:9] op_sel_hi:[0,1]
	v_pk_fma_f32 v[138:139], v[64:65], s[62:63], v[104:105] op_sel_hi:[0, 1, 1]
	v_pk_mul_f32 v[104:105], v[58:59], v[6:7] op_sel_hi:[0,1]
	v_exp_f32_e32 v104, v104
	v_exp_f32_e32 v105, v105
	v_exp_f32_e32 v106, v106
	v_exp_f32_e32 v107, v107
	v_pk_fma_f32 v[102:103], s[92:93], v[136:137], v[102:103]
	v_pk_mul_f32 v[104:105], v[104:105], v[140:141]
	v_pk_fma_f32 v[102:103], s[94:95], v[138:139], v[102:103]
	v_pk_fma_f32 v[140:141], v[64:65], s[64:65], v[104:105] op_sel_hi:[0, 1, 1]
	v_pk_mul_f32 v[104:105], v[106:107], v[142:143]
	v_pk_fma_f32 v[102:103], s[96:97], v[140:141], v[102:103]
	v_pk_fma_f32 v[142:143], v[64:65], s[66:67], v[104:105] op_sel_hi:[0, 1, 1]
	v_pk_mul_f32 v[104:105], v[58:59], v[2:3] op_sel_hi:[0,1]
	v_exp_f32_e32 v104, v104
	v_exp_f32_e32 v105, v105
	v_pk_mul_f32 v[58:59], v[58:59], v[4:5] op_sel_hi:[0,1]
	v_exp_f32_e32 v58, v58
	v_exp_f32_e32 v59, v59
	v_pk_mul_f32 v[104:105], v[104:105], v[144:145]
	v_pk_fma_f32 v[102:103], s[98:99], v[142:143], v[102:103]
	v_pk_fma_f32 v[144:145], v[64:65], s[68:69], v[104:105] op_sel_hi:[0, 1, 1]
	v_pk_mul_f32 v[54:55], v[58:59], v[54:55]
	v_pk_fma_f32 v[102:103], s[20:21], v[144:145], v[102:103]
	v_pk_fma_f32 v[54:55], v[64:65], s[70:71], v[54:55] op_sel_hi:[0, 1, 1]
	v_pk_fma_f32 v[58:59], s[22:23], v[54:55], v[102:103]
	s_nop 0
	v_add_f32_e32 v58, v58, v59
	v_fma_mix_f32 v56, v1, v56, v58 op_sel:[0,1,0] op_sel_hi:[0,1,0]
	v_fma_mixlo_f16 v56, v56, v60, 0 op_sel:[0,1,0] op_sel_hi:[0,1,0]
	ds_write_b16 v68, v56 offset:9296
	s_waitcnt lgkmcnt(0)
	s_load_dwordx16 s[56:71], s[54:55], 0x380
	s_load_dwordx8 s[88:95], s[54:55], 0x3c0
	s_load_dwordx4 s[96:99], s[54:55], 0x3e0
	s_load_dwordx4 s[20:23], s[54:55], 0x3f0
	v_cvt_f32_f16_e32 v56, v65
	v_pk_mul_f32 v[146:147], v[56:57], v[14:15] op_sel_hi:[0,1]
	v_exp_f32_e32 v146, v146
	v_exp_f32_e32 v147, v147
	v_pk_mul_f32 v[148:149], v[56:57], v[16:17] op_sel_hi:[0,1]
	v_exp_f32_e32 v148, v148
	v_exp_f32_e32 v149, v149
	v_fma_mix_f32 v58, v56, v57, 0 op_sel_hi:[0,1,0]
	v_pk_mul_f32 v[62:63], v[146:147], v[62:63]
	v_pk_fma_f32 v[62:63], v[58:59], s[36:37], v[62:63] op_sel_hi:[0, 1, 1]
	v_pk_fma_f32 v[70:71], s[72:73], v[62:63], 0 op_sel_hi:[1, 1, 0]
	v_pk_mul_f32 v[86:87], v[148:149], v[134:135]
	s_nop 0
	v_pk_fma_f32 v[134:135], v[58:59], s[38:39], v[86:87] op_sel_hi:[0, 1, 1]
	v_pk_mul_f32 v[72:73], v[56:57], v[10:11] op_sel_hi:[0,1]
	v_exp_f32_e32 v72, v72
	v_exp_f32_e32 v73, v73
	v_pk_mul_f32 v[86:87], v[56:57], v[12:13] op_sel_hi:[0,1]
	v_exp_f32_e32 v86, v86
	v_exp_f32_e32 v87, v87
	v_pk_mul_f32 v[72:73], v[72:73], v[136:137]
	v_pk_fma_f32 v[70:71], s[74:75], v[134:135], v[70:71]
	v_pk_fma_f32 v[136:137], v[58:59], s[40:41], v[72:73] op_sel_hi:[0, 1, 1]
	v_pk_mul_f32 v[72:73], v[86:87], v[138:139]
	v_pk_mul_f32 v[74:75], v[56:57], v[8:9] op_sel_hi:[0,1]
	v_pk_fma_f32 v[138:139], v[58:59], s[42:43], v[72:73] op_sel_hi:[0, 1, 1]
	v_pk_mul_f32 v[72:73], v[56:57], v[6:7] op_sel_hi:[0,1]
	v_exp_f32_e32 v72, v72
	v_exp_f32_e32 v73, v73
	v_exp_f32_e32 v74, v74
	v_exp_f32_e32 v75, v75
	v_pk_fma_f32 v[70:71], s[76:77], v[136:137], v[70:71]
	v_pk_mul_f32 v[72:73], v[72:73], v[140:141]
	v_pk_fma_f32 v[70:71], s[78:79], v[138:139], v[70:71]
	v_pk_fma_f32 v[140:141], v[58:59], s[44:45], v[72:73] op_sel_hi:[0, 1, 1]
	v_pk_mul_f32 v[72:73], v[74:75], v[142:143]
	v_pk_mul_f32 v[74:75], v[56:57], v[4:5] op_sel_hi:[0,1]
	v_pk_fma_f32 v[142:143], v[58:59], s[46:47], v[72:73] op_sel_hi:[0, 1, 1]
	v_pk_mul_f32 v[72:73], v[56:57], v[2:3] op_sel_hi:[0,1]
	v_exp_f32_e32 v72, v72
	v_exp_f32_e32 v73, v73
	v_exp_f32_e32 v74, v74
	v_exp_f32_e32 v75, v75
	v_pk_fma_f32 v[70:71], s[80:81], v[140:141], v[70:71]
	v_pk_mul_f32 v[72:73], v[72:73], v[144:145]
	v_pk_fma_f32 v[70:71], s[82:83], v[142:143], v[70:71]
	v_pk_fma_f32 v[144:145], v[58:59], s[48:49], v[72:73] op_sel_hi:[0, 1, 1]
	v_pk_mul_f32 v[54:55], v[74:75], v[54:55]
	v_pk_fma_f32 v[70:71], s[84:85], v[144:145], v[70:71]
	v_pk_fma_f32 v[54:55], v[58:59], s[50:51], v[54:55] op_sel_hi:[0, 1, 1]
	v_pk_fma_f32 v[58:59], s[86:87], v[54:55], v[70:71]
	s_nop 0
	v_add_f32_e32 v56, v58, v59
	v_fma_mix_f32 v56, v1, v57, v56 op_sel_hi:[0,1,0]
	v_fma_mixlo_f16 v56, v56, v61, 0 op_sel_hi:[0,1,0]
	ds_write_b16 v68, v56 offset:10336
	s_waitcnt lgkmcnt(0)
	s_load_dwordx16 s[36:51], s[54:55], 0x400
	s_load_dwordx16 s[72:87], s[54:55], 0x440
	v_cvt_f32_f16_sdwa v56, v65 dst_sel:DWORD dst_unused:UNUSED_PAD src0_sel:WORD_1
	v_pk_mul_f32 v[64:65], v[56:57], v[14:15] op_sel_hi:[0,1]
	v_pk_mul_f32 v[146:147], v[56:57], v[16:17] op_sel_hi:[0,1]
	v_exp_f32_e32 v64, v64
	v_exp_f32_e32 v65, v65
	v_exp_f32_e32 v146, v146
	v_exp_f32_e32 v147, v147
	v_fma_mix_f32 v58, v56, v57, 0 op_sel:[0,1,0] op_sel_hi:[0,1,0]
	v_pk_mul_f32 v[62:63], v[64:65], v[62:63]
	v_pk_mul_f32 v[64:65], v[146:147], v[134:135]
	v_pk_fma_f32 v[134:135], v[58:59], s[58:59], v[64:65] op_sel_hi:[0, 1, 1]
	v_pk_mul_f32 v[64:65], v[56:57], v[10:11] op_sel_hi:[0,1]
	v_pk_fma_f32 v[148:149], v[58:59], s[56:57], v[62:63] op_sel_hi:[0, 1, 1]
	v_exp_f32_e32 v64, v64
	v_exp_f32_e32 v65, v65
	v_pk_mul_f32 v[102:103], v[56:57], v[12:13] op_sel_hi:[0,1]
	v_exp_f32_e32 v102, v102
	v_exp_f32_e32 v103, v103
	v_pk_fma_f32 v[62:63], s[88:89], v[148:149], 0 op_sel_hi:[1, 1, 0]
	v_pk_mul_f32 v[64:65], v[64:65], v[136:137]
	v_pk_fma_f32 v[62:63], s[90:91], v[134:135], v[62:63]
	v_pk_fma_f32 v[136:137], v[58:59], s[60:61], v[64:65] op_sel_hi:[0, 1, 1]
	v_pk_mul_f32 v[64:65], v[102:103], v[138:139]
	v_pk_fma_f32 v[62:63], s[92:93], v[136:137], v[62:63]
	v_pk_fma_f32 v[122:123], v[58:59], s[62:63], v[64:65] op_sel_hi:[0, 1, 1]
	v_pk_mul_f32 v[64:65], v[56:57], v[6:7] op_sel_hi:[0,1]
	v_exp_f32_e32 v64, v64
	v_exp_f32_e32 v65, v65
	v_pk_mul_f32 v[102:103], v[56:57], v[8:9] op_sel_hi:[0,1]
	v_exp_f32_e32 v102, v102
	v_exp_f32_e32 v103, v103
	v_pk_mul_f32 v[64:65], v[64:65], v[140:141]
	v_pk_fma_f32 v[62:63], s[94:95], v[122:123], v[62:63]
	v_pk_fma_f32 v[124:125], v[58:59], s[64:65], v[64:65] op_sel_hi:[0, 1, 1]
	v_pk_mul_f32 v[64:65], v[102:103], v[142:143]
	v_pk_fma_f32 v[62:63], s[96:97], v[124:125], v[62:63]
	v_pk_fma_f32 v[126:127], v[58:59], s[66:67], v[64:65] op_sel_hi:[0, 1, 1]
	v_pk_mul_f32 v[64:65], v[56:57], v[2:3] op_sel_hi:[0,1]
	v_exp_f32_e32 v64, v64
	v_exp_f32_e32 v65, v65
	v_pk_mul_f32 v[102:103], v[56:57], v[4:5] op_sel_hi:[0,1]
	v_exp_f32_e32 v102, v102
	v_exp_f32_e32 v103, v103
	v_pk_mul_f32 v[64:65], v[64:65], v[144:145]
	v_pk_fma_f32 v[62:63], s[98:99], v[126:127], v[62:63]
	v_pk_fma_f32 v[128:129], v[58:59], s[68:69], v[64:65] op_sel_hi:[0, 1, 1]
	v_pk_mul_f32 v[54:55], v[102:103], v[54:55]
	v_pk_fma_f32 v[62:63], s[20:21], v[128:129], v[62:63]
	v_pk_fma_f32 v[130:131], v[58:59], s[70:71], v[54:55] op_sel_hi:[0, 1, 1]
	v_pk_fma_f32 v[54:55], s[22:23], v[130:131], v[62:63]
	s_nop 0
	v_add_f32_e32 v54, v54, v55
	v_fma_mix_f32 v54, v1, v57, v54 op_sel:[0,1,0] op_sel_hi:[0,1,0]
	v_fma_mixlo_f16 v54, v54, v61, 0 op_sel:[0,1,0] op_sel_hi:[0,1,0]
	ds_write_b16 v68, v54 offset:11376
	s_waitcnt lgkmcnt(0)
	s_load_dwordx16 s[56:71], s[54:55], 0x480
	s_load_dwordx8 s[88:95], s[54:55], 0x4c0
	s_load_dwordx4 s[96:99], s[54:55], 0x4e0
	s_load_dwordx4 s[20:23], s[54:55], 0x4f0
	s_waitcnt vmcnt(8)
	v_cvt_f32_f16_e32 v132, v50
	s_waitcnt vmcnt(7)
	v_pk_mul_f32 v[140:141], v[132:133], v[14:15] op_sel_hi:[0,1]
	v_exp_f32_e32 v140, v140
	v_exp_f32_e32 v141, v141
	v_pk_mul_f32 v[142:143], v[132:133], v[16:17] op_sel_hi:[0,1]
	v_exp_f32_e32 v142, v142
	v_exp_f32_e32 v143, v143
	v_fma_mix_f32 v138, v132, v42, 0 op_sel_hi:[0,1,0]
	v_pk_mul_f32 v[140:141], v[140:141], v[148:149]
	v_pk_fma_f32 v[140:141], v[138:139], s[36:37], v[140:141] op_sel_hi:[0, 1, 1]
	v_pk_fma_f32 v[70:71], s[72:73], v[140:141], 0 op_sel_hi:[1, 1, 0]
	v_pk_mul_f32 v[86:87], v[142:143], v[134:135]
	s_nop 0
	v_pk_fma_f32 v[134:135], v[138:139], s[38:39], v[86:87] op_sel_hi:[0, 1, 1]
	v_pk_mul_f32 v[72:73], v[132:133], v[10:11] op_sel_hi:[0,1]
	v_exp_f32_e32 v72, v72
	v_exp_f32_e32 v73, v73
	v_pk_mul_f32 v[86:87], v[132:133], v[12:13] op_sel_hi:[0,1]
	v_exp_f32_e32 v86, v86
	v_exp_f32_e32 v87, v87
	v_pk_mul_f32 v[72:73], v[72:73], v[136:137]
	v_pk_fma_f32 v[70:71], s[74:75], v[134:135], v[70:71]
	v_pk_fma_f32 v[136:137], v[138:139], s[40:41], v[72:73] op_sel_hi:[0, 1, 1]
	v_pk_mul_f32 v[72:73], v[86:87], v[122:123]
	v_pk_mul_f32 v[74:75], v[132:133], v[8:9] op_sel_hi:[0,1]
	v_pk_fma_f32 v[122:123], v[138:139], s[42:43], v[72:73] op_sel_hi:[0, 1, 1]
	v_pk_mul_f32 v[72:73], v[132:133], v[6:7] op_sel_hi:[0,1]
	v_exp_f32_e32 v72, v72
	v_exp_f32_e32 v73, v73
	v_exp_f32_e32 v74, v74
	v_exp_f32_e32 v75, v75
	v_pk_fma_f32 v[70:71], s[76:77], v[136:137], v[70:71]
	v_pk_mul_f32 v[72:73], v[72:73], v[124:125]
	v_pk_fma_f32 v[70:71], s[78:79], v[122:123], v[70:71]
	v_pk_fma_f32 v[124:125], v[138:139], s[44:45], v[72:73] op_sel_hi:[0, 1, 1]
	v_pk_mul_f32 v[72:73], v[74:75], v[126:127]
	v_pk_mul_f32 v[74:75], v[132:133], v[4:5] op_sel_hi:[0,1]
	v_pk_fma_f32 v[126:127], v[138:139], s[46:47], v[72:73] op_sel_hi:[0, 1, 1]
	v_pk_mul_f32 v[72:73], v[132:133], v[2:3] op_sel_hi:[0,1]
	v_exp_f32_e32 v72, v72
	v_exp_f32_e32 v73, v73
	v_exp_f32_e32 v74, v74
	v_exp_f32_e32 v75, v75
	v_pk_fma_f32 v[70:71], s[80:81], v[124:125], v[70:71]
	v_pk_mul_f32 v[72:73], v[72:73], v[128:129]
	v_pk_fma_f32 v[70:71], s[82:83], v[126:127], v[70:71]
	v_pk_fma_f32 v[128:129], v[138:139], s[48:49], v[72:73] op_sel_hi:[0, 1, 1]
	v_pk_mul_f32 v[72:73], v[74:75], v[130:131]
	v_pk_fma_f32 v[70:71], s[84:85], v[128:129], v[70:71]
	v_pk_fma_f32 v[130:131], v[138:139], s[50:51], v[72:73] op_sel_hi:[0, 1, 1]
	v_pk_fma_f32 v[70:71], s[86:87], v[130:131], v[70:71]
	s_nop 0
	v_add_f32_e32 v69, v70, v71
	v_fma_mix_f32 v69, v1, v42, v69 op_sel_hi:[0,1,0]
	s_waitcnt vmcnt(6)
	v_fma_mixlo_f16 v69, v69, v46, 0 op_sel_hi:[0,1,0]
	ds_write_b16 v68, v69 offset:12416
	s_waitcnt lgkmcnt(0)
	s_load_dwordx16 s[36:51], s[54:55], 0x500
	s_load_dwordx16 s[72:87], s[54:55], 0x540
	v_cvt_f32_f16_sdwa v50, v50 dst_sel:DWORD dst_unused:UNUSED_PAD src0_sel:WORD_1
	v_pk_mul_f32 v[138:139], v[50:51], v[14:15] op_sel_hi:[0,1]
	v_exp_f32_e32 v138, v138
	v_exp_f32_e32 v139, v139
	v_pk_mul_f32 v[142:143], v[50:51], v[16:17] op_sel_hi:[0,1]
	v_exp_f32_e32 v142, v142
	v_exp_f32_e32 v143, v143
	v_fma_mix_f32 v132, v50, v42, 0 op_sel:[0,1,0] op_sel_hi:[0,1,0]
	v_pk_mul_f32 v[138:139], v[138:139], v[140:141]
	v_pk_fma_f32 v[138:139], v[132:133], s[56:57], v[138:139] op_sel_hi:[0, 1, 1]
	v_pk_fma_f32 v[54:55], s[88:89], v[138:139], 0 op_sel_hi:[1, 1, 0]
	v_pk_mul_f32 v[106:107], v[142:143], v[134:135]
	s_nop 0
	v_pk_fma_f32 v[134:135], v[132:133], s[58:59], v[106:107] op_sel_hi:[0, 1, 1]
	v_pk_mul_f32 v[56:57], v[50:51], v[10:11] op_sel_hi:[0,1]
	v_exp_f32_e32 v56, v56
	v_exp_f32_e32 v57, v57
	v_pk_mul_f32 v[106:107], v[50:51], v[12:13] op_sel_hi:[0,1]
	v_exp_f32_e32 v106, v106
	v_exp_f32_e32 v107, v107
	v_pk_mul_f32 v[56:57], v[56:57], v[136:137]
	v_pk_fma_f32 v[54:55], s[90:91], v[134:135], v[54:55]
	v_pk_fma_f32 v[136:137], v[132:133], s[60:61], v[56:57] op_sel_hi:[0, 1, 1]
	v_pk_mul_f32 v[56:57], v[106:107], v[122:123]
	v_pk_mul_f32 v[58:59], v[50:51], v[8:9] op_sel_hi:[0,1]
	v_pk_fma_f32 v[122:123], v[132:133], s[62:63], v[56:57] op_sel_hi:[0, 1, 1]
	v_pk_mul_f32 v[56:57], v[50:51], v[6:7] op_sel_hi:[0,1]
	v_exp_f32_e32 v56, v56
	v_exp_f32_e32 v57, v57
	v_exp_f32_e32 v58, v58
	v_exp_f32_e32 v59, v59
	v_pk_fma_f32 v[54:55], s[92:93], v[136:137], v[54:55]
	v_pk_mul_f32 v[56:57], v[56:57], v[124:125]
	v_pk_fma_f32 v[54:55], s[94:95], v[122:123], v[54:55]
	v_pk_fma_f32 v[124:125], v[132:133], s[64:65], v[56:57] op_sel_hi:[0, 1, 1]
	v_pk_mul_f32 v[56:57], v[58:59], v[126:127]
	v_pk_mul_f32 v[58:59], v[50:51], v[4:5] op_sel_hi:[0,1]
	v_pk_fma_f32 v[126:127], v[132:133], s[66:67], v[56:57] op_sel_hi:[0, 1, 1]
	v_pk_mul_f32 v[56:57], v[50:51], v[2:3] op_sel_hi:[0,1]
	v_exp_f32_e32 v56, v56
	v_exp_f32_e32 v57, v57
	v_exp_f32_e32 v58, v58
	v_exp_f32_e32 v59, v59
	v_pk_fma_f32 v[54:55], s[96:97], v[124:125], v[54:55]
	v_pk_mul_f32 v[56:57], v[56:57], v[128:129]
	v_pk_fma_f32 v[54:55], s[98:99], v[126:127], v[54:55]
	v_pk_fma_f32 v[128:129], v[132:133], s[68:69], v[56:57] op_sel_hi:[0, 1, 1]
	v_pk_mul_f32 v[56:57], v[58:59], v[130:131]
	v_pk_fma_f32 v[54:55], s[20:21], v[128:129], v[54:55]
	v_pk_fma_f32 v[130:131], v[132:133], s[70:71], v[56:57] op_sel_hi:[0, 1, 1]
	v_pk_fma_f32 v[54:55], s[22:23], v[130:131], v[54:55]
	s_nop 0
	v_add_f32_e32 v50, v54, v55
	v_fma_mix_f32 v42, v1, v42, v50 op_sel:[0,1,0] op_sel_hi:[0,1,0]
	v_fma_mixlo_f16 v42, v42, v46, 0 op_sel:[0,1,0] op_sel_hi:[0,1,0]
	ds_write_b16 v68, v42 offset:13456
	s_waitcnt lgkmcnt(0)
	s_load_dwordx16 s[56:71], s[54:55], 0x580
	s_load_dwordx8 s[88:95], s[54:55], 0x5c0
	s_load_dwordx4 s[96:99], s[54:55], 0x5e0
	s_load_dwordx4 s[20:23], s[54:55], 0x5f0
	v_cvt_f32_f16_e32 v42, v51
	v_pk_mul_f32 v[132:133], v[42:43], v[14:15] op_sel_hi:[0,1]
	v_exp_f32_e32 v132, v132
	v_exp_f32_e32 v133, v133
	v_pk_mul_f32 v[140:141], v[42:43], v[16:17] op_sel_hi:[0,1]
	v_exp_f32_e32 v140, v140
	v_exp_f32_e32 v141, v141
	v_fma_mix_f32 v46, v42, v43, 0 op_sel_hi:[0,1,0]
	v_pk_mul_f32 v[132:133], v[132:133], v[138:139]
	v_pk_fma_f32 v[132:133], v[46:47], s[36:37], v[132:133] op_sel_hi:[0, 1, 1]
	v_pk_fma_f32 v[70:71], s[72:73], v[132:133], 0 op_sel_hi:[1, 1, 0]
	v_pk_mul_f32 v[86:87], v[140:141], v[134:135]
	s_nop 0
	v_pk_fma_f32 v[134:135], v[46:47], s[38:39], v[86:87] op_sel_hi:[0, 1, 1]
	v_pk_mul_f32 v[72:73], v[42:43], v[10:11] op_sel_hi:[0,1]
	v_exp_f32_e32 v72, v72
	v_exp_f32_e32 v73, v73
	v_pk_mul_f32 v[86:87], v[42:43], v[12:13] op_sel_hi:[0,1]
	v_exp_f32_e32 v86, v86
	v_exp_f32_e32 v87, v87
	v_pk_mul_f32 v[72:73], v[72:73], v[136:137]
	v_pk_fma_f32 v[70:71], s[74:75], v[134:135], v[70:71]
	v_pk_fma_f32 v[136:137], v[46:47], s[40:41], v[72:73] op_sel_hi:[0, 1, 1]
	v_pk_mul_f32 v[72:73], v[86:87], v[122:123]
	v_pk_mul_f32 v[74:75], v[42:43], v[8:9] op_sel_hi:[0,1]
	v_pk_fma_f32 v[122:123], v[46:47], s[42:43], v[72:73] op_sel_hi:[0, 1, 1]
	v_pk_mul_f32 v[72:73], v[42:43], v[6:7] op_sel_hi:[0,1]
	v_exp_f32_e32 v72, v72
	v_exp_f32_e32 v73, v73
	v_exp_f32_e32 v74, v74
	v_exp_f32_e32 v75, v75
	v_pk_fma_f32 v[70:71], s[76:77], v[136:137], v[70:71]
	v_pk_mul_f32 v[72:73], v[72:73], v[124:125]
	v_pk_fma_f32 v[70:71], s[78:79], v[122:123], v[70:71]
	v_pk_fma_f32 v[124:125], v[46:47], s[44:45], v[72:73] op_sel_hi:[0, 1, 1]
	v_pk_mul_f32 v[72:73], v[74:75], v[126:127]
	v_pk_mul_f32 v[74:75], v[42:43], v[4:5] op_sel_hi:[0,1]
	v_pk_fma_f32 v[126:127], v[46:47], s[46:47], v[72:73] op_sel_hi:[0, 1, 1]
	v_pk_mul_f32 v[72:73], v[42:43], v[2:3] op_sel_hi:[0,1]
	v_exp_f32_e32 v72, v72
	v_exp_f32_e32 v73, v73
	v_exp_f32_e32 v74, v74
	v_exp_f32_e32 v75, v75
	v_pk_fma_f32 v[70:71], s[80:81], v[124:125], v[70:71]
	v_pk_mul_f32 v[72:73], v[72:73], v[128:129]
	v_pk_fma_f32 v[70:71], s[82:83], v[126:127], v[70:71]
	v_pk_fma_f32 v[128:129], v[46:47], s[48:49], v[72:73] op_sel_hi:[0, 1, 1]
	v_pk_mul_f32 v[72:73], v[74:75], v[130:131]
	v_pk_fma_f32 v[70:71], s[84:85], v[128:129], v[70:71]
	v_pk_fma_f32 v[130:131], v[46:47], s[50:51], v[72:73] op_sel_hi:[0, 1, 1]
	v_pk_fma_f32 v[70:71], s[86:87], v[130:131], v[70:71]
	s_nop 0
	v_add_f32_e32 v42, v70, v71
	v_fma_mix_f32 v42, v1, v43, v42 op_sel_hi:[0,1,0]
	v_fma_mixlo_f16 v42, v42, v47, 0 op_sel_hi:[0,1,0]
	ds_write_b16 v68, v42 offset:14496
	s_waitcnt lgkmcnt(0)
	s_load_dwordx16 s[36:51], s[54:55], 0x600
	s_load_dwordx16 s[72:87], s[54:55], 0x640
	v_cvt_f32_f16_sdwa v42, v51 dst_sel:DWORD dst_unused:UNUSED_PAD src0_sel:WORD_1
	v_pk_mul_f32 v[50:51], v[42:43], v[14:15] op_sel_hi:[0,1]
	v_exp_f32_e32 v50, v50
	v_exp_f32_e32 v51, v51
	v_pk_mul_f32 v[138:139], v[42:43], v[16:17] op_sel_hi:[0,1]
	v_exp_f32_e32 v138, v138
	v_exp_f32_e32 v139, v139
	v_fma_mix_f32 v46, v42, v43, 0 op_sel:[0,1,0] op_sel_hi:[0,1,0]
	v_pk_mul_f32 v[50:51], v[50:51], v[132:133]
	v_pk_fma_f32 v[50:51], v[46:47], s[56:57], v[50:51] op_sel_hi:[0, 1, 1]
	v_pk_fma_f32 v[54:55], s[88:89], v[50:51], 0 op_sel_hi:[1, 1, 0]
	v_pk_mul_f32 v[106:107], v[138:139], v[134:135]
	s_nop 0
	v_pk_fma_f32 v[132:133], v[46:47], s[58:59], v[106:107] op_sel_hi:[0, 1, 1]
	v_pk_mul_f32 v[56:57], v[42:43], v[10:11] op_sel_hi:[0,1]
	v_exp_f32_e32 v56, v56
	v_exp_f32_e32 v57, v57
	v_pk_mul_f32 v[106:107], v[42:43], v[12:13] op_sel_hi:[0,1]
	v_exp_f32_e32 v106, v106
	v_exp_f32_e32 v107, v107
	v_pk_mul_f32 v[56:57], v[56:57], v[136:137]
	v_pk_fma_f32 v[54:55], s[90:91], v[132:133], v[54:55]
	v_pk_fma_f32 v[134:135], v[46:47], s[60:61], v[56:57] op_sel_hi:[0, 1, 1]
	v_pk_mul_f32 v[56:57], v[106:107], v[122:123]
	v_pk_mul_f32 v[58:59], v[42:43], v[8:9] op_sel_hi:[0,1]
	v_pk_fma_f32 v[122:123], v[46:47], s[62:63], v[56:57] op_sel_hi:[0, 1, 1]
	v_pk_mul_f32 v[56:57], v[42:43], v[6:7] op_sel_hi:[0,1]
	v_exp_f32_e32 v56, v56
	v_exp_f32_e32 v57, v57
	v_exp_f32_e32 v58, v58
	v_exp_f32_e32 v59, v59
	v_pk_fma_f32 v[54:55], s[92:93], v[134:135], v[54:55]
	v_pk_mul_f32 v[56:57], v[56:57], v[124:125]
	v_pk_fma_f32 v[54:55], s[94:95], v[122:123], v[54:55]
	v_pk_fma_f32 v[124:125], v[46:47], s[64:65], v[56:57] op_sel_hi:[0, 1, 1]
	v_pk_mul_f32 v[56:57], v[58:59], v[126:127]
	v_pk_mul_f32 v[58:59], v[42:43], v[4:5] op_sel_hi:[0,1]
	v_pk_fma_f32 v[126:127], v[46:47], s[66:67], v[56:57] op_sel_hi:[0, 1, 1]
	v_pk_mul_f32 v[56:57], v[42:43], v[2:3] op_sel_hi:[0,1]
	v_exp_f32_e32 v56, v56
	v_exp_f32_e32 v57, v57
	v_exp_f32_e32 v58, v58
	v_exp_f32_e32 v59, v59
	v_pk_fma_f32 v[54:55], s[96:97], v[124:125], v[54:55]
	v_pk_mul_f32 v[56:57], v[56:57], v[128:129]
	v_pk_fma_f32 v[54:55], s[98:99], v[126:127], v[54:55]
	v_pk_fma_f32 v[128:129], v[46:47], s[68:69], v[56:57] op_sel_hi:[0, 1, 1]
	v_pk_mul_f32 v[56:57], v[58:59], v[130:131]
	v_pk_fma_f32 v[54:55], s[20:21], v[128:129], v[54:55]
	v_pk_fma_f32 v[130:131], v[46:47], s[70:71], v[56:57] op_sel_hi:[0, 1, 1]
	v_pk_fma_f32 v[54:55], s[22:23], v[130:131], v[54:55]
	s_nop 0
	v_add_f32_e32 v42, v54, v55
	v_fma_mix_f32 v42, v1, v43, v42 op_sel:[0,1,0] op_sel_hi:[0,1,0]
	v_fma_mixlo_f16 v42, v42, v47, 0 op_sel:[0,1,0] op_sel_hi:[0,1,0]
	ds_write_b16 v68, v42 offset:15536
	s_waitcnt lgkmcnt(0)
	s_load_dwordx16 s[56:71], s[54:55], 0x680
	s_load_dwordx8 s[88:95], s[54:55], 0x6c0
	s_load_dwordx4 s[96:99], s[54:55], 0x6e0
	s_load_dwordx4 s[20:23], s[54:55], 0x6f0
	v_cvt_f32_f16_e32 v42, v52
	v_pk_mul_f32 v[136:137], v[42:43], v[14:15] op_sel_hi:[0,1]
	v_exp_f32_e32 v136, v136
	v_exp_f32_e32 v137, v137
	v_pk_mul_f32 v[138:139], v[42:43], v[16:17] op_sel_hi:[0,1]
	v_exp_f32_e32 v138, v138
	v_exp_f32_e32 v139, v139
	v_fma_mix_f32 v46, v42, v44, 0 op_sel_hi:[0,1,0]
	v_pk_mul_f32 v[50:51], v[136:137], v[50:51]
	v_pk_fma_f32 v[50:51], v[46:47], s[36:37], v[50:51] op_sel_hi:[0, 1, 1]
	v_pk_fma_f32 v[70:71], s[72:73], v[50:51], 0 op_sel_hi:[1, 1, 0]
	v_pk_mul_f32 v[86:87], v[138:139], v[132:133]
	s_nop 0
	v_pk_fma_f32 v[132:133], v[46:47], s[38:39], v[86:87] op_sel_hi:[0, 1, 1]
	v_pk_mul_f32 v[72:73], v[42:43], v[10:11] op_sel_hi:[0,1]
	v_exp_f32_e32 v72, v72
	v_exp_f32_e32 v73, v73
	v_pk_mul_f32 v[86:87], v[42:43], v[12:13] op_sel_hi:[0,1]
	v_exp_f32_e32 v86, v86
	v_exp_f32_e32 v87, v87
	v_pk_mul_f32 v[72:73], v[72:73], v[134:135]
	v_pk_fma_f32 v[70:71], s[74:75], v[132:133], v[70:71]
	v_pk_fma_f32 v[134:135], v[46:47], s[40:41], v[72:73] op_sel_hi:[0, 1, 1]
	v_pk_mul_f32 v[72:73], v[86:87], v[122:123]
	v_pk_mul_f32 v[74:75], v[42:43], v[8:9] op_sel_hi:[0,1]
	v_pk_fma_f32 v[122:123], v[46:47], s[42:43], v[72:73] op_sel_hi:[0, 1, 1]
	v_pk_mul_f32 v[72:73], v[42:43], v[6:7] op_sel_hi:[0,1]
	v_exp_f32_e32 v72, v72
	v_exp_f32_e32 v73, v73
	v_exp_f32_e32 v74, v74
	v_exp_f32_e32 v75, v75
	v_pk_fma_f32 v[70:71], s[76:77], v[134:135], v[70:71]
	v_pk_mul_f32 v[72:73], v[72:73], v[124:125]
	v_pk_fma_f32 v[70:71], s[78:79], v[122:123], v[70:71]
	v_pk_fma_f32 v[124:125], v[46:47], s[44:45], v[72:73] op_sel_hi:[0, 1, 1]
	v_pk_mul_f32 v[72:73], v[74:75], v[126:127]
	v_pk_fma_f32 v[70:71], s[80:81], v[124:125], v[70:71]
	v_pk_fma_f32 v[126:127], v[46:47], s[46:47], v[72:73] op_sel_hi:[0, 1, 1]
	v_pk_mul_f32 v[72:73], v[42:43], v[2:3] op_sel_hi:[0,1]
	v_exp_f32_e32 v72, v72
	v_exp_f32_e32 v73, v73
	v_pk_mul_f32 v[42:43], v[42:43], v[4:5] op_sel_hi:[0,1]
	v_exp_f32_e32 v42, v42
	v_exp_f32_e32 v43, v43
	v_pk_mul_f32 v[72:73], v[72:73], v[128:129]
	v_pk_fma_f32 v[70:71], s[82:83], v[126:127], v[70:71]
	v_pk_fma_f32 v[128:129], v[46:47], s[48:49], v[72:73] op_sel_hi:[0, 1, 1]
	v_pk_mul_f32 v[42:43], v[42:43], v[130:131]
	v_pk_fma_f32 v[70:71], s[84:85], v[128:129], v[70:71]
	v_pk_fma_f32 v[42:43], v[46:47], s[50:51], v[42:43] op_sel_hi:[0, 1, 1]
	v_pk_fma_f32 v[46:47], s[86:87], v[42:43], v[70:71]
	s_nop 0
	v_add_f32_e32 v46, v46, v47
	v_fma_mix_f32 v46, v1, v44, v46 op_sel_hi:[0,1,0]
	v_fma_mixlo_f16 v46, v46, v48, 0 op_sel_hi:[0,1,0]
	ds_write_b16 v68, v46 offset:16576
	s_waitcnt lgkmcnt(0)
	s_load_dwordx16 s[36:51], s[54:55], 0x700
	s_load_dwordx16 s[72:87], s[54:55], 0x740
	v_cvt_f32_f16_sdwa v46, v52 dst_sel:DWORD dst_unused:UNUSED_PAD src0_sel:WORD_1
	v_pk_mul_f32 v[130:131], v[46:47], v[14:15] op_sel_hi:[0,1]
	v_exp_f32_e32 v130, v130
	v_exp_f32_e32 v131, v131
	v_pk_mul_f32 v[136:137], v[46:47], v[16:17] op_sel_hi:[0,1]
	v_exp_f32_e32 v136, v136
	v_exp_f32_e32 v137, v137
	v_fma_mix_f32 v52, v46, v44, 0 op_sel:[0,1,0] op_sel_hi:[0,1,0]
	v_pk_mul_f32 v[50:51], v[130:131], v[50:51]
	v_pk_fma_f32 v[50:51], v[52:53], s[56:57], v[50:51] op_sel_hi:[0, 1, 1]
	v_pk_fma_f32 v[54:55], s[88:89], v[50:51], 0 op_sel_hi:[1, 1, 0]
	v_pk_mul_f32 v[106:107], v[136:137], v[132:133]
	s_nop 0
	v_pk_fma_f32 v[130:131], v[52:53], s[58:59], v[106:107] op_sel_hi:[0, 1, 1]
	v_pk_mul_f32 v[56:57], v[46:47], v[10:11] op_sel_hi:[0,1]
	v_exp_f32_e32 v56, v56
	v_exp_f32_e32 v57, v57
	v_pk_mul_f32 v[106:107], v[46:47], v[12:13] op_sel_hi:[0,1]
	v_exp_f32_e32 v106, v106
	v_exp_f32_e32 v107, v107
	v_pk_mul_f32 v[56:57], v[56:57], v[134:135]
	v_pk_fma_f32 v[54:55], s[90:91], v[130:131], v[54:55]
	v_pk_fma_f32 v[132:133], v[52:53], s[60:61], v[56:57] op_sel_hi:[0, 1, 1]
	v_pk_mul_f32 v[56:57], v[106:107], v[122:123]
	v_pk_mul_f32 v[58:59], v[46:47], v[8:9] op_sel_hi:[0,1]
	v_pk_fma_f32 v[122:123], v[52:53], s[62:63], v[56:57] op_sel_hi:[0, 1, 1]
	v_pk_mul_f32 v[56:57], v[46:47], v[6:7] op_sel_hi:[0,1]
	v_exp_f32_e32 v56, v56
	v_exp_f32_e32 v57, v57
	v_exp_f32_e32 v58, v58
	v_exp_f32_e32 v59, v59
	v_pk_fma_f32 v[54:55], s[92:93], v[132:133], v[54:55]
	v_pk_mul_f32 v[56:57], v[56:57], v[124:125]
	v_pk_fma_f32 v[54:55], s[94:95], v[122:123], v[54:55]
	v_pk_fma_f32 v[124:125], v[52:53], s[64:65], v[56:57] op_sel_hi:[0, 1, 1]
	v_pk_mul_f32 v[56:57], v[58:59], v[126:127]
	v_pk_fma_f32 v[54:55], s[96:97], v[124:125], v[54:55]
	v_pk_fma_f32 v[126:127], v[52:53], s[66:67], v[56:57] op_sel_hi:[0, 1, 1]
	v_pk_mul_f32 v[56:57], v[46:47], v[2:3] op_sel_hi:[0,1]
	v_exp_f32_e32 v56, v56
	v_exp_f32_e32 v57, v57
	v_pk_mul_f32 v[46:47], v[46:47], v[4:5] op_sel_hi:[0,1]
	v_exp_f32_e32 v46, v46
	v_exp_f32_e32 v47, v47
	v_pk_mul_f32 v[56:57], v[56:57], v[128:129]
	v_pk_fma_f32 v[54:55], s[98:99], v[126:127], v[54:55]
	v_pk_fma_f32 v[128:129], v[52:53], s[68:69], v[56:57] op_sel_hi:[0, 1, 1]
	v_pk_mul_f32 v[42:43], v[46:47], v[42:43]
	v_pk_fma_f32 v[54:55], s[20:21], v[128:129], v[54:55]
	v_pk_fma_f32 v[42:43], v[52:53], s[70:71], v[42:43] op_sel_hi:[0, 1, 1]
	v_pk_fma_f32 v[46:47], s[22:23], v[42:43], v[54:55]
	s_nop 0
	v_add_f32_e32 v46, v46, v47
	v_fma_mix_f32 v44, v1, v44, v46 op_sel:[0,1,0] op_sel_hi:[0,1,0]
	v_fma_mixlo_f16 v44, v44, v48, 0 op_sel:[0,1,0] op_sel_hi:[0,1,0]
	ds_write_b16 v68, v44 offset:17616
	s_waitcnt lgkmcnt(0)
	s_load_dwordx16 s[56:71], s[54:55], 0x780
	s_load_dwordx8 s[88:95], s[54:55], 0x7c0
	s_load_dwordx4 s[96:99], s[54:55], 0x7e0
	s_load_dwordx4 s[20:23], s[54:55], 0x7f0
	v_cvt_f32_f16_e32 v44, v53
	v_pk_mul_f32 v[134:135], v[44:45], v[14:15] op_sel_hi:[0,1]
	v_exp_f32_e32 v134, v134
	v_exp_f32_e32 v135, v135
	v_pk_mul_f32 v[136:137], v[44:45], v[16:17] op_sel_hi:[0,1]
	v_exp_f32_e32 v136, v136
	v_exp_f32_e32 v137, v137
	v_fma_mix_f32 v46, v44, v45, 0 op_sel_hi:[0,1,0]
	v_pk_mul_f32 v[50:51], v[134:135], v[50:51]
	v_pk_fma_f32 v[50:51], v[46:47], s[36:37], v[50:51] op_sel_hi:[0, 1, 1]
	v_pk_fma_f32 v[70:71], s[72:73], v[50:51], 0 op_sel_hi:[1, 1, 0]
	v_pk_mul_f32 v[86:87], v[136:137], v[130:131]
	s_nop 0
	v_pk_fma_f32 v[130:131], v[46:47], s[38:39], v[86:87] op_sel_hi:[0, 1, 1]
	v_pk_mul_f32 v[72:73], v[44:45], v[10:11] op_sel_hi:[0,1]
	v_exp_f32_e32 v72, v72
	v_exp_f32_e32 v73, v73
	v_pk_mul_f32 v[86:87], v[44:45], v[12:13] op_sel_hi:[0,1]
	v_exp_f32_e32 v86, v86
	v_exp_f32_e32 v87, v87
	v_pk_mul_f32 v[72:73], v[72:73], v[132:133]
	v_pk_fma_f32 v[70:71], s[74:75], v[130:131], v[70:71]
	v_pk_fma_f32 v[132:133], v[46:47], s[40:41], v[72:73] op_sel_hi:[0, 1, 1]
	v_pk_mul_f32 v[72:73], v[86:87], v[122:123]
	v_pk_mul_f32 v[74:75], v[44:45], v[8:9] op_sel_hi:[0,1]
	v_pk_fma_f32 v[122:123], v[46:47], s[42:43], v[72:73] op_sel_hi:[0, 1, 1]
	v_pk_mul_f32 v[72:73], v[44:45], v[6:7] op_sel_hi:[0,1]
	v_exp_f32_e32 v72, v72
	v_exp_f32_e32 v73, v73
	v_exp_f32_e32 v74, v74
	v_exp_f32_e32 v75, v75
	v_pk_fma_f32 v[70:71], s[76:77], v[132:133], v[70:71]
	v_pk_mul_f32 v[72:73], v[72:73], v[124:125]
	v_pk_fma_f32 v[70:71], s[78:79], v[122:123], v[70:71]
	v_pk_fma_f32 v[124:125], v[46:47], s[44:45], v[72:73] op_sel_hi:[0, 1, 1]
	v_pk_mul_f32 v[72:73], v[74:75], v[126:127]
	v_pk_mul_f32 v[74:75], v[44:45], v[4:5] op_sel_hi:[0,1]
	v_pk_fma_f32 v[126:127], v[46:47], s[46:47], v[72:73] op_sel_hi:[0, 1, 1]
	v_pk_mul_f32 v[72:73], v[44:45], v[2:3] op_sel_hi:[0,1]
	v_exp_f32_e32 v72, v72
	v_exp_f32_e32 v73, v73
	v_exp_f32_e32 v74, v74
	v_exp_f32_e32 v75, v75
	v_pk_fma_f32 v[70:71], s[80:81], v[124:125], v[70:71]
	v_pk_mul_f32 v[72:73], v[72:73], v[128:129]
	v_pk_fma_f32 v[70:71], s[82:83], v[126:127], v[70:71]
	v_pk_fma_f32 v[128:129], v[46:47], s[48:49], v[72:73] op_sel_hi:[0, 1, 1]
	v_pk_mul_f32 v[42:43], v[74:75], v[42:43]
	v_pk_fma_f32 v[70:71], s[84:85], v[128:129], v[70:71]
	v_pk_fma_f32 v[42:43], v[46:47], s[50:51], v[42:43] op_sel_hi:[0, 1, 1]
	v_pk_fma_f32 v[46:47], s[86:87], v[42:43], v[70:71]
	s_nop 0
	v_add_f32_e32 v44, v46, v47
	v_fma_mix_f32 v44, v1, v45, v44 op_sel_hi:[0,1,0]
	v_fma_mixlo_f16 v44, v44, v49, 0 op_sel_hi:[0,1,0]
	ds_write_b16 v68, v44 offset:18656
	s_waitcnt lgkmcnt(0)
	s_load_dwordx16 s[36:51], s[54:55], 0x800
	s_load_dwordx16 s[72:87], s[54:55], 0x840
	v_cvt_f32_f16_sdwa v44, v53 dst_sel:DWORD dst_unused:UNUSED_PAD src0_sel:WORD_1
	v_pk_mul_f32 v[52:53], v[44:45], v[14:15] op_sel_hi:[0,1]
	v_pk_mul_f32 v[134:135], v[44:45], v[16:17] op_sel_hi:[0,1]
	v_exp_f32_e32 v52, v52
	v_exp_f32_e32 v53, v53
	v_exp_f32_e32 v134, v134
	v_exp_f32_e32 v135, v135
	v_fma_mix_f32 v46, v44, v45, 0 op_sel:[0,1,0] op_sel_hi:[0,1,0]
	v_pk_mul_f32 v[50:51], v[52:53], v[50:51]
	v_pk_mul_f32 v[52:53], v[134:135], v[130:131]
	v_pk_fma_f32 v[130:131], v[46:47], s[58:59], v[52:53] op_sel_hi:[0, 1, 1]
	v_pk_mul_f32 v[52:53], v[44:45], v[10:11] op_sel_hi:[0,1]
	v_pk_fma_f32 v[136:137], v[46:47], s[56:57], v[50:51] op_sel_hi:[0, 1, 1]
	v_exp_f32_e32 v52, v52
	v_exp_f32_e32 v53, v53
	v_pk_mul_f32 v[54:55], v[44:45], v[12:13] op_sel_hi:[0,1]
	v_exp_f32_e32 v54, v54
	v_exp_f32_e32 v55, v55
	v_pk_fma_f32 v[50:51], s[88:89], v[136:137], 0 op_sel_hi:[1, 1, 0]
	v_pk_mul_f32 v[52:53], v[52:53], v[132:133]
	v_pk_fma_f32 v[50:51], s[90:91], v[130:131], v[50:51]
	v_pk_fma_f32 v[132:133], v[46:47], s[60:61], v[52:53] op_sel_hi:[0, 1, 1]
	v_pk_mul_f32 v[52:53], v[54:55], v[122:123]
	v_pk_fma_f32 v[50:51], s[92:93], v[132:133], v[50:51]
	v_pk_fma_f32 v[110:111], v[46:47], s[62:63], v[52:53] op_sel_hi:[0, 1, 1]
	v_pk_mul_f32 v[52:53], v[44:45], v[6:7] op_sel_hi:[0,1]
	v_exp_f32_e32 v52, v52
	v_exp_f32_e32 v53, v53
	v_pk_mul_f32 v[54:55], v[44:45], v[8:9] op_sel_hi:[0,1]
	v_exp_f32_e32 v54, v54
	v_exp_f32_e32 v55, v55
	v_pk_mul_f32 v[52:53], v[52:53], v[124:125]
	v_pk_fma_f32 v[50:51], s[94:95], v[110:111], v[50:51]
	v_pk_fma_f32 v[112:113], v[46:47], s[64:65], v[52:53] op_sel_hi:[0, 1, 1]
	v_pk_mul_f32 v[52:53], v[54:55], v[126:127]
	v_pk_fma_f32 v[50:51], s[96:97], v[112:113], v[50:51]
	v_pk_fma_f32 v[114:115], v[46:47], s[66:67], v[52:53] op_sel_hi:[0, 1, 1]
	v_pk_mul_f32 v[52:53], v[44:45], v[2:3] op_sel_hi:[0,1]
	v_exp_f32_e32 v52, v52
	v_exp_f32_e32 v53, v53
	v_pk_mul_f32 v[54:55], v[44:45], v[4:5] op_sel_hi:[0,1]
	v_exp_f32_e32 v54, v54
	v_exp_f32_e32 v55, v55
	v_pk_mul_f32 v[52:53], v[52:53], v[128:129]
	v_pk_fma_f32 v[50:51], s[98:99], v[114:115], v[50:51]
	v_pk_fma_f32 v[116:117], v[46:47], s[68:69], v[52:53] op_sel_hi:[0, 1, 1]
	v_pk_mul_f32 v[42:43], v[54:55], v[42:43]
	v_pk_fma_f32 v[50:51], s[20:21], v[116:117], v[50:51]
	v_pk_fma_f32 v[118:119], v[46:47], s[70:71], v[42:43] op_sel_hi:[0, 1, 1]
	v_pk_fma_f32 v[42:43], s[22:23], v[118:119], v[50:51]
	s_nop 0
	v_add_f32_e32 v42, v42, v43
	v_fma_mix_f32 v42, v1, v45, v42 op_sel:[0,1,0] op_sel_hi:[0,1,0]
	v_fma_mixlo_f16 v42, v42, v49, 0 op_sel:[0,1,0] op_sel_hi:[0,1,0]
	ds_write_b16 v68, v42 offset:19696
	s_waitcnt lgkmcnt(0)
	s_load_dwordx16 s[56:71], s[54:55], 0x880
	s_load_dwordx8 s[88:95], s[54:55], 0x8c0
	s_load_dwordx4 s[96:99], s[54:55], 0x8e0
	s_load_dwordx4 s[20:23], s[54:55], 0x8f0
	s_waitcnt vmcnt(5)
	v_cvt_f32_f16_e32 v120, v38
	s_waitcnt vmcnt(4)
	v_pk_mul_f32 v[124:125], v[120:121], v[14:15] op_sel_hi:[0,1]
	v_exp_f32_e32 v124, v124
	v_exp_f32_e32 v125, v125
	v_pk_mul_f32 v[126:127], v[120:121], v[16:17] op_sel_hi:[0,1]
	v_exp_f32_e32 v126, v126
	v_exp_f32_e32 v127, v127
	v_fma_mix_f32 v122, v120, v30, 0 op_sel_hi:[0,1,0]
	v_pk_mul_f32 v[124:125], v[124:125], v[136:137]
	v_pk_fma_f32 v[124:125], v[122:123], s[36:37], v[124:125] op_sel_hi:[0, 1, 1]
	v_pk_fma_f32 v[70:71], s[72:73], v[124:125], 0 op_sel_hi:[1, 1, 0]
	v_pk_mul_f32 v[86:87], v[126:127], v[130:131]
	s_nop 0
	v_pk_fma_f32 v[126:127], v[122:123], s[38:39], v[86:87] op_sel_hi:[0, 1, 1]
	v_pk_mul_f32 v[72:73], v[120:121], v[10:11] op_sel_hi:[0,1]
	v_exp_f32_e32 v72, v72
	v_exp_f32_e32 v73, v73
	v_pk_mul_f32 v[86:87], v[120:121], v[12:13] op_sel_hi:[0,1]
	v_exp_f32_e32 v86, v86
	v_exp_f32_e32 v87, v87
	v_pk_mul_f32 v[72:73], v[72:73], v[132:133]
	v_pk_fma_f32 v[70:71], s[74:75], v[126:127], v[70:71]
	v_pk_fma_f32 v[128:129], v[122:123], s[40:41], v[72:73] op_sel_hi:[0, 1, 1]
	v_pk_mul_f32 v[72:73], v[86:87], v[110:111]
	v_pk_mul_f32 v[74:75], v[120:121], v[8:9] op_sel_hi:[0,1]
	v_pk_fma_f32 v[110:111], v[122:123], s[42:43], v[72:73] op_sel_hi:[0, 1, 1]
	v_pk_mul_f32 v[72:73], v[120:121], v[6:7] op_sel_hi:[0,1]
	v_exp_f32_e32 v72, v72
	v_exp_f32_e32 v73, v73
	v_exp_f32_e32 v74, v74
	v_exp_f32_e32 v75, v75
	v_pk_fma_f32 v[70:71], s[76:77], v[128:129], v[70:71]
	v_pk_mul_f32 v[72:73], v[72:73], v[112:113]
	v_pk_fma_f32 v[70:71], s[78:79], v[110:111], v[70:71]
	v_pk_fma_f32 v[112:113], v[122:123], s[44:45], v[72:73] op_sel_hi:[0, 1, 1]
	v_pk_mul_f32 v[72:73], v[74:75], v[114:115]
	v_pk_mul_f32 v[74:75], v[120:121], v[4:5] op_sel_hi:[0,1]
	v_pk_fma_f32 v[114:115], v[122:123], s[46:47], v[72:73] op_sel_hi:[0, 1, 1]
	v_pk_mul_f32 v[72:73], v[120:121], v[2:3] op_sel_hi:[0,1]
	v_exp_f32_e32 v72, v72
	v_exp_f32_e32 v73, v73
	v_exp_f32_e32 v74, v74
	v_exp_f32_e32 v75, v75
	v_pk_fma_f32 v[70:71], s[80:81], v[112:113], v[70:71]
	v_pk_mul_f32 v[72:73], v[72:73], v[116:117]
	v_pk_fma_f32 v[70:71], s[82:83], v[114:115], v[70:71]
	v_pk_fma_f32 v[116:117], v[122:123], s[48:49], v[72:73] op_sel_hi:[0, 1, 1]
	v_pk_mul_f32 v[72:73], v[74:75], v[118:119]
	v_pk_fma_f32 v[70:71], s[84:85], v[116:117], v[70:71]
	v_pk_fma_f32 v[118:119], v[122:123], s[50:51], v[72:73] op_sel_hi:[0, 1, 1]
	v_pk_fma_f32 v[70:71], s[86:87], v[118:119], v[70:71]
	s_nop 0
	v_add_f32_e32 v69, v70, v71
	v_fma_mix_f32 v69, v1, v30, v69 op_sel_hi:[0,1,0]
	s_waitcnt vmcnt(3)
	v_fma_mixlo_f16 v69, v69, v34, 0 op_sel_hi:[0,1,0]
	ds_write_b16 v68, v69 offset:20736
	s_waitcnt lgkmcnt(0)
	s_load_dwordx16 s[36:51], s[54:55], 0x900
	s_load_dwordx16 s[72:87], s[54:55], 0x940
	v_cvt_f32_f16_sdwa v38, v38 dst_sel:DWORD dst_unused:UNUSED_PAD src0_sel:WORD_1
	v_pk_mul_f32 v[122:123], v[38:39], v[14:15] op_sel_hi:[0,1]
	v_exp_f32_e32 v122, v122
	v_exp_f32_e32 v123, v123
	v_pk_mul_f32 v[130:131], v[38:39], v[16:17] op_sel_hi:[0,1]
	v_exp_f32_e32 v130, v130
	v_exp_f32_e32 v131, v131
	v_fma_mix_f32 v120, v38, v30, 0 op_sel:[0,1,0] op_sel_hi:[0,1,0]
	v_pk_mul_f32 v[122:123], v[122:123], v[124:125]
	v_pk_fma_f32 v[122:123], v[120:121], s[56:57], v[122:123] op_sel_hi:[0, 1, 1]
	v_pk_fma_f32 v[42:43], s[88:89], v[122:123], 0 op_sel_hi:[1, 1, 0]
	v_pk_mul_f32 v[58:59], v[130:131], v[126:127]
	s_nop 0
	v_pk_fma_f32 v[124:125], v[120:121], s[58:59], v[58:59] op_sel_hi:[0, 1, 1]
	v_pk_mul_f32 v[44:45], v[38:39], v[10:11] op_sel_hi:[0,1]
	v_exp_f32_e32 v44, v44
	v_exp_f32_e32 v45, v45
	v_pk_mul_f32 v[58:59], v[38:39], v[12:13] op_sel_hi:[0,1]
	v_exp_f32_e32 v58, v58
	v_exp_f32_e32 v59, v59
	v_pk_mul_f32 v[44:45], v[44:45], v[128:129]
	v_pk_fma_f32 v[42:43], s[90:91], v[124:125], v[42:43]
	v_pk_fma_f32 v[126:127], v[120:121], s[60:61], v[44:45] op_sel_hi:[0, 1, 1]
	v_pk_mul_f32 v[44:45], v[58:59], v[110:111]
	v_pk_mul_f32 v[46:47], v[38:39], v[8:9] op_sel_hi:[0,1]
	v_pk_fma_f32 v[110:111], v[120:121], s[62:63], v[44:45] op_sel_hi:[0, 1, 1]
	v_pk_mul_f32 v[44:45], v[38:39], v[6:7] op_sel_hi:[0,1]
	v_exp_f32_e32 v44, v44
	v_exp_f32_e32 v45, v45
	v_exp_f32_e32 v46, v46
	v_exp_f32_e32 v47, v47
	v_pk_fma_f32 v[42:43], s[92:93], v[126:127], v[42:43]
	v_pk_mul_f32 v[44:45], v[44:45], v[112:113]
	v_pk_fma_f32 v[42:43], s[94:95], v[110:111], v[42:43]
	v_pk_fma_f32 v[112:113], v[120:121], s[64:65], v[44:45] op_sel_hi:[0, 1, 1]
	v_pk_mul_f32 v[44:45], v[46:47], v[114:115]
	v_pk_mul_f32 v[46:47], v[38:39], v[4:5] op_sel_hi:[0,1]
	v_pk_fma_f32 v[114:115], v[120:121], s[66:67], v[44:45] op_sel_hi:[0, 1, 1]
	v_pk_mul_f32 v[44:45], v[38:39], v[2:3] op_sel_hi:[0,1]
	v_exp_f32_e32 v44, v44
	v_exp_f32_e32 v45, v45
	v_exp_f32_e32 v46, v46
	v_exp_f32_e32 v47, v47
	v_pk_fma_f32 v[42:43], s[96:97], v[112:113], v[42:43]
	v_pk_mul_f32 v[44:45], v[44:45], v[116:117]
	v_pk_fma_f32 v[42:43], s[98:99], v[114:115], v[42:43]
	v_pk_fma_f32 v[116:117], v[120:121], s[68:69], v[44:45] op_sel_hi:[0, 1, 1]
	v_pk_mul_f32 v[44:45], v[46:47], v[118:119]
	v_pk_fma_f32 v[42:43], s[20:21], v[116:117], v[42:43]
	v_pk_fma_f32 v[118:119], v[120:121], s[70:71], v[44:45] op_sel_hi:[0, 1, 1]
	v_pk_fma_f32 v[42:43], s[22:23], v[118:119], v[42:43]
	s_nop 0
	v_add_f32_e32 v38, v42, v43
	v_fma_mix_f32 v30, v1, v30, v38 op_sel:[0,1,0] op_sel_hi:[0,1,0]
	v_fma_mixlo_f16 v30, v30, v34, 0 op_sel:[0,1,0] op_sel_hi:[0,1,0]
	ds_write_b16 v68, v30 offset:21776
	s_waitcnt lgkmcnt(0)
	s_load_dwordx16 s[56:71], s[54:55], 0x980
	s_load_dwordx8 s[88:95], s[54:55], 0x9c0
	s_load_dwordx4 s[96:99], s[54:55], 0x9e0
	s_load_dwordx4 s[20:23], s[54:55], 0x9f0
	v_cvt_f32_f16_e32 v30, v39
	v_pk_mul_f32 v[120:121], v[30:31], v[14:15] op_sel_hi:[0,1]
	v_exp_f32_e32 v120, v120
	v_exp_f32_e32 v121, v121
	v_pk_mul_f32 v[128:129], v[30:31], v[16:17] op_sel_hi:[0,1]
	v_exp_f32_e32 v128, v128
	v_exp_f32_e32 v129, v129
	v_fma_mix_f32 v34, v30, v31, 0 op_sel_hi:[0,1,0]
	v_pk_mul_f32 v[120:121], v[120:121], v[122:123]
	v_pk_fma_f32 v[120:121], v[34:35], s[36:37], v[120:121] op_sel_hi:[0, 1, 1]
	v_pk_fma_f32 v[70:71], s[72:73], v[120:121], 0 op_sel_hi:[1, 1, 0]
	v_pk_mul_f32 v[86:87], v[128:129], v[124:125]
	s_nop 0
	v_pk_fma_f32 v[122:123], v[34:35], s[38:39], v[86:87] op_sel_hi:[0, 1, 1]
	v_pk_mul_f32 v[72:73], v[30:31], v[10:11] op_sel_hi:[0,1]
	v_exp_f32_e32 v72, v72
	v_exp_f32_e32 v73, v73
	v_pk_mul_f32 v[86:87], v[30:31], v[12:13] op_sel_hi:[0,1]
	v_exp_f32_e32 v86, v86
	v_exp_f32_e32 v87, v87
	v_pk_mul_f32 v[72:73], v[72:73], v[126:127]
	v_pk_fma_f32 v[70:71], s[74:75], v[122:123], v[70:71]
	v_pk_fma_f32 v[124:125], v[34:35], s[40:41], v[72:73] op_sel_hi:[0, 1, 1]
	v_pk_mul_f32 v[72:73], v[86:87], v[110:111]
	v_pk_mul_f32 v[74:75], v[30:31], v[8:9] op_sel_hi:[0,1]
	v_pk_fma_f32 v[110:111], v[34:35], s[42:43], v[72:73] op_sel_hi:[0, 1, 1]
	v_pk_mul_f32 v[72:73], v[30:31], v[6:7] op_sel_hi:[0,1]
	v_exp_f32_e32 v72, v72
	v_exp_f32_e32 v73, v73
	v_exp_f32_e32 v74, v74
	v_exp_f32_e32 v75, v75
	v_pk_fma_f32 v[70:71], s[76:77], v[124:125], v[70:71]
	v_pk_mul_f32 v[72:73], v[72:73], v[112:113]
	v_pk_fma_f32 v[70:71], s[78:79], v[110:111], v[70:71]
	v_pk_fma_f32 v[112:113], v[34:35], s[44:45], v[72:73] op_sel_hi:[0, 1, 1]
	v_pk_mul_f32 v[72:73], v[74:75], v[114:115]
	v_pk_mul_f32 v[74:75], v[30:31], v[4:5] op_sel_hi:[0,1]
	v_pk_fma_f32 v[114:115], v[34:35], s[46:47], v[72:73] op_sel_hi:[0, 1, 1]
	v_pk_mul_f32 v[72:73], v[30:31], v[2:3] op_sel_hi:[0,1]
	v_exp_f32_e32 v72, v72
	v_exp_f32_e32 v73, v73
	v_exp_f32_e32 v74, v74
	v_exp_f32_e32 v75, v75
	v_pk_fma_f32 v[70:71], s[80:81], v[112:113], v[70:71]
	v_pk_mul_f32 v[72:73], v[72:73], v[116:117]
	v_pk_fma_f32 v[70:71], s[82:83], v[114:115], v[70:71]
	v_pk_fma_f32 v[116:117], v[34:35], s[48:49], v[72:73] op_sel_hi:[0, 1, 1]
	v_pk_mul_f32 v[72:73], v[74:75], v[118:119]
	v_pk_fma_f32 v[70:71], s[84:85], v[116:117], v[70:71]
	v_pk_fma_f32 v[118:119], v[34:35], s[50:51], v[72:73] op_sel_hi:[0, 1, 1]
	v_pk_fma_f32 v[70:71], s[86:87], v[118:119], v[70:71]
	s_nop 0
	v_add_f32_e32 v30, v70, v71
	v_fma_mix_f32 v30, v1, v31, v30 op_sel_hi:[0,1,0]
	v_fma_mixlo_f16 v30, v30, v35, 0 op_sel_hi:[0,1,0]
	ds_write_b16 v68, v30 offset:22816
	s_waitcnt lgkmcnt(0)
	s_load_dwordx16 s[36:51], s[54:55], 0xa00
	s_load_dwordx16 s[72:87], s[54:55], 0xa40
	v_cvt_f32_f16_sdwa v30, v39 dst_sel:DWORD dst_unused:UNUSED_PAD src0_sel:WORD_1
	v_pk_mul_f32 v[38:39], v[30:31], v[14:15] op_sel_hi:[0,1]
	v_exp_f32_e32 v38, v38
	v_exp_f32_e32 v39, v39
	v_pk_mul_f32 v[126:127], v[30:31], v[16:17] op_sel_hi:[0,1]
	v_exp_f32_e32 v126, v126
	v_exp_f32_e32 v127, v127
	v_fma_mix_f32 v34, v30, v31, 0 op_sel:[0,1,0] op_sel_hi:[0,1,0]
	v_pk_mul_f32 v[38:39], v[38:39], v[120:121]
	v_pk_fma_f32 v[38:39], v[34:35], s[56:57], v[38:39] op_sel_hi:[0, 1, 1]
	v_pk_fma_f32 v[42:43], s[88:89], v[38:39], 0 op_sel_hi:[1, 1, 0]
	v_pk_mul_f32 v[58:59], v[126:127], v[122:123]
	s_nop 0
	v_pk_fma_f32 v[120:121], v[34:35], s[58:59], v[58:59] op_sel_hi:[0, 1, 1]
	v_pk_mul_f32 v[44:45], v[30:31], v[10:11] op_sel_hi:[0,1]
	v_exp_f32_e32 v44, v44
	v_exp_f32_e32 v45, v45
	v_pk_mul_f32 v[58:59], v[30:31], v[12:13] op_sel_hi:[0,1]
	v_exp_f32_e32 v58, v58
	v_exp_f32_e32 v59, v59
	v_pk_mul_f32 v[44:45], v[44:45], v[124:125]
	v_pk_fma_f32 v[42:43], s[90:91], v[120:121], v[42:43]
	v_pk_fma_f32 v[122:123], v[34:35], s[60:61], v[44:45] op_sel_hi:[0, 1, 1]
	v_pk_mul_f32 v[44:45], v[58:59], v[110:111]
	v_pk_mul_f32 v[46:47], v[30:31], v[8:9] op_sel_hi:[0,1]
	v_pk_fma_f32 v[110:111], v[34:35], s[62:63], v[44:45] op_sel_hi:[0, 1, 1]
	v_pk_mul_f32 v[44:45], v[30:31], v[6:7] op_sel_hi:[0,1]
	v_exp_f32_e32 v44, v44
	v_exp_f32_e32 v45, v45
	v_exp_f32_e32 v46, v46
	v_exp_f32_e32 v47, v47
	v_pk_fma_f32 v[42:43], s[92:93], v[122:123], v[42:43]
	v_pk_mul_f32 v[44:45], v[44:45], v[112:113]
	v_pk_fma_f32 v[42:43], s[94:95], v[110:111], v[42:43]
	v_pk_fma_f32 v[112:113], v[34:35], s[64:65], v[44:45] op_sel_hi:[0, 1, 1]
	v_pk_mul_f32 v[44:45], v[46:47], v[114:115]
	v_pk_mul_f32 v[46:47], v[30:31], v[4:5] op_sel_hi:[0,1]
	v_pk_fma_f32 v[114:115], v[34:35], s[66:67], v[44:45] op_sel_hi:[0, 1, 1]
	v_pk_mul_f32 v[44:45], v[30:31], v[2:3] op_sel_hi:[0,1]
	v_exp_f32_e32 v44, v44
	v_exp_f32_e32 v45, v45
	v_exp_f32_e32 v46, v46
	v_exp_f32_e32 v47, v47
	v_pk_fma_f32 v[42:43], s[96:97], v[112:113], v[42:43]
	v_pk_mul_f32 v[44:45], v[44:45], v[116:117]
	v_pk_fma_f32 v[42:43], s[98:99], v[114:115], v[42:43]
	v_pk_fma_f32 v[116:117], v[34:35], s[68:69], v[44:45] op_sel_hi:[0, 1, 1]
	v_pk_mul_f32 v[44:45], v[46:47], v[118:119]
	v_pk_fma_f32 v[42:43], s[20:21], v[116:117], v[42:43]
	v_pk_fma_f32 v[118:119], v[34:35], s[70:71], v[44:45] op_sel_hi:[0, 1, 1]
	v_pk_fma_f32 v[42:43], s[22:23], v[118:119], v[42:43]
	s_nop 0
	v_add_f32_e32 v30, v42, v43
	v_fma_mix_f32 v30, v1, v31, v30 op_sel:[0,1,0] op_sel_hi:[0,1,0]
	v_fma_mixlo_f16 v30, v30, v35, 0 op_sel:[0,1,0] op_sel_hi:[0,1,0]
	ds_write_b16 v68, v30 offset:23856
	s_waitcnt lgkmcnt(0)
	s_load_dwordx16 s[56:71], s[54:55], 0xa80
	s_load_dwordx8 s[88:95], s[54:55], 0xac0
	s_load_dwordx4 s[96:99], s[54:55], 0xae0
	s_load_dwordx4 s[20:23], s[54:55], 0xaf0
	v_cvt_f32_f16_e32 v30, v40
	v_pk_mul_f32 v[124:125], v[30:31], v[14:15] op_sel_hi:[0,1]
	v_exp_f32_e32 v124, v124
	v_exp_f32_e32 v125, v125
	v_pk_mul_f32 v[126:127], v[30:31], v[16:17] op_sel_hi:[0,1]
	v_exp_f32_e32 v126, v126
	v_exp_f32_e32 v127, v127
	v_fma_mix_f32 v34, v30, v32, 0 op_sel_hi:[0,1,0]
	v_pk_mul_f32 v[38:39], v[124:125], v[38:39]
	v_pk_fma_f32 v[38:39], v[34:35], s[36:37], v[38:39] op_sel_hi:[0, 1, 1]
	v_pk_fma_f32 v[70:71], s[72:73], v[38:39], 0 op_sel_hi:[1, 1, 0]
	v_pk_mul_f32 v[86:87], v[126:127], v[120:121]
	s_nop 0
	v_pk_fma_f32 v[120:121], v[34:35], s[38:39], v[86:87] op_sel_hi:[0, 1, 1]
	v_pk_mul_f32 v[72:73], v[30:31], v[10:11] op_sel_hi:[0,1]
	v_exp_f32_e32 v72, v72
	v_exp_f32_e32 v73, v73
	v_pk_mul_f32 v[86:87], v[30:31], v[12:13] op_sel_hi:[0,1]
	v_exp_f32_e32 v86, v86
	v_exp_f32_e32 v87, v87
	v_pk_mul_f32 v[72:73], v[72:73], v[122:123]
	v_pk_fma_f32 v[70:71], s[74:75], v[120:121], v[70:71]
	v_pk_fma_f32 v[122:123], v[34:35], s[40:41], v[72:73] op_sel_hi:[0, 1, 1]
	v_pk_mul_f32 v[72:73], v[86:87], v[110:111]
	v_pk_mul_f32 v[74:75], v[30:31], v[8:9] op_sel_hi:[0,1]
	v_pk_fma_f32 v[110:111], v[34:35], s[42:43], v[72:73] op_sel_hi:[0, 1, 1]
	v_pk_mul_f32 v[72:73], v[30:31], v[6:7] op_sel_hi:[0,1]
	v_exp_f32_e32 v72, v72
	v_exp_f32_e32 v73, v73
	v_exp_f32_e32 v74, v74
	v_exp_f32_e32 v75, v75
	v_pk_fma_f32 v[70:71], s[76:77], v[122:123], v[70:71]
	v_pk_mul_f32 v[72:73], v[72:73], v[112:113]
	v_pk_fma_f32 v[70:71], s[78:79], v[110:111], v[70:71]
	v_pk_fma_f32 v[112:113], v[34:35], s[44:45], v[72:73] op_sel_hi:[0, 1, 1]
	v_pk_mul_f32 v[72:73], v[74:75], v[114:115]
	v_pk_fma_f32 v[70:71], s[80:81], v[112:113], v[70:71]
	v_pk_fma_f32 v[114:115], v[34:35], s[46:47], v[72:73] op_sel_hi:[0, 1, 1]
	v_pk_mul_f32 v[72:73], v[30:31], v[2:3] op_sel_hi:[0,1]
	v_exp_f32_e32 v72, v72
	v_exp_f32_e32 v73, v73
	v_pk_mul_f32 v[30:31], v[30:31], v[4:5] op_sel_hi:[0,1]
	v_exp_f32_e32 v30, v30
	v_exp_f32_e32 v31, v31
	v_pk_mul_f32 v[72:73], v[72:73], v[116:117]
	v_pk_fma_f32 v[70:71], s[82:83], v[114:115], v[70:71]
	v_pk_fma_f32 v[116:117], v[34:35], s[48:49], v[72:73] op_sel_hi:[0, 1, 1]
	v_pk_mul_f32 v[30:31], v[30:31], v[118:119]
	v_pk_fma_f32 v[70:71], s[84:85], v[116:117], v[70:71]
	v_pk_fma_f32 v[30:31], v[34:35], s[50:51], v[30:31] op_sel_hi:[0, 1, 1]
	v_pk_fma_f32 v[34:35], s[86:87], v[30:31], v[70:71]
	s_nop 0
	v_add_f32_e32 v34, v34, v35
	v_fma_mix_f32 v34, v1, v32, v34 op_sel_hi:[0,1,0]
	v_fma_mixlo_f16 v34, v34, v36, 0 op_sel_hi:[0,1,0]
	ds_write_b16 v68, v34 offset:24896
	s_waitcnt lgkmcnt(0)
	s_load_dwordx16 s[36:51], s[54:55], 0xb00
	s_load_dwordx16 s[72:87], s[54:55], 0xb40
	v_cvt_f32_f16_sdwa v34, v40 dst_sel:DWORD dst_unused:UNUSED_PAD src0_sel:WORD_1
	v_pk_mul_f32 v[118:119], v[34:35], v[14:15] op_sel_hi:[0,1]
	v_exp_f32_e32 v118, v118
	v_exp_f32_e32 v119, v119
	v_pk_mul_f32 v[124:125], v[34:35], v[16:17] op_sel_hi:[0,1]
	v_exp_f32_e32 v124, v124
	v_exp_f32_e32 v125, v125
	v_fma_mix_f32 v40, v34, v32, 0 op_sel:[0,1,0] op_sel_hi:[0,1,0]
	v_pk_mul_f32 v[38:39], v[118:119], v[38:39]
	v_pk_fma_f32 v[38:39], v[40:41], s[56:57], v[38:39] op_sel_hi:[0, 1, 1]
	v_pk_fma_f32 v[42:43], s[88:89], v[38:39], 0 op_sel_hi:[1, 1, 0]
	v_pk_mul_f32 v[58:59], v[124:125], v[120:121]
	s_nop 0
	v_pk_fma_f32 v[118:119], v[40:41], s[58:59], v[58:59] op_sel_hi:[0, 1, 1]
	v_pk_mul_f32 v[44:45], v[34:35], v[10:11] op_sel_hi:[0,1]
	v_exp_f32_e32 v44, v44
	v_exp_f32_e32 v45, v45
	v_pk_mul_f32 v[58:59], v[34:35], v[12:13] op_sel_hi:[0,1]
	v_exp_f32_e32 v58, v58
	v_exp_f32_e32 v59, v59
	v_pk_mul_f32 v[44:45], v[44:45], v[122:123]
	v_pk_fma_f32 v[42:43], s[90:91], v[118:119], v[42:43]
	v_pk_fma_f32 v[120:121], v[40:41], s[60:61], v[44:45] op_sel_hi:[0, 1, 1]
	v_pk_mul_f32 v[44:45], v[58:59], v[110:111]
	v_pk_mul_f32 v[46:47], v[34:35], v[8:9] op_sel_hi:[0,1]
	v_pk_fma_f32 v[110:111], v[40:41], s[62:63], v[44:45] op_sel_hi:[0, 1, 1]
	v_pk_mul_f32 v[44:45], v[34:35], v[6:7] op_sel_hi:[0,1]
	v_exp_f32_e32 v44, v44
	v_exp_f32_e32 v45, v45
	v_exp_f32_e32 v46, v46
	v_exp_f32_e32 v47, v47
	v_pk_fma_f32 v[42:43], s[92:93], v[120:121], v[42:43]
	v_pk_mul_f32 v[44:45], v[44:45], v[112:113]
	v_pk_fma_f32 v[42:43], s[94:95], v[110:111], v[42:43]
	v_pk_fma_f32 v[112:113], v[40:41], s[64:65], v[44:45] op_sel_hi:[0, 1, 1]
	v_pk_mul_f32 v[44:45], v[46:47], v[114:115]
	v_pk_fma_f32 v[42:43], s[96:97], v[112:113], v[42:43]
	v_pk_fma_f32 v[114:115], v[40:41], s[66:67], v[44:45] op_sel_hi:[0, 1, 1]
	v_pk_mul_f32 v[44:45], v[34:35], v[2:3] op_sel_hi:[0,1]
	v_exp_f32_e32 v44, v44
	v_exp_f32_e32 v45, v45
	v_pk_mul_f32 v[34:35], v[34:35], v[4:5] op_sel_hi:[0,1]
	v_exp_f32_e32 v34, v34
	v_exp_f32_e32 v35, v35
	v_pk_mul_f32 v[44:45], v[44:45], v[116:117]
	v_pk_fma_f32 v[42:43], s[98:99], v[114:115], v[42:43]
	v_pk_fma_f32 v[116:117], v[40:41], s[68:69], v[44:45] op_sel_hi:[0, 1, 1]
	v_pk_mul_f32 v[30:31], v[34:35], v[30:31]
	v_pk_fma_f32 v[42:43], s[20:21], v[116:117], v[42:43]
	v_pk_fma_f32 v[30:31], v[40:41], s[70:71], v[30:31] op_sel_hi:[0, 1, 1]
	v_pk_fma_f32 v[34:35], s[22:23], v[30:31], v[42:43]
	s_nop 0
	v_add_f32_e32 v34, v34, v35
	v_fma_mix_f32 v32, v1, v32, v34 op_sel:[0,1,0] op_sel_hi:[0,1,0]
	v_fma_mixlo_f16 v32, v32, v36, 0 op_sel:[0,1,0] op_sel_hi:[0,1,0]
	ds_write_b16 v68, v32 offset:25936
	s_waitcnt lgkmcnt(0)
	s_load_dwordx16 s[56:71], s[54:55], 0xb80
	s_load_dwordx8 s[88:95], s[54:55], 0xbc0
	s_load_dwordx4 s[96:99], s[54:55], 0xbe0
	s_load_dwordx4 s[20:23], s[54:55], 0xbf0
	v_cvt_f32_f16_e32 v32, v41
	v_pk_mul_f32 v[122:123], v[32:33], v[14:15] op_sel_hi:[0,1]
	v_exp_f32_e32 v122, v122
	v_exp_f32_e32 v123, v123
	v_pk_mul_f32 v[124:125], v[32:33], v[16:17] op_sel_hi:[0,1]
	v_exp_f32_e32 v124, v124
	v_exp_f32_e32 v125, v125
	v_fma_mix_f32 v34, v32, v33, 0 op_sel_hi:[0,1,0]
	v_pk_mul_f32 v[38:39], v[122:123], v[38:39]
	v_pk_fma_f32 v[38:39], v[34:35], s[36:37], v[38:39] op_sel_hi:[0, 1, 1]
	v_pk_fma_f32 v[70:71], s[72:73], v[38:39], 0 op_sel_hi:[1, 1, 0]
	v_pk_mul_f32 v[86:87], v[124:125], v[118:119]
	s_nop 0
	v_pk_fma_f32 v[118:119], v[34:35], s[38:39], v[86:87] op_sel_hi:[0, 1, 1]
	v_pk_mul_f32 v[72:73], v[32:33], v[10:11] op_sel_hi:[0,1]
	v_exp_f32_e32 v72, v72
	v_exp_f32_e32 v73, v73
	v_pk_mul_f32 v[86:87], v[32:33], v[12:13] op_sel_hi:[0,1]
	v_exp_f32_e32 v86, v86
	v_exp_f32_e32 v87, v87
	v_pk_mul_f32 v[72:73], v[72:73], v[120:121]
	v_pk_fma_f32 v[70:71], s[74:75], v[118:119], v[70:71]
	v_pk_fma_f32 v[120:121], v[34:35], s[40:41], v[72:73] op_sel_hi:[0, 1, 1]
	v_pk_mul_f32 v[72:73], v[86:87], v[110:111]
	v_pk_mul_f32 v[74:75], v[32:33], v[8:9] op_sel_hi:[0,1]
	v_pk_fma_f32 v[110:111], v[34:35], s[42:43], v[72:73] op_sel_hi:[0, 1, 1]
	v_pk_mul_f32 v[72:73], v[32:33], v[6:7] op_sel_hi:[0,1]
	v_exp_f32_e32 v72, v72
	v_exp_f32_e32 v73, v73
	v_exp_f32_e32 v74, v74
	v_exp_f32_e32 v75, v75
	v_pk_fma_f32 v[70:71], s[76:77], v[120:121], v[70:71]
	v_pk_mul_f32 v[72:73], v[72:73], v[112:113]
	v_pk_fma_f32 v[70:71], s[78:79], v[110:111], v[70:71]
	v_pk_fma_f32 v[112:113], v[34:35], s[44:45], v[72:73] op_sel_hi:[0, 1, 1]
	v_pk_mul_f32 v[72:73], v[74:75], v[114:115]
	v_pk_mul_f32 v[74:75], v[32:33], v[4:5] op_sel_hi:[0,1]
	v_pk_fma_f32 v[114:115], v[34:35], s[46:47], v[72:73] op_sel_hi:[0, 1, 1]
	v_pk_mul_f32 v[72:73], v[32:33], v[2:3] op_sel_hi:[0,1]
	v_exp_f32_e32 v72, v72
	v_exp_f32_e32 v73, v73
	v_exp_f32_e32 v74, v74
	v_exp_f32_e32 v75, v75
	v_pk_fma_f32 v[70:71], s[80:81], v[112:113], v[70:71]
	v_pk_mul_f32 v[72:73], v[72:73], v[116:117]
	v_pk_fma_f32 v[70:71], s[82:83], v[114:115], v[70:71]
	v_pk_fma_f32 v[116:117], v[34:35], s[48:49], v[72:73] op_sel_hi:[0, 1, 1]
	v_pk_mul_f32 v[30:31], v[74:75], v[30:31]
	v_pk_fma_f32 v[70:71], s[84:85], v[116:117], v[70:71]
	v_pk_fma_f32 v[30:31], v[34:35], s[50:51], v[30:31] op_sel_hi:[0, 1, 1]
	v_pk_fma_f32 v[34:35], s[86:87], v[30:31], v[70:71]
	s_nop 0
	v_add_f32_e32 v32, v34, v35
	v_fma_mix_f32 v32, v1, v33, v32 op_sel_hi:[0,1,0]
	v_fma_mixlo_f16 v32, v32, v37, 0 op_sel_hi:[0,1,0]
	ds_write_b16 v68, v32 offset:26976
	s_waitcnt lgkmcnt(0)
	s_load_dwordx16 s[36:51], s[54:55], 0xc00
	s_load_dwordx16 s[72:87], s[54:55], 0xc40
	v_cvt_f32_f16_sdwa v32, v41 dst_sel:DWORD dst_unused:UNUSED_PAD src0_sel:WORD_1
	v_pk_mul_f32 v[40:41], v[32:33], v[14:15] op_sel_hi:[0,1]
	v_pk_mul_f32 v[122:123], v[32:33], v[16:17] op_sel_hi:[0,1]
	v_exp_f32_e32 v40, v40
	v_exp_f32_e32 v41, v41
	v_exp_f32_e32 v122, v122
	v_exp_f32_e32 v123, v123
	v_fma_mix_f32 v34, v32, v33, 0 op_sel:[0,1,0] op_sel_hi:[0,1,0]
	v_pk_mul_f32 v[38:39], v[40:41], v[38:39]
	v_pk_mul_f32 v[40:41], v[122:123], v[118:119]
	v_pk_fma_f32 v[118:119], v[34:35], s[58:59], v[40:41] op_sel_hi:[0, 1, 1]
	v_pk_mul_f32 v[40:41], v[32:33], v[10:11] op_sel_hi:[0,1]
	v_pk_fma_f32 v[124:125], v[34:35], s[56:57], v[38:39] op_sel_hi:[0, 1, 1]
	v_exp_f32_e32 v40, v40
	v_exp_f32_e32 v41, v41
	v_pk_mul_f32 v[42:43], v[32:33], v[12:13] op_sel_hi:[0,1]
	v_exp_f32_e32 v42, v42
	v_exp_f32_e32 v43, v43
	v_pk_fma_f32 v[38:39], s[88:89], v[124:125], 0 op_sel_hi:[1, 1, 0]
	v_pk_mul_f32 v[40:41], v[40:41], v[120:121]
	v_pk_fma_f32 v[38:39], s[90:91], v[118:119], v[38:39]
	v_pk_fma_f32 v[120:121], v[34:35], s[60:61], v[40:41] op_sel_hi:[0, 1, 1]
	v_pk_mul_f32 v[40:41], v[42:43], v[110:111]
	v_pk_fma_f32 v[38:39], s[92:93], v[120:121], v[38:39]
	v_pk_fma_f32 v[62:63], v[34:35], s[62:63], v[40:41] op_sel_hi:[0, 1, 1]
	v_pk_mul_f32 v[40:41], v[32:33], v[6:7] op_sel_hi:[0,1]
	v_exp_f32_e32 v40, v40
	v_exp_f32_e32 v41, v41
	v_pk_mul_f32 v[42:43], v[32:33], v[8:9] op_sel_hi:[0,1]
	v_exp_f32_e32 v42, v42
	v_exp_f32_e32 v43, v43
	v_pk_mul_f32 v[40:41], v[40:41], v[112:113]
	v_pk_fma_f32 v[38:39], s[94:95], v[62:63], v[38:39]
	v_pk_fma_f32 v[64:65], v[34:35], s[64:65], v[40:41] op_sel_hi:[0, 1, 1]
	v_pk_mul_f32 v[40:41], v[42:43], v[114:115]
	v_pk_fma_f32 v[38:39], s[96:97], v[64:65], v[38:39]
	v_pk_fma_f32 v[102:103], v[34:35], s[66:67], v[40:41] op_sel_hi:[0, 1, 1]
	v_pk_mul_f32 v[40:41], v[32:33], v[2:3] op_sel_hi:[0,1]
	v_exp_f32_e32 v40, v40
	v_exp_f32_e32 v41, v41
	v_pk_mul_f32 v[42:43], v[32:33], v[4:5] op_sel_hi:[0,1]
	v_exp_f32_e32 v42, v42
	v_exp_f32_e32 v43, v43
	v_pk_mul_f32 v[40:41], v[40:41], v[116:117]
	v_pk_fma_f32 v[38:39], s[98:99], v[102:103], v[38:39]
	v_pk_fma_f32 v[104:105], v[34:35], s[68:69], v[40:41] op_sel_hi:[0, 1, 1]
	v_pk_mul_f32 v[30:31], v[42:43], v[30:31]
	v_pk_fma_f32 v[38:39], s[20:21], v[104:105], v[38:39]
	v_pk_fma_f32 v[106:107], v[34:35], s[70:71], v[30:31] op_sel_hi:[0, 1, 1]
	v_pk_fma_f32 v[30:31], s[22:23], v[106:107], v[38:39]
	s_nop 0
	v_add_f32_e32 v30, v30, v31
	v_fma_mix_f32 v30, v1, v33, v30 op_sel:[0,1,0] op_sel_hi:[0,1,0]
	v_fma_mixlo_f16 v30, v30, v37, 0 op_sel:[0,1,0] op_sel_hi:[0,1,0]
	ds_write_b16 v68, v30 offset:28016
	s_waitcnt lgkmcnt(0)
	s_load_dwordx16 s[56:71], s[54:55], 0xc80
	s_load_dwordx8 s[88:95], s[54:55], 0xcc0
	s_load_dwordx4 s[96:99], s[54:55], 0xce0
	s_load_dwordx4 s[20:23], s[54:55], 0xcf0
	s_waitcnt vmcnt(2)
	v_cvt_f32_f16_e32 v108, v26
	s_waitcnt vmcnt(1)
	v_pk_mul_f32 v[112:113], v[108:109], v[14:15] op_sel_hi:[0,1]
	v_exp_f32_e32 v112, v112
	v_exp_f32_e32 v113, v113
	v_pk_mul_f32 v[114:115], v[108:109], v[16:17] op_sel_hi:[0,1]
	v_exp_f32_e32 v114, v114
	v_exp_f32_e32 v115, v115
	v_fma_mix_f32 v110, v108, v18, 0 op_sel_hi:[0,1,0]
	v_pk_mul_f32 v[112:113], v[112:113], v[124:125]
	v_pk_fma_f32 v[112:113], v[110:111], s[36:37], v[112:113] op_sel_hi:[0, 1, 1]
	v_pk_fma_f32 v[70:71], s[72:73], v[112:113], 0 op_sel_hi:[1, 1, 0]
	v_pk_mul_f32 v[86:87], v[114:115], v[118:119]
	s_nop 0
	v_pk_fma_f32 v[114:115], v[110:111], s[38:39], v[86:87] op_sel_hi:[0, 1, 1]
	v_pk_mul_f32 v[72:73], v[108:109], v[10:11] op_sel_hi:[0,1]
	v_exp_f32_e32 v72, v72
	v_exp_f32_e32 v73, v73
	v_pk_mul_f32 v[86:87], v[108:109], v[12:13] op_sel_hi:[0,1]
	v_exp_f32_e32 v86, v86
	v_exp_f32_e32 v87, v87
	v_pk_mul_f32 v[72:73], v[72:73], v[120:121]
	v_pk_fma_f32 v[70:71], s[74:75], v[114:115], v[70:71]
	v_pk_fma_f32 v[116:117], v[110:111], s[40:41], v[72:73] op_sel_hi:[0, 1, 1]
	v_pk_mul_f32 v[62:63], v[86:87], v[62:63]
	v_pk_fma_f32 v[70:71], s[76:77], v[116:117], v[70:71]
	v_pk_fma_f32 v[118:119], v[110:111], s[42:43], v[62:63] op_sel_hi:[0, 1, 1]
	v_pk_fma_f32 v[62:63], s[78:79], v[118:119], v[70:71]
	v_pk_mul_f32 v[70:71], v[108:109], v[6:7] op_sel_hi:[0,1]
	v_exp_f32_e32 v70, v70
	v_exp_f32_e32 v71, v71
	v_pk_mul_f32 v[72:73], v[108:109], v[8:9] op_sel_hi:[0,1]
	v_exp_f32_e32 v72, v72
	v_exp_f32_e32 v73, v73
	v_pk_mul_f32 v[64:65], v[70:71], v[64:65]
	v_pk_mul_f32 v[70:71], v[108:109], v[4:5] op_sel_hi:[0,1]
	v_pk_fma_f32 v[120:121], v[110:111], s[44:45], v[64:65] op_sel_hi:[0, 1, 1]
	v_pk_mul_f32 v[64:65], v[72:73], v[102:103]
	v_exp_f32_e32 v70, v70
	v_pk_fma_f32 v[102:103], v[110:111], s[46:47], v[64:65] op_sel_hi:[0, 1, 1]
	v_pk_mul_f32 v[64:65], v[108:109], v[2:3] op_sel_hi:[0,1]
	v_exp_f32_e32 v64, v64
	v_exp_f32_e32 v65, v65
	v_exp_f32_e32 v71, v71
	v_pk_fma_f32 v[62:63], s[80:81], v[120:121], v[62:63]
	v_pk_mul_f32 v[64:65], v[64:65], v[104:105]
	v_pk_fma_f32 v[62:63], s[82:83], v[102:103], v[62:63]
	v_pk_fma_f32 v[104:105], v[110:111], s[48:49], v[64:65] op_sel_hi:[0, 1, 1]
	v_pk_mul_f32 v[64:65], v[70:71], v[106:107]
	v_pk_fma_f32 v[62:63], s[84:85], v[104:105], v[62:63]
	v_pk_fma_f32 v[98:99], v[110:111], s[50:51], v[64:65] op_sel_hi:[0, 1, 1]
	v_pk_fma_f32 v[62:63], s[86:87], v[98:99], v[62:63]
	s_nop 0
	v_add_f32_e32 v62, v62, v63
	v_fma_mix_f32 v62, v1, v18, v62 op_sel_hi:[0,1,0]
	s_waitcnt vmcnt(0)
	v_fma_mixlo_f16 v62, v62, v22, 0 op_sel_hi:[0,1,0]
	ds_write_b16 v68, v62 offset:29056
	v_lshrrev_b32_e32 v196, 6, v0
	v_and_b32_e32 v197, 48, v0
	v_lshl_or_b32 v196, v196, 7, v197
	v_and_b32_e32 v197, 15, v0
	v_or_b32_e32 v197, s28, v197
	v_lshl_or_b32 v196, v197, 10, v196
	v_add_u32_e32 v197, 0x4000, v196
	global_load_dwordx4 v[180:183], v196, s[4:5]
	global_load_dwordx4 v[184:187], v196, s[4:5] offset:64
	global_load_dwordx4 v[188:191], v197, s[4:5]
	global_load_dwordx4 v[192:195], v197, s[4:5] offset:64
	v_and_b32_e32 v196, 63, v0
	v_lshlrev_b32_e32 v196, 4, v196
	global_load_dwordx4 v[204:207], v196, s[6:7]
	global_load_dwordx4 v[208:211], v196, s[8:9]
	s_waitcnt lgkmcnt(0)
	s_load_dwordx16 s[36:51], s[54:55], 0xd00
	s_load_dwordx16 s[72:87], s[54:55], 0xd40
	v_cvt_f32_f16_sdwa v26, v26 dst_sel:DWORD dst_unused:UNUSED_PAD src0_sel:WORD_1
	v_pk_mul_f32 v[106:107], v[26:27], v[14:15] op_sel_hi:[0,1]
	v_exp_f32_e32 v106, v106
	v_exp_f32_e32 v107, v107
	v_pk_mul_f32 v[108:109], v[26:27], v[16:17] op_sel_hi:[0,1]
	v_exp_f32_e32 v108, v108
	v_exp_f32_e32 v109, v109
	v_fma_mix_f32 v100, v26, v18, 0 op_sel:[0,1,0] op_sel_hi:[0,1,0]
	v_pk_mul_f32 v[106:107], v[106:107], v[112:113]
	v_pk_fma_f32 v[106:107], v[100:101], s[56:57], v[106:107] op_sel_hi:[0, 1, 1]
	v_pk_fma_f32 v[30:31], s[88:89], v[106:107], 0 op_sel_hi:[1, 1, 0]
	v_pk_mul_f32 v[46:47], v[108:109], v[114:115]
	s_nop 0
	v_pk_fma_f32 v[108:109], v[100:101], s[58:59], v[46:47] op_sel_hi:[0, 1, 1]
	v_pk_mul_f32 v[32:33], v[26:27], v[10:11] op_sel_hi:[0,1]
	v_exp_f32_e32 v32, v32
	v_exp_f32_e32 v33, v33
	v_pk_mul_f32 v[46:47], v[26:27], v[12:13] op_sel_hi:[0,1]
	v_exp_f32_e32 v46, v46
	v_exp_f32_e32 v47, v47
	v_pk_mul_f32 v[32:33], v[32:33], v[116:117]
	v_pk_fma_f32 v[30:31], s[90:91], v[108:109], v[30:31]
	v_pk_fma_f32 v[110:111], v[100:101], s[60:61], v[32:33] op_sel_hi:[0, 1, 1]
	v_pk_mul_f32 v[32:33], v[46:47], v[118:119]
	v_pk_mul_f32 v[34:35], v[26:27], v[8:9] op_sel_hi:[0,1]
	v_pk_fma_f32 v[112:113], v[100:101], s[62:63], v[32:33] op_sel_hi:[0, 1, 1]
	v_pk_mul_f32 v[32:33], v[26:27], v[6:7] op_sel_hi:[0,1]
	v_exp_f32_e32 v32, v32
	v_exp_f32_e32 v33, v33
	v_exp_f32_e32 v34, v34
	v_exp_f32_e32 v35, v35
	v_pk_fma_f32 v[30:31], s[92:93], v[110:111], v[30:31]
	v_pk_mul_f32 v[32:33], v[32:33], v[120:121]
	v_pk_fma_f32 v[30:31], s[94:95], v[112:113], v[30:31]
	v_pk_fma_f32 v[114:115], v[100:101], s[64:65], v[32:33] op_sel_hi:[0, 1, 1]
	v_pk_mul_f32 v[32:33], v[34:35], v[102:103]
	v_pk_mul_f32 v[34:35], v[26:27], v[4:5] op_sel_hi:[0,1]
	v_pk_fma_f32 v[102:103], v[100:101], s[66:67], v[32:33] op_sel_hi:[0, 1, 1]
	v_pk_mul_f32 v[32:33], v[26:27], v[2:3] op_sel_hi:[0,1]
	v_exp_f32_e32 v32, v32
	v_exp_f32_e32 v33, v33
	v_exp_f32_e32 v34, v34
	v_exp_f32_e32 v35, v35
	v_pk_fma_f32 v[30:31], s[96:97], v[114:115], v[30:31]
	v_pk_mul_f32 v[32:33], v[32:33], v[104:105]
	v_pk_fma_f32 v[30:31], s[98:99], v[102:103], v[30:31]
	v_pk_fma_f32 v[104:105], v[100:101], s[68:69], v[32:33] op_sel_hi:[0, 1, 1]
	v_pk_mul_f32 v[32:33], v[34:35], v[98:99]
	v_pk_fma_f32 v[30:31], s[20:21], v[104:105], v[30:31]
	v_pk_fma_f32 v[98:99], v[100:101], s[70:71], v[32:33] op_sel_hi:[0, 1, 1]
	v_pk_fma_f32 v[30:31], s[22:23], v[98:99], v[30:31]
	s_nop 0
	v_add_f32_e32 v26, v30, v31
	v_fma_mix_f32 v18, v1, v18, v26 op_sel:[0,1,0] op_sel_hi:[0,1,0]
	v_fma_mixlo_f16 v18, v18, v22, 0 op_sel:[0,1,0] op_sel_hi:[0,1,0]
	ds_write_b16 v68, v18 offset:30096
	s_waitcnt lgkmcnt(0)
	s_load_dwordx16 s[56:71], s[54:55], 0xd80
	s_load_dwordx8 s[88:95], s[54:55], 0xdc0
	s_load_dwordx4 s[96:99], s[54:55], 0xde0
	s_load_dwordx4 s[20:23], s[54:55], 0xdf0
	v_cvt_f32_f16_e32 v18, v27
	v_pk_mul_f32 v[100:101], v[18:19], v[14:15] op_sel_hi:[0,1]
	v_exp_f32_e32 v100, v100
	v_exp_f32_e32 v101, v101
	v_pk_mul_f32 v[116:117], v[18:19], v[16:17] op_sel_hi:[0,1]
	v_exp_f32_e32 v116, v116
	v_exp_f32_e32 v117, v117
	v_fma_mix_f32 v22, v18, v19, 0 op_sel_hi:[0,1,0]
	v_pk_mul_f32 v[100:101], v[100:101], v[106:107]
	v_pk_fma_f32 v[100:101], v[22:23], s[36:37], v[100:101] op_sel_hi:[0, 1, 1]
	v_pk_fma_f32 v[62:63], s[72:73], v[100:101], 0 op_sel_hi:[1, 1, 0]
	v_pk_mul_f32 v[82:83], v[116:117], v[108:109]
	s_nop 0
	v_pk_fma_f32 v[106:107], v[22:23], s[38:39], v[82:83] op_sel_hi:[0, 1, 1]
	v_pk_mul_f32 v[64:65], v[18:19], v[10:11] op_sel_hi:[0,1]
	v_exp_f32_e32 v64, v64
	v_exp_f32_e32 v65, v65
	v_pk_mul_f32 v[82:83], v[18:19], v[12:13] op_sel_hi:[0,1]
	v_exp_f32_e32 v82, v82
	v_exp_f32_e32 v83, v83
	v_pk_mul_f32 v[64:65], v[64:65], v[110:111]
	v_pk_fma_f32 v[62:63], s[74:75], v[106:107], v[62:63]
	v_pk_fma_f32 v[108:109], v[22:23], s[40:41], v[64:65] op_sel_hi:[0, 1, 1]
	v_pk_mul_f32 v[64:65], v[82:83], v[112:113]
	v_pk_mul_f32 v[70:71], v[18:19], v[8:9] op_sel_hi:[0,1]
	v_pk_fma_f32 v[110:111], v[22:23], s[42:43], v[64:65] op_sel_hi:[0, 1, 1]
	v_pk_mul_f32 v[64:65], v[18:19], v[6:7] op_sel_hi:[0,1]
	v_exp_f32_e32 v64, v64
	v_exp_f32_e32 v65, v65
	v_exp_f32_e32 v70, v70
	v_exp_f32_e32 v71, v71
	v_pk_fma_f32 v[62:63], s[76:77], v[108:109], v[62:63]
	v_pk_mul_f32 v[64:65], v[64:65], v[114:115]
	v_pk_fma_f32 v[62:63], s[78:79], v[110:111], v[62:63]
	v_pk_fma_f32 v[112:113], v[22:23], s[44:45], v[64:65] op_sel_hi:[0, 1, 1]
	v_pk_mul_f32 v[64:65], v[70:71], v[102:103]
	v_pk_mul_f32 v[70:71], v[18:19], v[4:5] op_sel_hi:[0,1]
	v_pk_fma_f32 v[102:103], v[22:23], s[46:47], v[64:65] op_sel_hi:[0, 1, 1]
	v_pk_mul_f32 v[64:65], v[18:19], v[2:3] op_sel_hi:[0,1]
	v_exp_f32_e32 v64, v64
	v_exp_f32_e32 v65, v65
	v_exp_f32_e32 v70, v70
	v_exp_f32_e32 v71, v71
	v_pk_fma_f32 v[62:63], s[80:81], v[112:113], v[62:63]
	v_pk_mul_f32 v[64:65], v[64:65], v[104:105]
	v_pk_fma_f32 v[62:63], s[82:83], v[102:103], v[62:63]
	v_pk_fma_f32 v[104:105], v[22:23], s[48:49], v[64:65] op_sel_hi:[0, 1, 1]
	v_pk_mul_f32 v[64:65], v[70:71], v[98:99]
	v_pk_fma_f32 v[62:63], s[84:85], v[104:105], v[62:63]
	v_pk_fma_f32 v[98:99], v[22:23], s[50:51], v[64:65] op_sel_hi:[0, 1, 1]
	v_pk_fma_f32 v[62:63], s[86:87], v[98:99], v[62:63]
	s_nop 0
	v_add_f32_e32 v18, v62, v63
	v_fma_mix_f32 v18, v1, v19, v18 op_sel_hi:[0,1,0]
	v_fma_mixlo_f16 v18, v18, v23, 0 op_sel_hi:[0,1,0]
	ds_write_b16 v68, v18 offset:31136
	s_waitcnt lgkmcnt(0)
	s_load_dwordx16 s[36:51], s[54:55], 0xe00
	s_load_dwordx16 s[72:87], s[54:55], 0xe40
	v_cvt_f32_f16_sdwa v18, v27 dst_sel:DWORD dst_unused:UNUSED_PAD src0_sel:WORD_1
	v_pk_mul_f32 v[26:27], v[18:19], v[14:15] op_sel_hi:[0,1]
	v_exp_f32_e32 v26, v26
	v_exp_f32_e32 v27, v27
	v_pk_mul_f32 v[114:115], v[18:19], v[16:17] op_sel_hi:[0,1]
	v_exp_f32_e32 v114, v114
	v_exp_f32_e32 v115, v115
	v_fma_mix_f32 v22, v18, v19, 0 op_sel:[0,1,0] op_sel_hi:[0,1,0]
	v_pk_mul_f32 v[26:27], v[26:27], v[100:101]
	v_pk_fma_f32 v[26:27], v[22:23], s[56:57], v[26:27] op_sel_hi:[0, 1, 1]
	v_pk_fma_f32 v[30:31], s[88:89], v[26:27], 0 op_sel_hi:[1, 1, 0]
	v_pk_mul_f32 v[46:47], v[114:115], v[106:107]
	s_nop 0
	v_pk_fma_f32 v[100:101], v[22:23], s[58:59], v[46:47] op_sel_hi:[0, 1, 1]
	v_pk_mul_f32 v[32:33], v[18:19], v[10:11] op_sel_hi:[0,1]
	v_exp_f32_e32 v32, v32
	v_exp_f32_e32 v33, v33
	v_pk_mul_f32 v[46:47], v[18:19], v[12:13] op_sel_hi:[0,1]
	v_exp_f32_e32 v46, v46
	v_exp_f32_e32 v47, v47
	v_pk_mul_f32 v[32:33], v[32:33], v[108:109]
	v_pk_fma_f32 v[30:31], s[90:91], v[100:101], v[30:31]
	v_pk_fma_f32 v[106:107], v[22:23], s[60:61], v[32:33] op_sel_hi:[0, 1, 1]
	v_pk_mul_f32 v[32:33], v[46:47], v[110:111]
	v_pk_mul_f32 v[34:35], v[18:19], v[8:9] op_sel_hi:[0,1]
	v_pk_fma_f32 v[108:109], v[22:23], s[62:63], v[32:33] op_sel_hi:[0, 1, 1]
	v_pk_mul_f32 v[32:33], v[18:19], v[6:7] op_sel_hi:[0,1]
	v_exp_f32_e32 v32, v32
	v_exp_f32_e32 v33, v33
	v_exp_f32_e32 v34, v34
	v_exp_f32_e32 v35, v35
	v_pk_fma_f32 v[30:31], s[92:93], v[106:107], v[30:31]
	v_pk_mul_f32 v[32:33], v[32:33], v[112:113]
	v_pk_fma_f32 v[30:31], s[94:95], v[108:109], v[30:31]
	v_pk_fma_f32 v[110:111], v[22:23], s[64:65], v[32:33] op_sel_hi:[0, 1, 1]
	v_pk_mul_f32 v[32:33], v[34:35], v[102:103]
	v_pk_mul_f32 v[34:35], v[18:19], v[4:5] op_sel_hi:[0,1]
	v_pk_fma_f32 v[102:103], v[22:23], s[66:67], v[32:33] op_sel_hi:[0, 1, 1]
	v_pk_mul_f32 v[32:33], v[18:19], v[2:3] op_sel_hi:[0,1]
	v_exp_f32_e32 v32, v32
	v_exp_f32_e32 v33, v33
	v_exp_f32_e32 v34, v34
	v_exp_f32_e32 v35, v35
	v_pk_fma_f32 v[30:31], s[96:97], v[110:111], v[30:31]
	v_pk_mul_f32 v[32:33], v[32:33], v[104:105]
	v_pk_fma_f32 v[30:31], s[98:99], v[102:103], v[30:31]
	v_pk_fma_f32 v[104:105], v[22:23], s[68:69], v[32:33] op_sel_hi:[0, 1, 1]
	v_pk_mul_f32 v[32:33], v[34:35], v[98:99]
	v_pk_fma_f32 v[30:31], s[20:21], v[104:105], v[30:31]
	v_pk_fma_f32 v[98:99], v[22:23], s[70:71], v[32:33] op_sel_hi:[0, 1, 1]
	v_pk_fma_f32 v[30:31], s[22:23], v[98:99], v[30:31]
	s_nop 0
	v_add_f32_e32 v18, v30, v31
	v_fma_mix_f32 v18, v1, v19, v18 op_sel:[0,1,0] op_sel_hi:[0,1,0]
	v_fma_mixlo_f16 v18, v18, v23, 0 op_sel:[0,1,0] op_sel_hi:[0,1,0]
	ds_write_b16 v68, v18 offset:32176
	s_waitcnt lgkmcnt(0)
	s_load_dwordx16 s[56:71], s[54:55], 0xe80
	s_load_dwordx8 s[88:95], s[54:55], 0xec0
	s_load_dwordx4 s[96:99], s[54:55], 0xee0
	s_load_dwordx4 s[20:23], s[54:55], 0xef0
	v_cvt_f32_f16_e32 v18, v28
	v_pk_mul_f32 v[112:113], v[18:19], v[14:15] op_sel_hi:[0,1]
	v_exp_f32_e32 v112, v112
	v_exp_f32_e32 v113, v113
	v_pk_mul_f32 v[114:115], v[18:19], v[16:17] op_sel_hi:[0,1]
	v_exp_f32_e32 v114, v114
	v_exp_f32_e32 v115, v115
	v_fma_mix_f32 v22, v18, v20, 0 op_sel_hi:[0,1,0]
	v_pk_mul_f32 v[26:27], v[112:113], v[26:27]
	v_pk_fma_f32 v[26:27], v[22:23], s[36:37], v[26:27] op_sel_hi:[0, 1, 1]
	v_pk_fma_f32 v[62:63], s[72:73], v[26:27], 0 op_sel_hi:[1, 1, 0]
	v_pk_mul_f32 v[82:83], v[114:115], v[100:101]
	s_nop 0
	v_pk_fma_f32 v[100:101], v[22:23], s[38:39], v[82:83] op_sel_hi:[0, 1, 1]
	v_pk_mul_f32 v[64:65], v[18:19], v[10:11] op_sel_hi:[0,1]
	v_exp_f32_e32 v64, v64
	v_exp_f32_e32 v65, v65
	v_pk_mul_f32 v[82:83], v[18:19], v[12:13] op_sel_hi:[0,1]
	v_exp_f32_e32 v82, v82
	v_exp_f32_e32 v83, v83
	v_pk_mul_f32 v[64:65], v[64:65], v[106:107]
	v_pk_fma_f32 v[62:63], s[74:75], v[100:101], v[62:63]
	v_pk_fma_f32 v[106:107], v[22:23], s[40:41], v[64:65] op_sel_hi:[0, 1, 1]
	v_pk_mul_f32 v[64:65], v[82:83], v[108:109]
	v_pk_mul_f32 v[70:71], v[18:19], v[8:9] op_sel_hi:[0,1]
	v_pk_fma_f32 v[108:109], v[22:23], s[42:43], v[64:65] op_sel_hi:[0, 1, 1]
	v_pk_mul_f32 v[64:65], v[18:19], v[6:7] op_sel_hi:[0,1]
	v_exp_f32_e32 v64, v64
	v_exp_f32_e32 v65, v65
	v_exp_f32_e32 v70, v70
	v_exp_f32_e32 v71, v71
	v_pk_fma_f32 v[62:63], s[76:77], v[106:107], v[62:63]
	v_pk_mul_f32 v[64:65], v[64:65], v[110:111]
	v_pk_fma_f32 v[62:63], s[78:79], v[108:109], v[62:63]
	v_pk_fma_f32 v[110:111], v[22:23], s[44:45], v[64:65] op_sel_hi:[0, 1, 1]
	v_pk_mul_f32 v[64:65], v[70:71], v[102:103]
	v_pk_fma_f32 v[62:63], s[80:81], v[110:111], v[62:63]
	v_pk_fma_f32 v[102:103], v[22:23], s[46:47], v[64:65] op_sel_hi:[0, 1, 1]
	v_pk_mul_f32 v[64:65], v[18:19], v[2:3] op_sel_hi:[0,1]
	v_exp_f32_e32 v64, v64
	v_exp_f32_e32 v65, v65
	v_pk_mul_f32 v[18:19], v[18:19], v[4:5] op_sel_hi:[0,1]
	v_exp_f32_e32 v18, v18
	v_exp_f32_e32 v19, v19
	v_pk_mul_f32 v[64:65], v[64:65], v[104:105]
	v_pk_fma_f32 v[62:63], s[82:83], v[102:103], v[62:63]
	v_pk_fma_f32 v[104:105], v[22:23], s[48:49], v[64:65] op_sel_hi:[0, 1, 1]
	v_pk_mul_f32 v[18:19], v[18:19], v[98:99]
	v_pk_fma_f32 v[62:63], s[84:85], v[104:105], v[62:63]
	v_pk_fma_f32 v[18:19], v[22:23], s[50:51], v[18:19] op_sel_hi:[0, 1, 1]
	v_pk_fma_f32 v[22:23], s[86:87], v[18:19], v[62:63]
	s_nop 0
	v_add_f32_e32 v22, v22, v23
	v_fma_mix_f32 v22, v1, v20, v22 op_sel_hi:[0,1,0]
	v_fma_mixlo_f16 v22, v22, v24, 0 op_sel_hi:[0,1,0]
	ds_write_b16 v68, v22 offset:33216
	s_waitcnt lgkmcnt(0)
	s_load_dwordx16 s[36:51], s[54:55], 0xf00
	s_load_dwordx16 s[72:87], s[54:55], 0xf40
	v_cvt_f32_f16_sdwa v22, v28 dst_sel:DWORD dst_unused:UNUSED_PAD src0_sel:WORD_1
	v_pk_mul_f32 v[98:99], v[22:23], v[14:15] op_sel_hi:[0,1]
	v_exp_f32_e32 v98, v98
	v_exp_f32_e32 v99, v99
	v_pk_mul_f32 v[112:113], v[22:23], v[16:17] op_sel_hi:[0,1]
	v_exp_f32_e32 v112, v112
	v_exp_f32_e32 v113, v113
	v_fma_mix_f32 v28, v22, v20, 0 op_sel:[0,1,0] op_sel_hi:[0,1,0]
	v_pk_mul_f32 v[26:27], v[98:99], v[26:27]
	v_pk_fma_f32 v[26:27], v[28:29], s[56:57], v[26:27] op_sel_hi:[0, 1, 1]
	v_pk_fma_f32 v[30:31], s[88:89], v[26:27], 0 op_sel_hi:[1, 1, 0]
	v_pk_mul_f32 v[46:47], v[112:113], v[100:101]
	s_nop 0
	v_pk_fma_f32 v[98:99], v[28:29], s[58:59], v[46:47] op_sel_hi:[0, 1, 1]
	v_pk_mul_f32 v[32:33], v[22:23], v[10:11] op_sel_hi:[0,1]
	v_exp_f32_e32 v32, v32
	v_exp_f32_e32 v33, v33
	v_pk_mul_f32 v[46:47], v[22:23], v[12:13] op_sel_hi:[0,1]
	v_exp_f32_e32 v46, v46
	v_exp_f32_e32 v47, v47
	v_pk_mul_f32 v[32:33], v[32:33], v[106:107]
	v_pk_fma_f32 v[30:31], s[90:91], v[98:99], v[30:31]
	v_pk_fma_f32 v[100:101], v[28:29], s[60:61], v[32:33] op_sel_hi:[0, 1, 1]
	v_pk_mul_f32 v[32:33], v[46:47], v[108:109]
	v_pk_mul_f32 v[34:35], v[22:23], v[8:9] op_sel_hi:[0,1]
	v_pk_fma_f32 v[106:107], v[28:29], s[62:63], v[32:33] op_sel_hi:[0, 1, 1]
	v_pk_mul_f32 v[32:33], v[22:23], v[6:7] op_sel_hi:[0,1]
	v_exp_f32_e32 v32, v32
	v_exp_f32_e32 v33, v33
	v_exp_f32_e32 v34, v34
	v_exp_f32_e32 v35, v35
	v_pk_fma_f32 v[30:31], s[92:93], v[100:101], v[30:31]
	v_pk_mul_f32 v[32:33], v[32:33], v[110:111]
	v_pk_fma_f32 v[30:31], s[94:95], v[106:107], v[30:31]
	v_pk_fma_f32 v[108:109], v[28:29], s[64:65], v[32:33] op_sel_hi:[0, 1, 1]
	v_pk_mul_f32 v[32:33], v[34:35], v[102:103]
	v_pk_fma_f32 v[30:31], s[96:97], v[108:109], v[30:31]
	v_pk_fma_f32 v[102:103], v[28:29], s[66:67], v[32:33] op_sel_hi:[0, 1, 1]
	v_pk_mul_f32 v[32:33], v[22:23], v[2:3] op_sel_hi:[0,1]
	v_exp_f32_e32 v32, v32
	v_exp_f32_e32 v33, v33
	v_pk_mul_f32 v[22:23], v[22:23], v[4:5] op_sel_hi:[0,1]
	v_exp_f32_e32 v22, v22
	v_exp_f32_e32 v23, v23
	v_pk_mul_f32 v[32:33], v[32:33], v[104:105]
	v_pk_fma_f32 v[30:31], s[98:99], v[102:103], v[30:31]
	v_pk_fma_f32 v[104:105], v[28:29], s[68:69], v[32:33] op_sel_hi:[0, 1, 1]
	v_pk_mul_f32 v[18:19], v[22:23], v[18:19]
	v_pk_fma_f32 v[30:31], s[20:21], v[104:105], v[30:31]
	v_pk_fma_f32 v[18:19], v[28:29], s[70:71], v[18:19] op_sel_hi:[0, 1, 1]
	v_pk_fma_f32 v[22:23], s[22:23], v[18:19], v[30:31]
	s_nop 0
	v_add_f32_e32 v22, v22, v23
	v_fma_mix_f32 v20, v1, v20, v22 op_sel:[0,1,0] op_sel_hi:[0,1,0]
	v_fma_mixlo_f16 v20, v20, v24, 0 op_sel:[0,1,0] op_sel_hi:[0,1,0]
	ds_write_b16 v68, v20 offset:34256
	s_waitcnt lgkmcnt(0)
	s_load_dwordx16 s[56:71], s[54:55], 0xf80
	s_load_dwordx8 s[88:95], s[54:55], 0xfc0
	s_load_dwordx4 s[96:99], s[54:55], 0xfe0
	s_load_dwordx4 s[20:23], s[54:55], 0xff0
	v_cvt_f32_f16_e32 v20, v29
	v_pk_mul_f32 v[110:111], v[20:21], v[14:15] op_sel_hi:[0,1]
	v_exp_f32_e32 v110, v110
	v_exp_f32_e32 v111, v111
	v_pk_mul_f32 v[112:113], v[20:21], v[16:17] op_sel_hi:[0,1]
	v_exp_f32_e32 v112, v112
	v_exp_f32_e32 v113, v113
	v_fma_mix_f32 v22, v20, v21, 0 op_sel_hi:[0,1,0]
	v_pk_mul_f32 v[26:27], v[110:111], v[26:27]
	v_pk_fma_f32 v[26:27], v[22:23], s[36:37], v[26:27] op_sel_hi:[0, 1, 1]
	v_pk_fma_f32 v[62:63], s[72:73], v[26:27], 0 op_sel_hi:[1, 1, 0]
	v_pk_mul_f32 v[82:83], v[112:113], v[98:99]
	s_nop 0
	v_pk_fma_f32 v[64:65], v[22:23], s[38:39], v[82:83] op_sel_hi:[0, 1, 1]
	v_pk_mul_f32 v[82:83], v[20:21], v[10:11] op_sel_hi:[0,1]
	v_pk_fma_f32 v[62:63], s[74:75], v[64:65], v[62:63]
	v_exp_f32_e32 v82, v82
	v_exp_f32_e32 v83, v83
	v_pk_mul_f32 v[84:85], v[20:21], v[12:13] op_sel_hi:[0,1]
	v_exp_f32_e32 v84, v84
	v_exp_f32_e32 v85, v85
	v_pk_mul_f32 v[82:83], v[82:83], v[100:101]
	s_nop 0
	v_pk_fma_f32 v[70:71], v[22:23], s[40:41], v[82:83] op_sel_hi:[0, 1, 1]
	v_pk_mul_f32 v[82:83], v[84:85], v[106:107]
	v_pk_mul_f32 v[84:85], v[20:21], v[8:9] op_sel_hi:[0,1]
	v_pk_fma_f32 v[72:73], v[22:23], s[42:43], v[82:83] op_sel_hi:[0, 1, 1]
	v_pk_mul_f32 v[82:83], v[20:21], v[6:7] op_sel_hi:[0,1]
	v_exp_f32_e32 v82, v82
	v_exp_f32_e32 v83, v83
	v_exp_f32_e32 v84, v84
	v_exp_f32_e32 v85, v85
	v_pk_fma_f32 v[62:63], s[76:77], v[70:71], v[62:63]
	v_pk_mul_f32 v[82:83], v[82:83], v[108:109]
	v_pk_fma_f32 v[62:63], s[78:79], v[72:73], v[62:63]
	v_pk_fma_f32 v[74:75], v[22:23], s[44:45], v[82:83] op_sel_hi:[0, 1, 1]
	v_pk_mul_f32 v[82:83], v[84:85], v[102:103]
	v_pk_mul_f32 v[84:85], v[20:21], v[4:5] op_sel_hi:[0,1]
	v_pk_fma_f32 v[76:77], v[22:23], s[46:47], v[82:83] op_sel_hi:[0, 1, 1]
	v_pk_mul_f32 v[82:83], v[20:21], v[2:3] op_sel_hi:[0,1]
	v_exp_f32_e32 v82, v82
	v_exp_f32_e32 v83, v83
	v_exp_f32_e32 v84, v84
	v_exp_f32_e32 v85, v85
	v_pk_fma_f32 v[62:63], s[80:81], v[74:75], v[62:63]
	v_pk_mul_f32 v[82:83], v[82:83], v[104:105]
	v_pk_fma_f32 v[62:63], s[82:83], v[76:77], v[62:63]
	v_pk_fma_f32 v[78:79], v[22:23], s[48:49], v[82:83] op_sel_hi:[0, 1, 1]
	v_pk_mul_f32 v[18:19], v[84:85], v[18:19]
	v_pk_fma_f32 v[62:63], s[84:85], v[78:79], v[62:63]
	v_pk_fma_f32 v[18:19], v[22:23], s[50:51], v[18:19] op_sel_hi:[0, 1, 1]
	v_pk_fma_f32 v[22:23], s[86:87], v[18:19], v[62:63]
	s_nop 0
	v_add_f32_e32 v20, v22, v23
	v_fma_mix_f32 v20, v1, v21, v20 op_sel_hi:[0,1,0]
	v_fma_mixlo_f16 v20, v20, v25, 0 op_sel_hi:[0,1,0]
	ds_write_b16 v68, v20 offset:35296
	s_waitcnt lgkmcnt(0)
	v_cvt_f32_f16_sdwa v20, v29 dst_sel:DWORD dst_unused:UNUSED_PAD src0_sel:WORD_1
	v_pk_mul_f32 v[14:15], v[20:21], v[14:15] op_sel_hi:[0,1]
	v_exp_f32_e32 v14, v14
	v_exp_f32_e32 v15, v15
	v_pk_mul_f32 v[16:17], v[20:21], v[16:17] op_sel_hi:[0,1]
	v_exp_f32_e32 v16, v16
	v_exp_f32_e32 v17, v17
	v_pk_mul_f32 v[10:11], v[20:21], v[10:11] op_sel_hi:[0,1]
	v_exp_f32_e32 v10, v10
	v_exp_f32_e32 v11, v11
	v_pk_mul_f32 v[12:13], v[20:21], v[12:13] op_sel_hi:[0,1]
	v_exp_f32_e32 v12, v12
	v_exp_f32_e32 v13, v13
	v_pk_mul_f32 v[6:7], v[20:21], v[6:7] op_sel_hi:[0,1]
	v_fma_mix_f32 v22, v20, v21, 0 op_sel:[0,1,0] op_sel_hi:[0,1,0]
	v_pk_mul_f32 v[14:15], v[14:15], v[26:27]
	v_exp_f32_e32 v6, v6
	v_exp_f32_e32 v7, v7
	v_pk_mul_f32 v[8:9], v[20:21], v[8:9] op_sel_hi:[0,1]
	v_pk_fma_f32 v[14:15], v[22:23], s[56:57], v[14:15] op_sel_hi:[0, 1, 1]
	v_pk_mul_f32 v[16:17], v[16:17], v[64:65]
	v_exp_f32_e32 v8, v8
	v_exp_f32_e32 v9, v9
	v_pk_mul_f32 v[2:3], v[20:21], v[2:3] op_sel_hi:[0,1]
	v_pk_fma_f32 v[14:15], s[88:89], v[14:15], 0 op_sel_hi:[1, 1, 0]
	v_pk_fma_f32 v[16:17], v[22:23], s[58:59], v[16:17] op_sel_hi:[0, 1, 1]
	v_pk_mul_f32 v[10:11], v[10:11], v[70:71]
	v_exp_f32_e32 v2, v2
	v_exp_f32_e32 v3, v3
	v_pk_mul_f32 v[4:5], v[20:21], v[4:5] op_sel_hi:[0,1]
	v_pk_fma_f32 v[14:15], s[90:91], v[16:17], v[14:15]
	v_pk_fma_f32 v[10:11], v[22:23], s[60:61], v[10:11] op_sel_hi:[0, 1, 1]
	v_pk_mul_f32 v[12:13], v[12:13], v[72:73]
	v_exp_f32_e32 v4, v4
	v_exp_f32_e32 v5, v5
	v_pk_fma_f32 v[10:11], s[92:93], v[10:11], v[14:15]
	v_pk_fma_f32 v[12:13], v[22:23], s[62:63], v[12:13] op_sel_hi:[0, 1, 1]
	v_pk_mul_f32 v[6:7], v[6:7], v[74:75]
	v_pk_fma_f32 v[10:11], s[94:95], v[12:13], v[10:11]
	v_pk_fma_f32 v[6:7], v[22:23], s[64:65], v[6:7] op_sel_hi:[0, 1, 1]
	v_pk_mul_f32 v[8:9], v[8:9], v[76:77]
	v_pk_fma_f32 v[6:7], s[96:97], v[6:7], v[10:11]
	v_pk_fma_f32 v[8:9], v[22:23], s[66:67], v[8:9] op_sel_hi:[0, 1, 1]
	v_pk_mul_f32 v[2:3], v[2:3], v[78:79]
	v_pk_fma_f32 v[6:7], s[98:99], v[8:9], v[6:7]
	v_pk_fma_f32 v[2:3], v[22:23], s[68:69], v[2:3] op_sel_hi:[0, 1, 1]
	v_pk_mul_f32 v[4:5], v[4:5], v[18:19]
	v_pk_fma_f32 v[2:3], s[20:21], v[2:3], v[6:7]
	v_pk_fma_f32 v[4:5], v[22:23], s[70:71], v[4:5] op_sel_hi:[0, 1, 1]
	v_pk_fma_f32 v[2:3], s[22:23], v[4:5], v[2:3]
	s_nop 0
	v_add_f32_e32 v2, v2, v3
	v_fma_mix_f32 v1, v1, v21, v2 op_sel:[0,1,0] op_sel_hi:[0,1,0]
	v_fma_mixlo_f16 v1, v1, v25, 0 op_sel:[0,1,0] op_sel_hi:[0,1,0]
	ds_write_b16 v68, v1 offset:36336
	v_lshlrev_b32_e32 v1, 9, v0
	v_and_b32_e32 v2, 0x38000, v1
	v_mov_b32_e32 v3, v67
	v_and_b32_e32 v1, 63, v0
	s_bfe_u32 s14, s2, 0x40003
	v_lshl_add_u64 v[2:3], s[18:19], 0, v[2:3]
	v_lshlrev_b32_e32 v58, 4, v1
	v_mov_b32_e32 v59, v67
	s_lshl_b32 s13, s14, 6
	v_lshl_add_u64 v[20:21], v[2:3], 0, v[58:59]
	s_lshl_b32 s26, s14, 10
	s_add_i32 s12, s13, 64
	v_lshl_add_u64 v[2:3], v[20:21], 0, s[26:27]
	s_and_b32 s15, s12, 0x3c0
	v_add_co_u32_e32 v4, vcc, s52, v2
	s_lshl_b32 s26, s15, 4
	s_lshl_b32 s12, s12, 4
	v_addc_co_u32_e32 v5, vcc, 0, v3, vcc
	global_load_dwordx4 v[28:31], v[2:3], off
	global_load_dwordx4 v[32:35], v[4:5], off
	v_lshl_add_u64 v[2:3], v[20:21], 0, s[26:27]
	s_or_b32 s26, s12, 0x4000
	s_add_i32 s12, s13, 0x80
	s_and_b32 s15, s12, 0x3c0
	v_lshl_add_u64 v[4:5], v[20:21], 0, s[26:27]
	s_lshl_b32 s26, s15, 4
	s_lshl_b32 s12, s12, 4
	global_load_dwordx4 v[36:39], v[2:3], off
	global_load_dwordx4 v[40:43], v[4:5], off
	v_lshl_add_u64 v[2:3], v[20:21], 0, s[26:27]
	s_or_b32 s26, s12, 0x4000
	s_add_i32 s12, s13, 0xc0
	s_and_b32 s15, s12, 0x3c0
	v_lshl_add_u64 v[4:5], v[20:21], 0, s[26:27]
	s_lshl_b32 s26, s15, 4
	s_lshl_b32 s12, s12, 4
	global_load_dwordx4 v[44:47], v[2:3], off
	global_load_dwordx4 v[48:51], v[4:5], off
	v_lshl_add_u64 v[2:3], v[20:21], 0, s[26:27]
	s_or_b32 s26, s12, 0x4000
	s_add_i32 s12, s13, 0x100
	s_and_b32 s15, s12, 0x3c0
	v_lshl_add_u64 v[4:5], v[20:21], 0, s[26:27]
	s_lshl_b32 s26, s15, 4
	s_lshl_b32 s12, s12, 4
	global_load_dwordx4 v[52:55], v[2:3], off
	global_load_dwordx4 v[60:63], v[4:5], off
	v_lshl_add_u64 v[2:3], v[20:21], 0, s[26:27]
	s_or_b32 s26, s12, 0x4000
	s_add_i32 s12, s13, 0x140
	s_and_b32 s15, s12, 0x3c0
	v_lshl_add_u64 v[4:5], v[20:21], 0, s[26:27]
	s_lshl_b32 s26, s15, 4
	s_lshl_b32 s12, s12, 4
	global_load_dwordx4 v[68:71], v[2:3], off
	global_load_dwordx4 v[72:75], v[4:5], off
	v_lshl_add_u64 v[2:3], v[20:21], 0, s[26:27]
	s_or_b32 s26, s12, 0x4000
	s_add_i32 s12, s13, 0x180
	s_and_b32 s15, s12, 0x3c0
	v_lshl_add_u64 v[4:5], v[20:21], 0, s[26:27]
	s_lshl_b32 s26, s15, 4
	s_lshl_b32 s12, s12, 4
	global_load_dwordx4 v[76:79], v[2:3], off
	global_load_dwordx4 v[82:85], v[4:5], off
	v_lshl_add_u64 v[2:3], v[20:21], 0, s[26:27]
	s_or_b32 s26, s12, 0x4000
	s_add_i32 s12, s13, 0x1c0
	s_and_b32 s15, s12, 0x3c0
	v_lshl_add_u64 v[4:5], v[20:21], 0, s[26:27]
	s_lshl_b32 s26, s15, 4
	s_lshl_b32 s12, s12, 4
	v_lshl_add_u64 v[18:19], v[20:21], 0, s[26:27]
	s_or_b32 s26, s12, 0x4000
	s_xor_b32 s15, s13, 0x200
	v_lshl_add_u64 v[22:23], v[20:21], 0, s[26:27]
	s_lshl_b32 s26, s15, 4
	global_load_dwordx4 v[14:17], v[2:3], off
	global_load_dwordx4 v[10:13], v[4:5], off
	global_load_dwordx4 v[6:9], v[18:19], off
	s_nop 0
	global_load_dwordx4 v[2:5], v[22:23], off
	v_lshl_add_u64 v[18:19], v[20:21], 0, s[26:27]
	v_add_co_u32_e32 v22, vcc, s52, v18
	s_waitcnt lgkmcnt(0)
	s_barrier
	v_addc_co_u32_e32 v23, vcc, 0, v19, vcc
	global_load_dwordx4 v[86:89], v[18:19], off
	global_load_dwordx4 v[90:93], v[22:23], off
	v_lshrrev_b32_e32 v118, 6, v0
	v_lshlrev_b32_e32 v22, 7, v118
	v_mov_b32_e32 v23, v67
	v_and_b32_e32 v81, 15, v0
	v_lshl_add_u64 v[24:25], s[4:5], 0, v[22:23]
	v_and_b32_e32 v18, 48, v0
	v_mov_b32_e32 v19, v67
	s_movk_i32 s12, 0x410
	v_lshl_add_u64 v[56:57], v[24:25], 0, v[18:19]
	v_mad_u32_u24 v19, v81, s12, v18
	v_add_u32_e32 v23, s13, v19
	ds_read_b128 v[94:97], v23 offset:4096
	ds_read_b128 v[98:101], v23 offset:20736
	v_or_b32_e32 v26, s28, v81
	v_mov_b32_e32 v27, v67
	v_lshlrev_b64 v[24:25], 10, v[26:27]
	v_or_b32_e32 v26, 16, v26
	v_lshlrev_b64 v[26:27], 10, v[26:27]
	v_lshrrev_b32_e32 v23, 1, v0
	v_lshl_add_u64 v[24:25], v[56:57], 0, v[24:25]
	v_lshl_add_u64 v[26:27], v[56:57], 0, v[26:27]
	v_and_b32_e32 v80, 24, v23
	s_lshl_b32 s14, s14, 5
	s_setprio 1
	s_waitcnt vmcnt(17) lgkmcnt(1)
	v_mfma_f32_16x16x32_f16 v[102:105], v[28:31], v[94:97], 0
	s_waitcnt lgkmcnt(0)
	v_mfma_f32_16x16x32_f16 v[28:31], v[28:31], v[98:101], 0
	s_waitcnt vmcnt(16)
	v_mfma_f32_16x16x32_f16 v[94:97], v[32:35], v[94:97], 0
	v_mfma_f32_16x16x32_f16 v[32:35], v[32:35], v[98:101], 0
	s_setprio 0
	s_add_i32 s16, s13, 0x240
	s_and_b32 s17, s16, 0x3c0
	s_lshl_b32 s26, s17, 4
	s_lshl_b32 s16, s16, 4
	v_lshl_add_u64 v[56:57], v[20:21], 0, s[26:27]
	s_or_b32 s26, s16, 0x4000
	v_lshl_add_u64 v[64:65], v[20:21], 0, s[26:27]
	global_load_dwordx4 v[98:101], v[56:57], off
	global_load_dwordx4 v[106:109], v[64:65], off
	s_add_i32 s16, s14, 32
	s_and_b32 s16, s16, 0x1e0
	v_lshl_add_u32 v23, s16, 1, v19
	ds_read_b128 v[110:113], v23 offset:4096
	ds_read_b128 v[114:117], v23 offset:20736
	s_setprio 1
	s_waitcnt vmcnt(17) lgkmcnt(1)
	v_mfma_f32_16x16x32_f16 v[102:105], v[36:39], v[110:113], v[102:105]
	s_waitcnt lgkmcnt(0)
	v_mfma_f32_16x16x32_f16 v[28:31], v[36:39], v[114:117], v[28:31]
	s_waitcnt vmcnt(16)
	v_mfma_f32_16x16x32_f16 v[36:39], v[40:43], v[110:113], v[94:97]
	v_mfma_f32_16x16x32_f16 v[32:35], v[40:43], v[114:117], v[32:35]
	s_setprio 0
	s_add_i32 s16, s13, 0x280
	s_and_b32 s17, s16, 0x3c0
	s_lshl_b32 s26, s17, 4
	s_lshl_b32 s16, s16, 4
	v_lshl_add_u64 v[56:57], v[20:21], 0, s[26:27]
	s_or_b32 s26, s16, 0x4000
	v_lshl_add_u64 v[64:65], v[20:21], 0, s[26:27]
	global_load_dwordx4 v[40:43], v[56:57], off
	global_load_dwordx4 v[94:97], v[64:65], off
	s_add_i32 s16, s14, 64
	s_and_b32 s16, s16, 0x1e0
	v_lshl_add_u32 v23, s16, 1, v19
	ds_read_b128 v[110:113], v23 offset:4096
	ds_read_b128 v[114:117], v23 offset:20736
	s_setprio 1
	s_waitcnt vmcnt(17) lgkmcnt(1)
	v_mfma_f32_16x16x32_f16 v[102:105], v[44:47], v[110:113], v[102:105]
	s_waitcnt lgkmcnt(0)
	v_mfma_f32_16x16x32_f16 v[28:31], v[44:47], v[114:117], v[28:31]
	s_waitcnt vmcnt(16)
	v_mfma_f32_16x16x32_f16 v[36:39], v[48:51], v[110:113], v[36:39]
	v_mfma_f32_16x16x32_f16 v[32:35], v[48:51], v[114:117], v[32:35]
	s_setprio 0
	s_add_i32 s16, s13, 0x2c0
	s_and_b32 s17, s16, 0x3c0
	s_lshl_b32 s26, s17, 4
	s_lshl_b32 s16, s16, 4
	v_lshl_add_u64 v[56:57], v[20:21], 0, s[26:27]
	s_or_b32 s26, s16, 0x4000
	v_lshl_add_u64 v[64:65], v[20:21], 0, s[26:27]
	global_load_dwordx4 v[44:47], v[56:57], off
	global_load_dwordx4 v[48:51], v[64:65], off
	s_add_i32 s16, s14, 0x60
	s_and_b32 s16, s16, 0x1e0
	v_lshl_add_u32 v23, s16, 1, v19
	ds_read_b128 v[110:113], v23 offset:4096
	ds_read_b128 v[114:117], v23 offset:20736
	s_setprio 1
	s_waitcnt vmcnt(17) lgkmcnt(1)
	v_mfma_f32_16x16x32_f16 v[102:105], v[52:55], v[110:113], v[102:105]
	s_waitcnt lgkmcnt(0)
	v_mfma_f32_16x16x32_f16 v[28:31], v[52:55], v[114:117], v[28:31]
	s_waitcnt vmcnt(16)
	v_mfma_f32_16x16x32_f16 v[36:39], v[60:63], v[110:113], v[36:39]
	v_mfma_f32_16x16x32_f16 v[32:35], v[60:63], v[114:117], v[32:35]
	s_setprio 0
	s_add_i32 s16, s13, 0x300
	s_and_b32 s17, s16, 0x3c0
	s_lshl_b32 s26, s17, 4
	s_lshl_b32 s16, s16, 4
	v_lshl_add_u64 v[56:57], v[20:21], 0, s[26:27]
	s_or_b32 s26, s16, 0x4000
	v_lshl_add_u64 v[64:65], v[20:21], 0, s[26:27]
	global_load_dwordx4 v[52:55], v[56:57], off
	global_load_dwordx4 v[60:63], v[64:65], off
	s_add_i32 s16, s14, 0x80
	s_and_b32 s16, s16, 0x1e0
	v_lshl_add_u32 v23, s16, 1, v19
	ds_read_b128 v[110:113], v23 offset:4096
	ds_read_b128 v[114:117], v23 offset:20736
	s_setprio 1
	s_waitcnt vmcnt(17) lgkmcnt(1)
	v_mfma_f32_16x16x32_f16 v[102:105], v[68:71], v[110:113], v[102:105]
	s_waitcnt lgkmcnt(0)
	v_mfma_f32_16x16x32_f16 v[28:31], v[68:71], v[114:117], v[28:31]
	s_waitcnt vmcnt(16)
	v_mfma_f32_16x16x32_f16 v[36:39], v[72:75], v[110:113], v[36:39]
	v_mfma_f32_16x16x32_f16 v[32:35], v[72:75], v[114:117], v[32:35]
	s_setprio 0
	s_add_i32 s16, s13, 0x340
	s_and_b32 s17, s16, 0x3c0
	s_lshl_b32 s26, s17, 4
	s_lshl_b32 s16, s16, 4
	v_lshl_add_u64 v[56:57], v[20:21], 0, s[26:27]
	s_or_b32 s26, s16, 0x4000
	v_lshl_add_u64 v[64:65], v[20:21], 0, s[26:27]
	global_load_dwordx4 v[68:71], v[56:57], off
	global_load_dwordx4 v[72:75], v[64:65], off
	s_add_i32 s16, s14, 0xa0
	s_and_b32 s16, s16, 0x1e0
	v_lshl_add_u32 v23, s16, 1, v19
	ds_read_b128 v[110:113], v23 offset:4096
	ds_read_b128 v[114:117], v23 offset:20736
	s_setprio 1
	s_waitcnt vmcnt(17) lgkmcnt(1)
	v_mfma_f32_16x16x32_f16 v[102:105], v[76:79], v[110:113], v[102:105]
	s_waitcnt lgkmcnt(0)
	v_mfma_f32_16x16x32_f16 v[28:31], v[76:79], v[114:117], v[28:31]
	s_waitcnt vmcnt(16)
	v_mfma_f32_16x16x32_f16 v[36:39], v[82:85], v[110:113], v[36:39]
	v_mfma_f32_16x16x32_f16 v[32:35], v[82:85], v[114:117], v[32:35]
	s_setprio 0
	s_add_i32 s16, s13, 0x380
	s_and_b32 s17, s16, 0x3c0
	s_lshl_b32 s26, s17, 4
	s_lshl_b32 s16, s16, 4
	v_lshl_add_u64 v[56:57], v[20:21], 0, s[26:27]
	s_or_b32 s26, s16, 0x4000
	v_lshl_add_u64 v[64:65], v[20:21], 0, s[26:27]
	global_load_dwordx4 v[76:79], v[56:57], off
	global_load_dwordx4 v[82:85], v[64:65], off
	s_add_i32 s16, s14, 0xc0
	s_and_b32 s16, s16, 0x1e0
	v_lshl_add_u32 v23, s16, 1, v19
	ds_read_b128 v[110:113], v23 offset:4096
	ds_read_b128 v[114:117], v23 offset:20736
	s_setprio 1
	s_waitcnt vmcnt(17) lgkmcnt(1)
	v_mfma_f32_16x16x32_f16 v[102:105], v[14:17], v[110:113], v[102:105]
	s_waitcnt lgkmcnt(0)
	v_mfma_f32_16x16x32_f16 v[14:17], v[14:17], v[114:117], v[28:31]
	s_waitcnt vmcnt(16)
	v_mfma_f32_16x16x32_f16 v[28:31], v[10:13], v[110:113], v[36:39]
	v_mfma_f32_16x16x32_f16 v[10:13], v[10:13], v[114:117], v[32:35]
	s_setprio 0
	s_addk_i32 s13, 0x3c0
	s_and_b32 s16, s13, 0x3c0
	s_lshl_b32 s26, s16, 4
	s_lshl_b32 s13, s13, 4
	v_lshl_add_u64 v[56:57], v[20:21], 0, s[26:27]
	s_or_b32 s26, s13, 0x4000
	v_lshl_add_u64 v[20:21], v[20:21], 0, s[26:27]
	global_load_dwordx4 v[32:35], v[56:57], off
	global_load_dwordx4 v[36:39], v[20:21], off
	s_add_i32 s13, s14, 0xe0
	s_and_b32 s13, s13, 0x1e0
	v_lshl_add_u32 v20, s13, 1, v19
	ds_read_b128 v[110:113], v20 offset:4096
	ds_read_b128 v[114:117], v20 offset:20736
	s_setprio 1
	s_waitcnt vmcnt(17) lgkmcnt(1)
	v_mfma_f32_16x16x32_f16 v[102:105], v[6:9], v[110:113], v[102:105]
	s_waitcnt lgkmcnt(0)
	v_mfma_f32_16x16x32_f16 v[6:9], v[6:9], v[114:117], v[14:17]
	s_waitcnt vmcnt(16)
	v_mfma_f32_16x16x32_f16 v[14:17], v[2:5], v[110:113], v[28:31]
	v_mfma_f32_16x16x32_f16 v[2:5], v[2:5], v[114:117], v[10:13]
	s_setprio 0
	v_add_u32_e32 v20, s15, v19
	s_nop 0
	ds_read_b128 v[10:13], v20 offset:4096
	ds_read_b128 v[28:31], v20 offset:20736
	s_setprio 1
	s_waitcnt vmcnt(15) lgkmcnt(1)
	v_mfma_f32_16x16x32_f16 v[102:105], v[86:89], v[10:13], v[102:105]
	s_waitcnt lgkmcnt(0)
	v_mfma_f32_16x16x32_f16 v[6:9], v[86:89], v[28:31], v[6:9]
	s_waitcnt vmcnt(14)
	v_mfma_f32_16x16x32_f16 v[10:13], v[90:93], v[10:13], v[14:17]
	v_mfma_f32_16x16x32_f16 v[2:5], v[90:93], v[28:31], v[2:5]
	s_setprio 0
	s_add_i32 s13, s14, 0x120
	s_and_b32 s13, s13, 0x1e0
	v_lshl_add_u32 v20, s13, 1, v19
	ds_read_b128 v[14:17], v20 offset:4096
	ds_read_b128 v[28:31], v20 offset:20736
	s_setprio 1
	s_waitcnt vmcnt(13) lgkmcnt(1)
	v_mfma_f32_16x16x32_f16 v[86:89], v[98:101], v[14:17], v[102:105]
	s_waitcnt lgkmcnt(0)
	v_mfma_f32_16x16x32_f16 v[6:9], v[98:101], v[28:31], v[6:9]
	s_waitcnt vmcnt(12)
	v_mfma_f32_16x16x32_f16 v[10:13], v[106:109], v[14:17], v[10:13]
	v_mfma_f32_16x16x32_f16 v[2:5], v[106:109], v[28:31], v[2:5]
	s_setprio 0
	s_add_i32 s13, s14, 0x140
	s_and_b32 s13, s13, 0x1e0
	v_lshl_add_u32 v20, s13, 1, v19
	ds_read_b128 v[14:17], v20 offset:4096
	ds_read_b128 v[28:31], v20 offset:20736
	s_setprio 1
	s_waitcnt vmcnt(11) lgkmcnt(1)
	v_mfma_f32_16x16x32_f16 v[86:89], v[40:43], v[14:17], v[86:89]
	s_waitcnt lgkmcnt(0)
	v_mfma_f32_16x16x32_f16 v[6:9], v[40:43], v[28:31], v[6:9]
	s_waitcnt vmcnt(10)
	v_mfma_f32_16x16x32_f16 v[10:13], v[94:97], v[14:17], v[10:13]
	v_mfma_f32_16x16x32_f16 v[2:5], v[94:97], v[28:31], v[2:5]
	s_setprio 0
	s_add_i32 s13, s14, 0x160
	s_and_b32 s13, s13, 0x1e0
	v_lshl_add_u32 v20, s13, 1, v19
	ds_read_b128 v[14:17], v20 offset:4096
	ds_read_b128 v[28:31], v20 offset:20736
	s_setprio 1
	s_waitcnt vmcnt(9) lgkmcnt(1)
	v_mfma_f32_16x16x32_f16 v[40:43], v[44:47], v[14:17], v[86:89]
	s_waitcnt lgkmcnt(0)
	v_mfma_f32_16x16x32_f16 v[6:9], v[44:47], v[28:31], v[6:9]
	s_waitcnt vmcnt(8)
	v_mfma_f32_16x16x32_f16 v[10:13], v[48:51], v[14:17], v[10:13]
	v_mfma_f32_16x16x32_f16 v[2:5], v[48:51], v[28:31], v[2:5]
	s_setprio 0
	s_add_i32 s13, s14, 0x180
	s_and_b32 s13, s13, 0x1e0
	v_lshl_add_u32 v20, s13, 1, v19
	ds_read_b128 v[14:17], v20 offset:4096
	ds_read_b128 v[28:31], v20 offset:20736
	s_setprio 1
	s_waitcnt vmcnt(7) lgkmcnt(1)
	v_mfma_f32_16x16x32_f16 v[40:43], v[52:55], v[14:17], v[40:43]
	s_waitcnt lgkmcnt(0)
	v_mfma_f32_16x16x32_f16 v[6:9], v[52:55], v[28:31], v[6:9]
	s_waitcnt vmcnt(6)
	v_mfma_f32_16x16x32_f16 v[10:13], v[60:63], v[14:17], v[10:13]
	v_mfma_f32_16x16x32_f16 v[2:5], v[60:63], v[28:31], v[2:5]
	s_setprio 0
	s_add_i32 s13, s14, 0x1a0
	s_and_b32 s13, s13, 0x1e0
	v_lshl_add_u32 v20, s13, 1, v19
	ds_read_b128 v[14:17], v20 offset:4096
	ds_read_b128 v[28:31], v20 offset:20736
	s_setprio 1
	s_waitcnt vmcnt(5) lgkmcnt(1)
	v_mfma_f32_16x16x32_f16 v[40:43], v[68:71], v[14:17], v[40:43]
	s_waitcnt lgkmcnt(0)
	v_mfma_f32_16x16x32_f16 v[6:9], v[68:71], v[28:31], v[6:9]
	s_waitcnt vmcnt(4)
	v_mfma_f32_16x16x32_f16 v[10:13], v[72:75], v[14:17], v[10:13]
	v_mfma_f32_16x16x32_f16 v[2:5], v[72:75], v[28:31], v[2:5]
	s_setprio 0
	s_add_i32 s13, s14, 0x1c0
	s_and_b32 s13, s13, 0x1e0
	v_lshl_add_u32 v20, s13, 1, v19
	ds_read_b128 v[14:17], v20 offset:4096
	ds_read_b128 v[28:31], v20 offset:20736
	s_setprio 1
	s_waitcnt vmcnt(3) lgkmcnt(1)
	v_mfma_f32_16x16x32_f16 v[40:43], v[76:79], v[14:17], v[40:43]
	s_waitcnt lgkmcnt(0)
	v_mfma_f32_16x16x32_f16 v[6:9], v[76:79], v[28:31], v[6:9]
	s_waitcnt vmcnt(2)
	v_mfma_f32_16x16x32_f16 v[10:13], v[82:85], v[14:17], v[10:13]
	v_mfma_f32_16x16x32_f16 v[2:5], v[82:85], v[28:31], v[2:5]
	s_setprio 0
	s_addk_i32 s14, 0x1e0
	s_and_b32 s13, s14, 0x1e0
	v_lshl_add_u32 v20, s13, 1, v19
	ds_read_b128 v[14:17], v20 offset:4096
	ds_read_b128 v[28:31], v20 offset:20736
	s_setprio 1
	s_waitcnt vmcnt(1) lgkmcnt(1)
	v_mfma_f32_16x16x32_f16 v[40:43], v[32:35], v[14:17], v[40:43]
	s_waitcnt lgkmcnt(0)
	v_mfma_f32_16x16x32_f16 v[6:9], v[32:35], v[28:31], v[6:9]
	s_waitcnt vmcnt(0)
	v_mfma_f32_16x16x32_f16 v[10:13], v[36:39], v[14:17], v[10:13]
	v_mfma_f32_16x16x32_f16 v[2:5], v[36:39], v[28:31], v[2:5]
	s_setprio 0
	v_add_u32_e32 v19, v19, v22
	v_lshlrev_b32_e32 v20, 15, v118
	v_mov_b32_e32 v21, v67
	s_bfe_u32 s22, s2, 0x30003
	v_lshl_add_u64 v[20:21], s[10:11], 0, v[20:21]
	s_lshl_b32 s26, s22, 10
	v_lshl_add_u64 v[64:65], v[20:21], 0, v[58:59]
	v_lshl_add_u64 v[52:53], v[64:65], 0, s[26:27]
	v_add_co_u32_e32 v76, vcc, s29, v52
	s_lshl_b32 s53, s22, 6
	s_nop 0
	v_addc_co_u32_e32 v77, vcc, 0, v53, vcc
	s_mov_b32 s14, 0x14000
	v_mov_b32_e32 v22, 0x14000
	v_mul_u32_u24_e32 v23, 0x210, v81
	s_add_i32 s38, s53, 64
	v_lshlrev_b32_e32 v83, 2, v118
	s_movk_i32 s16, 0x1040
	s_movk_i32 s18, 0x840
	v_lshl_or_b32 v1, v1, 3, v22
	v_add3_u32 v84, v23, v18, s14
	s_and_b32 s14, s38, 0x1c0
	s_movk_i32 s20, 0x210
	s_mov_b32 s19, s27
	v_mad_u32_u24 v56, v118, s16, v58
	v_or_b32_e32 v22, 1, v83
	v_mad_u32_u24 v98, v118, s18, v1
	s_lshl_b32 s18, s14, 4
	v_mad_u32_u24 v99, v22, s12, v58
	v_mad_u32_u24 v85, v22, s20, v1
	v_lshl_add_u64 v[54:55], v[64:65], 0, s[18:19]
	s_add_i32 s12, s53, 0xc0
	s_and_b32 s2, s3, 0x7ffffff
	s_lshl_b32 s3, s22, 5
	s_and_b32 s39, s12, 0x1c0
	s_lshl_b32 s14, s39, 4
	s_add_i32 s39, s3, 32
	s_and_b32 s39, s39, 0xe0
	v_lshl_add_u32 v82, s39, 1, v84
	s_add_i32 s11, s53, 0x80
	s_lshl_b32 s16, s38, 4
	s_mov_b32 s21, s27
	s_and_b32 s30, s11, 0x1c0
	s_lshl_b32 s11, s11, 4
	s_or_b32 s20, s16, 0x2000
	s_mov_b32 s23, s27
	s_mov_b32 s31, s27
	s_mov_b32 s35, s27
	s_or_b32 s22, s16, 0x6000
	s_lshl_b32 s30, s30, 4
	s_or_b32 s34, s11, 0x2000
	v_lshl_add_u64 v[26:27], v[64:65], 0, s[20:21]
	v_lshl_add_u64 v[28:29], v[64:65], 0, s[22:23]
	v_lshl_add_u64 v[30:31], v[64:65], 0, s[30:31]
	v_lshl_add_u64 v[32:33], v[64:65], 0, s[34:35]
	s_mov_b64 s[40:41], 0x40000
	v_lshl_add_u64 v[60:61], v[64:65], 0, s[40:41]
	s_mov_b32 s37, s27
	s_or_b32 s36, s11, 0x6000
	v_lshl_add_u64 v[74:75], v[64:65], 0, s[36:37]
	s_mov_b32 s15, s27
	s_lshl_b32 s12, s12, 4
	v_lshl_add_u64 v[70:71], v[64:65], 0, s[14:15]
	s_mov_b32 s17, s27
	s_or_b32 s16, s12, 0x2000
	s_mov_b32 s13, s27
	s_or_b32 s12, s12, 0x6000
	v_lshl_add_u64 v[72:73], v[64:65], 0, s[16:17]
	v_lshl_add_u64 v[68:69], v[64:65], 0, s[12:13]
	v_add_u32_e32 v1, s53, v84
	s_xor_b32 s10, s26, 0x1000
	s_mov_b32 s11, s27
	s_mov_b32 s49, s27
	s_mov_b32 s51, s27
	s_mov_b32 s47, s27
	v_pk_add_f32 v[14:15], v[180:181], v[40:41]
	v_pk_add_f32 v[16:17], v[182:183], v[42:43]
	v_pk_add_f32 v[10:11], v[184:185], v[10:11]
	v_pk_add_f32 v[12:13], v[186:187], v[12:13]
	v_pk_add_f32 v[6:7], v[188:189], v[6:7]
	v_pk_add_f32 v[8:9], v[190:191], v[8:9]
	v_pk_add_f32 v[2:3], v[192:193], v[2:3]
	v_pk_add_f32 v[4:5], v[194:195], v[4:5]
	ds_write_b128 v19, v[14:17] offset:37376
	ds_write_b128 v19, v[10:13] offset:37440
	ds_write_b128 v19, v[6:9] offset:54016
	ds_write_b128 v19, v[2:5] offset:54080
	v_mov_b64_e32 v[34:35], v[204:205]
	v_mov_b64_e32 v[36:37], v[206:207]
	v_mov_b64_e32 v[38:39], v[208:209]
	v_mov_b64_e32 v[40:41], v[210:211]
	v_add_co_u32_e32 v2, vcc, s52, v52
	s_waitcnt lgkmcnt(0)
	s_nop 0
	v_addc_co_u32_e32 v3, vcc, 0, v53, vcc
	v_add_co_u32_e32 v4, vcc, s33, v52
	s_barrier
	s_nop 0
	v_addc_co_u32_e32 v5, vcc, 0, v53, vcc
	global_load_dwordx4 v[14:17], v[2:3], off
	global_load_dwordx4 v[18:21], v[4:5], off
	global_load_dwordx4 v[22:25], v[52:53], off
	global_load_dwordx4 v[10:13], v[54:55], off
	ds_read_b128 v[2:5], v56 offset:37376
	ds_read_b128 v[6:9], v99 offset:37376
	v_add_co_u32_e32 v78, vcc, s52, v54
	s_mov_b32 s43, s27
	s_waitcnt lgkmcnt(1)
	v_add_f32_e32 v42, v2, v3
	v_add_f32_e32 v42, v42, v4
	v_add_f32_e32 v42, v42, v5
	v_addc_co_u32_e32 v79, vcc, 0, v55, vcc
	s_nop 0
	v_add_f32_dpp v42, v42, v42 quad_perm:[1,0,3,2] row_mask:0xf bank_mask:0xf bound_ctrl:1
	s_mov_b32 s45, s27
	s_mov_b32 s41, s27
	v_add_f32_dpp v42, v42, v42 quad_perm:[2,3,0,1] row_mask:0xf bank_mask:0xf bound_ctrl:1
	v_lshl_add_u64 v[62:63], v[64:65], 0, s[10:11]
	v_lshl_add_u64 v[58:59], s[4:5], 0, v[58:59]
	v_add_f32_dpp v42, v42, v42 row_half_mirror row_mask:0xf bank_mask:0xf bound_ctrl:1
	v_lshl_add_u64 v[152:153], v[60:61], 0, s[26:27]
	v_lshl_add_u64 v[154:155], v[60:61], 0, s[18:19]
	v_add_f32_dpp v42, v42, v42 row_mirror row_mask:0xf bank_mask:0xf bound_ctrl:1
	v_lshl_add_u64 v[156:157], v[60:61], 0, s[20:21]
	v_readlane_b32 s8, v42, 16
	v_readlane_b32 s9, v42, 48
	v_readlane_b32 s6, v42, 0
	v_readlane_b32 s7, v42, 32
	v_mov_b32_e32 v42, s8
	v_mov_b32_e32 v43, s9
	v_pk_add_f32 v[42:43], s[6:7], v[42:43]
	s_mov_b32 s6, 0x3b800000
	v_add_f32_e32 v42, v42, v43
	v_mul_f32_e32 v42, 0x3b800000, v42
	v_pk_add_f32 v[86:87], v[2:3], v[42:43] op_sel_hi:[1,0] neg_lo:[0,1] neg_hi:[0,1]
	v_pk_add_f32 v[88:89], v[4:5], v[42:43] op_sel_hi:[1,0] neg_lo:[0,1] neg_hi:[0,1]
	v_pk_mul_f32 v[42:43], v[86:87], v[86:87]
	v_pk_mul_f32 v[44:45], v[88:89], v[88:89]
	v_add_f32_e32 v42, v42, v43
	v_add_f32_e32 v42, v44, v42
	s_waitcnt lgkmcnt(0)
	v_add_f32_e32 v44, v6, v7
	v_add_f32_e32 v42, v45, v42
	v_add_f32_e32 v44, v44, v8
	v_add_f32_e32 v44, v44, v9
	v_add_f32_dpp v42, v42, v42 quad_perm:[1,0,3,2] row_mask:0xf bank_mask:0xf bound_ctrl:1
	v_lshl_add_u64 v[158:159], v[60:61], 0, s[22:23]
	v_add_f32_dpp v44, v44, v44 quad_perm:[1,0,3,2] row_mask:0xf bank_mask:0xf bound_ctrl:1
	v_add_f32_dpp v42, v42, v42 quad_perm:[2,3,0,1] row_mask:0xf bank_mask:0xf bound_ctrl:1
	v_lshl_add_u64 v[160:161], v[60:61], 0, s[30:31]
	v_add_f32_dpp v44, v44, v44 quad_perm:[2,3,0,1] row_mask:0xf bank_mask:0xf bound_ctrl:1
	v_add_f32_dpp v42, v42, v42 row_half_mirror row_mask:0xf bank_mask:0xf bound_ctrl:1
	v_lshl_add_u64 v[162:163], v[60:61], 0, s[34:35]
	v_add_f32_dpp v44, v44, v44 row_half_mirror row_mask:0xf bank_mask:0xf bound_ctrl:1
	v_add_f32_dpp v42, v42, v42 row_mirror row_mask:0xf bank_mask:0xf bound_ctrl:1
	v_lshl_add_u64 v[164:165], v[60:61], 0, s[36:37]
	v_readlane_b32 s7, v42, 16
	v_readlane_b32 s39, v42, 48
	v_add_f32_dpp v44, v44, v44 row_mirror row_mask:0xf bank_mask:0xf bound_ctrl:1
	v_readlane_b32 s8, v42, 0
	v_readlane_b32 s9, v42, 32
	v_mov_b32_e32 v42, s7
	v_mov_b32_e32 v43, s39
	v_readlane_b32 s7, v44, 16
	v_readlane_b32 s39, v44, 48
	v_pk_add_f32 v[42:43], s[8:9], v[42:43]
	v_readlane_b32 s8, v44, 0
	v_readlane_b32 s9, v44, 32
	v_mov_b32_e32 v44, s7
	v_mov_b32_e32 v45, s39
	v_pk_add_f32 v[44:45], s[8:9], v[44:45]
	s_nop 0
	v_add_f32_e32 v44, v44, v45
	v_mul_f32_e32 v44, 0x3b800000, v44
	v_pk_add_f32 v[90:91], v[6:7], v[44:45] op_sel_hi:[1,0] neg_lo:[0,1] neg_hi:[0,1]
	v_pk_add_f32 v[92:93], v[8:9], v[44:45] op_sel_hi:[1,0] neg_lo:[0,1] neg_hi:[0,1]
	v_pk_mul_f32 v[46:47], v[90:91], v[90:91]
	v_pk_mul_f32 v[44:45], v[92:93], v[92:93]
	v_add_f32_e32 v46, v46, v47
	v_add_f32_e32 v44, v44, v46
	v_add_f32_e32 v44, v45, v44
	v_mov_b32_e32 v47, v42
	s_nop 0
	v_add_f32_dpp v44, v44, v44 quad_perm:[1,0,3,2] row_mask:0xf bank_mask:0xf bound_ctrl:1
	s_nop 1
	v_add_f32_dpp v44, v44, v44 quad_perm:[2,3,0,1] row_mask:0xf bank_mask:0xf bound_ctrl:1
	s_nop 1
	v_add_f32_dpp v44, v44, v44 row_half_mirror row_mask:0xf bank_mask:0xf bound_ctrl:1
	s_nop 1
	v_add_f32_dpp v44, v44, v44 row_mirror row_mask:0xf bank_mask:0xf bound_ctrl:1
	s_nop 0
	v_readlane_b32 s7, v44, 16
	v_readlane_b32 s39, v44, 48
	v_readlane_b32 s8, v44, 0
	v_readlane_b32 s9, v44, 32
	v_mov_b32_e32 v44, s7
	v_mov_b32_e32 v45, s39
	v_pk_add_f32 v[44:45], s[8:9], v[44:45]
	s_mov_b32 s8, 0x3727c5ac
	v_mov_b32_e32 v46, v44
	v_mov_b32_e32 v42, v45
	v_pk_add_f32 v[42:43], v[46:47], v[42:43]
	v_mov_b64_e32 v[94:95], s[8:9]
	v_pk_fma_f32 v[96:97], v[42:43], s[6:7], v[94:95] op_sel_hi:[1,0,0]
	s_mov_b32 s7, 0x800000
	v_mul_f32_e32 v42, 0x4b800000, v97
	v_cmp_gt_f32_e32 vcc, s7, v97
	s_nop 1
	v_cndmask_b32_e32 v42, v97, v42, vcc
	v_rsq_f32_e32 v97, v42
	global_load_dwordx4 v[54:57], v[26:27], off
	global_load_dwordx4 v[50:53], v[28:29], off
	global_load_dwordx4 v[46:49], v[30:31], off
	global_load_dwordx4 v[42:45], v[32:33], off
	v_mul_f32_e32 v26, 0x45800000, v97
	v_cndmask_b32_e32 v26, v97, v26, vcc
	v_pk_mul_f32 v[28:29], v[86:87], v[26:27] op_sel_hi:[1,0]
	v_cmp_gt_f32_e32 vcc, s7, v96
	s_waitcnt vmcnt(8)
	v_pk_fma_f32 v[28:29], v[34:35], v[28:29], v[38:39]
	v_pk_mul_f32 v[26:27], v[88:89], v[26:27] op_sel_hi:[1,0]
	v_cvt_pk_f16_f32 v28, v28, v29
	v_mul_f32_e32 v29, 0x4b800000, v96
	v_cndmask_b32_e32 v29, v96, v29, vcc
	v_rsq_f32_e32 v32, v29
	v_pk_fma_f32 v[26:27], v[36:37], v[26:27], v[40:41]
	s_nop 0
	v_cvt_pk_f16_f32 v29, v26, v27
	v_mul_f32_e32 v26, 0x45800000, v32
	v_cndmask_b32_e32 v26, v32, v26, vcc
	ds_write_b64 v98, v[28:29]
	v_pk_mul_f32 v[28:29], v[90:91], v[26:27] op_sel_hi:[1,0]
	v_pk_mul_f32 v[26:27], v[92:93], v[26:27] op_sel_hi:[1,0]
	v_pk_fma_f32 v[28:29], v[34:35], v[28:29], v[38:39]
	v_pk_fma_f32 v[26:27], v[36:37], v[26:27], v[40:41]
	v_cvt_pk_f16_f32 v28, v28, v29
	v_cvt_pk_f16_f32 v29, v26, v27
	ds_write_b64 v85, v[28:29]
	ds_read_b128 v[26:29], v99 offset:38416
	v_add_co_u32_e32 v102, vcc, s52, v30
	s_nop 1
	v_addc_co_u32_e32 v103, vcc, 0, v31, vcc
	ds_read_b128 v[30:33], v99 offset:39456
	s_waitcnt lgkmcnt(1)
	v_add_f32_e32 v86, v26, v27
	v_add_f32_e32 v86, v86, v28
	v_add_f32_e32 v86, v86, v29
	s_nop 1
	v_add_f32_dpp v86, v86, v86 quad_perm:[1,0,3,2] row_mask:0xf bank_mask:0xf bound_ctrl:1
	s_nop 1
	v_add_f32_dpp v86, v86, v86 quad_perm:[2,3,0,1] row_mask:0xf bank_mask:0xf bound_ctrl:1
	s_nop 1
	v_add_f32_dpp v86, v86, v86 row_half_mirror row_mask:0xf bank_mask:0xf bound_ctrl:1
	s_nop 1
	v_add_f32_dpp v86, v86, v86 row_mirror row_mask:0xf bank_mask:0xf bound_ctrl:1
	s_nop 0
	v_readlane_b32 s39, v86, 16
	v_readlane_b32 s40, v86, 48
	v_readlane_b32 s8, v86, 0
	v_readlane_b32 s9, v86, 32
	v_mov_b32_e32 v86, s39
	v_mov_b32_e32 v87, s40
	v_pk_add_f32 v[86:87], s[8:9], v[86:87]
	s_nop 0
	v_add_f32_e32 v86, v86, v87
	v_mul_f32_e32 v86, 0x3b800000, v86
	v_pk_add_f32 v[104:105], v[26:27], v[86:87] op_sel_hi:[1,0] neg_lo:[0,1] neg_hi:[0,1]
	v_pk_add_f32 v[106:107], v[28:29], v[86:87] op_sel_hi:[1,0] neg_lo:[0,1] neg_hi:[0,1]
	v_pk_mul_f32 v[88:89], v[104:105], v[104:105]
	v_pk_mul_f32 v[86:87], v[106:107], v[106:107]
	v_add_f32_e32 v88, v88, v89
	v_add_f32_e32 v86, v86, v88
	s_waitcnt lgkmcnt(0)
	v_add_f32_e32 v88, v30, v31
	v_add_f32_e32 v86, v87, v86
	v_add_f32_e32 v88, v88, v32
	v_add_f32_e32 v88, v88, v33
	v_add_f32_dpp v86, v86, v86 quad_perm:[1,0,3,2] row_mask:0xf bank_mask:0xf bound_ctrl:1
	s_nop 0
	v_add_f32_dpp v88, v88, v88 quad_perm:[1,0,3,2] row_mask:0xf bank_mask:0xf bound_ctrl:1
	v_add_f32_dpp v86, v86, v86 quad_perm:[2,3,0,1] row_mask:0xf bank_mask:0xf bound_ctrl:1
	s_nop 0
	v_add_f32_dpp v88, v88, v88 quad_perm:[2,3,0,1] row_mask:0xf bank_mask:0xf bound_ctrl:1
	v_add_f32_dpp v86, v86, v86 row_half_mirror row_mask:0xf bank_mask:0xf bound_ctrl:1
	s_nop 0
	v_add_f32_dpp v88, v88, v88 row_half_mirror row_mask:0xf bank_mask:0xf bound_ctrl:1
	v_add_f32_dpp v86, v86, v86 row_mirror row_mask:0xf bank_mask:0xf bound_ctrl:1
	s_nop 0
	v_readlane_b32 s39, v86, 16
	v_readlane_b32 s40, v86, 48
	v_add_f32_dpp v88, v88, v88 row_mirror row_mask:0xf bank_mask:0xf bound_ctrl:1
	v_readlane_b32 s8, v86, 0
	v_readlane_b32 s9, v86, 32
	v_mov_b32_e32 v86, s39
	v_mov_b32_e32 v87, s40
	v_readlane_b32 s39, v88, 16
	v_readlane_b32 s40, v88, 48
	v_pk_add_f32 v[86:87], s[8:9], v[86:87]
	v_readlane_b32 s8, v88, 0
	v_readlane_b32 s9, v88, 32
	v_mov_b32_e32 v88, s39
	v_mov_b32_e32 v89, s40
	v_pk_add_f32 v[88:89], s[8:9], v[88:89]
	s_nop 0
	v_add_f32_e32 v88, v88, v89
	v_mul_f32_e32 v88, 0x3b800000, v88
	v_pk_add_f32 v[108:109], v[30:31], v[88:89] op_sel_hi:[1,0] neg_lo:[0,1] neg_hi:[0,1]
	v_pk_add_f32 v[110:111], v[32:33], v[88:89] op_sel_hi:[1,0] neg_lo:[0,1] neg_hi:[0,1]
	v_pk_mul_f32 v[90:91], v[108:109], v[108:109]
	v_pk_mul_f32 v[88:89], v[110:111], v[110:111]
	v_add_f32_e32 v90, v90, v91
	v_add_f32_e32 v88, v88, v90
	v_add_f32_e32 v88, v89, v88
	v_mov_b32_e32 v91, v86
	s_nop 0
	v_add_f32_dpp v88, v88, v88 quad_perm:[1,0,3,2] row_mask:0xf bank_mask:0xf bound_ctrl:1
	s_nop 1
	v_add_f32_dpp v88, v88, v88 quad_perm:[2,3,0,1] row_mask:0xf bank_mask:0xf bound_ctrl:1
	s_nop 1
	v_add_f32_dpp v88, v88, v88 row_half_mirror row_mask:0xf bank_mask:0xf bound_ctrl:1
	s_nop 1
	v_add_f32_dpp v88, v88, v88 row_mirror row_mask:0xf bank_mask:0xf bound_ctrl:1
	s_nop 0
	v_readlane_b32 s39, v88, 16
	v_readlane_b32 s40, v88, 48
	v_readlane_b32 s8, v88, 0
	v_readlane_b32 s9, v88, 32
	v_mov_b32_e32 v88, s39
	v_mov_b32_e32 v89, s40
	v_pk_add_f32 v[88:89], s[8:9], v[88:89]
	s_mov_b32 s9, s27
	v_mov_b32_e32 v90, v88
	v_mov_b32_e32 v86, v89
	v_pk_add_f32 v[86:87], v[90:91], v[86:87]
	s_mov_b32 s39, s27
	v_pk_fma_f32 v[112:113], v[86:87], s[6:7], v[94:95] op_sel_hi:[1,0,0]
	s_add_i32 s6, s53, 0x140
	v_mul_f32_e32 v86, 0x4b800000, v113
	v_cmp_gt_f32_e32 vcc, s7, v113
	s_nop 1
	v_cndmask_b32_e32 v86, v113, v86, vcc
	v_rsq_f32_e32 v113, v86
	global_load_dwordx4 v[86:89], v[78:79], off
	global_load_dwordx4 v[90:93], v[102:103], off
	global_load_dwordx4 v[94:97], v[76:77], off
	global_load_dwordx4 v[98:101], v[74:75], off
	v_mul_f32_e32 v74, 0x45800000, v113
	v_cndmask_b32_e32 v74, v113, v74, vcc
	v_pk_mul_f32 v[76:77], v[104:105], v[74:75] op_sel_hi:[1,0]
	v_mul_f32_e32 v75, 0x4b800000, v112
	v_cmp_gt_f32_e32 vcc, s7, v112
	v_pk_fma_f32 v[76:77], v[34:35], v[76:77], v[38:39]
	s_and_b32 s7, s6, 0x1c0
	v_cndmask_b32_e32 v75, v112, v75, vcc
	v_rsq_f32_e32 v78, v75
	v_pk_mul_f32 v[74:75], v[106:107], v[74:75] op_sel_hi:[1,0]
	v_cvt_pk_f16_f32 v76, v76, v77
	v_pk_fma_f32 v[74:75], v[36:37], v[74:75], v[40:41]
	s_lshl_b32 s6, s6, 4
	v_cvt_pk_f16_f32 v77, v74, v75
	v_mul_f32_e32 v74, 0x45800000, v78
	v_cndmask_b32_e32 v74, v78, v74, vcc
	v_pk_mul_f32 v[78:79], v[108:109], v[74:75] op_sel_hi:[1,0]
	s_or_b32 s50, s6, 0x2000
	v_pk_fma_f32 v[34:35], v[34:35], v[78:79], v[38:39]
	v_pk_mul_f32 v[38:39], v[110:111], v[74:75] op_sel_hi:[1,0]
	v_add_co_u32_e32 v78, vcc, s52, v70
	v_pk_fma_f32 v[36:37], v[36:37], v[38:39], v[40:41]
	v_cvt_pk_f16_f32 v34, v34, v35
	v_cvt_pk_f16_f32 v35, v36, v37
	v_addc_co_u32_e32 v79, vcc, 0, v71, vcc
	ds_write2_b64 v85, v[76:77], v[34:35] offset0:66 offset1:132
	s_waitcnt lgkmcnt(0)
	s_barrier
	global_load_dwordx4 v[34:37], v[70:71], off
	global_load_dwordx4 v[38:41], v[72:73], off
	s_nop 0
	global_load_dwordx4 v[70:73], v[78:79], off
	global_load_dwordx4 v[74:77], v[68:69], off
	s_or_b32 s46, s6, 0x6000
	s_sub_i32 s6, s38, s3
	s_and_b32 s6, s6, 0xe0
	v_lshl_add_u32 v172, s6, 1, v84
	s_add_i32 s6, s53, 0x180
	s_lshl_b32 s48, s7, 4
	s_and_b32 s7, s6, 0x1c0
	s_lshl_b32 s6, s6, 4
	s_or_b32 s44, s6, 0x2000
	s_or_b32 s40, s6, 0x6000
	s_add_i32 s6, s3, 0x60
	s_and_b32 s6, s6, 0xe0
	v_lshl_add_u32 v173, s6, 1, v84
	s_add_i32 s6, s53, 0x1c0
	s_xor_b32 s53, s53, 0x100
	v_add_u32_e32 v174, s53, v84
	s_add_i32 s53, s3, 0xa0
	s_lshl_b32 s42, s7, 4
	s_and_b32 s7, s6, 0x1c0
	s_lshl_b32 s6, s6, 4
	s_and_b32 s53, s53, 0xe0
	s_lshl_b32 s8, s7, 4
	s_or_b32 s38, s6, 0x2000
	s_or_b32 s6, s6, 0x6000
	s_mov_b32 s7, s27
	v_lshl_add_u32 v175, s53, 1, v84
	s_add_i32 s53, s3, 0xc0
	s_addk_i32 s3, 0xe0
	v_lshl_add_u64 v[68:69], v[64:65], 0, s[48:49]
	v_lshl_add_u64 v[78:79], v[64:65], 0, s[50:51]
	v_lshl_add_u64 v[138:139], v[64:65], 0, s[46:47]
	v_lshl_add_u64 v[140:141], v[64:65], 0, s[42:43]
	v_lshl_add_u64 v[142:143], v[64:65], 0, s[44:45]
	v_lshl_add_u64 v[144:145], v[64:65], 0, s[40:41]
	v_lshl_add_u64 v[146:147], v[64:65], 0, s[8:9]
	v_lshl_add_u64 v[148:149], v[64:65], 0, s[38:39]
	v_lshl_add_u64 v[150:151], v[64:65], 0, s[6:7]
	s_and_b32 s53, s53, 0xe0
	s_and_b32 s3, s3, 0xe0
	v_add_u32_e32 v64, s28, v83
	v_mov_b32_e32 v65, v67
	v_lshl_add_u32 v176, s53, 1, v84
	v_lshl_add_u32 v177, s3, 1, v84
	v_lshlrev_b64 v[84:85], 10, v[64:65]
	ds_read_b128 v[102:105], v1
	ds_read_b128 v[106:109], v1 offset:8448
	v_lshl_add_u64 v[166:167], v[58:59], 0, v[84:85]
	v_or_b32_e32 v84, 1, v64
	v_mov_b32_e32 v85, v67
	v_lshlrev_b64 v[84:85], 10, v[84:85]
	v_lshl_add_u64 v[168:169], v[58:59], 0, v[84:85]
	v_or_b32_e32 v84, 2, v64
	v_mov_b32_e32 v85, v67
	v_or_b32_e32 v64, 3, v64
	v_lshlrev_b64 v[84:85], 10, v[84:85]
	v_lshlrev_b64 v[64:65], 10, v[64:65]
	v_lshl_add_u64 v[170:171], v[58:59], 0, v[84:85]
	v_lshl_add_u64 v[58:59], v[58:59], 0, v[64:65]
	s_setprio 1
	s_waitcnt vmcnt(13) lgkmcnt(1)
	v_mfma_f32_16x16x32_f16 v[110:113], v[102:105], v[22:25], 0
	s_waitcnt lgkmcnt(0)
	v_mfma_f32_16x16x32_f16 v[22:25], v[106:109], v[22:25], 0
	s_waitcnt vmcnt(5)
	v_mfma_f32_16x16x32_f16 v[114:117], v[102:105], v[94:97], 0
	v_mfma_f32_16x16x32_f16 v[94:97], v[106:109], v[94:97], 0
	v_mfma_f32_16x16x32_f16 v[118:121], v[102:105], v[14:17], 0
	v_mfma_f32_16x16x32_f16 v[14:17], v[106:109], v[14:17], 0
	v_mfma_f32_16x16x32_f16 v[102:105], v[102:105], v[18:21], 0
	v_mfma_f32_16x16x32_f16 v[18:21], v[106:109], v[18:21], 0
	s_setprio 0
	v_add_co_u32_e32 v64, vcc, s29, v62
	global_load_dwordx4 v[106:109], v[62:63], off
	s_nop 0
	v_addc_co_u32_e32 v65, vcc, 0, v63, vcc
	v_add_co_u32_e32 v84, vcc, s52, v62
	s_nop 1
	v_addc_co_u32_e32 v85, vcc, 0, v63, vcc
	v_add_co_u32_e32 v62, vcc, s33, v62
	global_load_dwordx4 v[122:125], v[64:65], off
	global_load_dwordx4 v[126:129], v[84:85], off
	v_addc_co_u32_e32 v63, vcc, 0, v63, vcc
	global_load_dwordx4 v[62:65], v[62:63], off
	ds_read_b128 v[130:133], v82
	ds_read_b128 v[134:137], v82 offset:8448
	s_setprio 1
	s_waitcnt lgkmcnt(1)
	v_mfma_f32_16x16x32_f16 v[110:113], v[130:133], v[10:13], v[110:113]
	s_waitcnt lgkmcnt(0)
	v_mfma_f32_16x16x32_f16 v[10:13], v[134:137], v[10:13], v[22:25]
	v_mfma_f32_16x16x32_f16 v[22:25], v[130:133], v[54:57], v[114:117]
	v_mfma_f32_16x16x32_f16 v[54:57], v[134:137], v[54:57], v[94:97]
	v_mfma_f32_16x16x32_f16 v[94:97], v[130:133], v[86:89], v[118:121]
	v_mfma_f32_16x16x32_f16 v[14:17], v[134:137], v[86:89], v[14:17]
	v_mfma_f32_16x16x32_f16 v[84:87], v[130:133], v[50:53], v[102:105]
	v_mfma_f32_16x16x32_f16 v[18:21], v[134:137], v[50:53], v[18:21]
	s_setprio 0
	global_load_dwordx4 v[50:53], v[68:69], off
	global_load_dwordx4 v[102:105], v[78:79], off
	v_add_co_u32_e32 v68, vcc, s52, v68
	s_nop 1
	v_addc_co_u32_e32 v69, vcc, 0, v69, vcc
	global_load_dwordx4 v[114:117], v[68:69], off
	global_load_dwordx4 v[118:121], v[138:139], off
	ds_read_b128 v[130:133], v172
	ds_read_b128 v[134:137], v172 offset:8448
	s_setprio 1
	s_waitcnt lgkmcnt(1)
	v_mfma_f32_16x16x32_f16 v[110:113], v[130:133], v[46:49], v[110:113]
	s_waitcnt lgkmcnt(0)
	v_mfma_f32_16x16x32_f16 v[10:13], v[134:137], v[46:49], v[10:13]
	v_mfma_f32_16x16x32_f16 v[22:25], v[130:133], v[42:45], v[22:25]
	v_mfma_f32_16x16x32_f16 v[42:45], v[134:137], v[42:45], v[54:57]
	v_mfma_f32_16x16x32_f16 v[46:49], v[130:133], v[90:93], v[94:97]
	v_mfma_f32_16x16x32_f16 v[14:17], v[134:137], v[90:93], v[14:17]
	s_waitcnt vmcnt(12)
	v_mfma_f32_16x16x32_f16 v[54:57], v[130:133], v[98:101], v[84:87]
	v_mfma_f32_16x16x32_f16 v[18:21], v[134:137], v[98:101], v[18:21]
	s_setprio 0
	v_add_co_u32_e32 v68, vcc, s52, v140
	global_load_dwordx4 v[84:87], v[140:141], off
	global_load_dwordx4 v[88:91], v[142:143], off
	v_addc_co_u32_e32 v69, vcc, 0, v141, vcc
	global_load_dwordx4 v[92:95], v[68:69], off
	global_load_dwordx4 v[96:99], v[144:145], off
	ds_read_b128 v[130:133], v173
	ds_read_b128 v[134:137], v173 offset:8448
	s_setprio 1
	s_waitcnt vmcnt(15) lgkmcnt(1)
	v_mfma_f32_16x16x32_f16 v[110:113], v[130:133], v[34:37], v[110:113]
	s_waitcnt lgkmcnt(0)
	v_mfma_f32_16x16x32_f16 v[10:13], v[134:137], v[34:37], v[10:13]
	s_waitcnt vmcnt(14)
	v_mfma_f32_16x16x32_f16 v[22:25], v[130:133], v[38:41], v[22:25]
	v_mfma_f32_16x16x32_f16 v[34:37], v[134:137], v[38:41], v[42:45]
	s_waitcnt vmcnt(13)
	v_mfma_f32_16x16x32_f16 v[38:41], v[130:133], v[70:73], v[46:49]
	v_mfma_f32_16x16x32_f16 v[14:17], v[134:137], v[70:73], v[14:17]
	s_waitcnt vmcnt(12)
	v_mfma_f32_16x16x32_f16 v[42:45], v[130:133], v[74:77], v[54:57]
	v_mfma_f32_16x16x32_f16 v[18:21], v[134:137], v[74:77], v[18:21]
	s_setprio 0
	v_add_co_u32_e32 v68, vcc, s52, v146
	global_load_dwordx4 v[46:49], v[146:147], off
	global_load_dwordx4 v[54:57], v[148:149], off
	v_addc_co_u32_e32 v69, vcc, 0, v147, vcc
	global_load_dwordx4 v[68:71], v[68:69], off
	s_nop 0
	global_load_dwordx4 v[72:75], v[150:151], off
	ds_read_b128 v[76:79], v174
	ds_read_b128 v[130:133], v174 offset:8448
	s_setprio 1
	s_waitcnt vmcnt(15) lgkmcnt(1)
	v_mfma_f32_16x16x32_f16 v[110:113], v[76:79], v[106:109], v[110:113]
	s_waitcnt lgkmcnt(0)
	v_mfma_f32_16x16x32_f16 v[10:13], v[130:133], v[106:109], v[10:13]
	s_waitcnt vmcnt(14)
	v_mfma_f32_16x16x32_f16 v[22:25], v[76:79], v[122:125], v[22:25]
	v_mfma_f32_16x16x32_f16 v[34:37], v[130:133], v[122:125], v[34:37]
	s_waitcnt vmcnt(13)
	v_mfma_f32_16x16x32_f16 v[38:41], v[76:79], v[126:129], v[38:41]
	v_mfma_f32_16x16x32_f16 v[14:17], v[130:133], v[126:129], v[14:17]
	s_waitcnt vmcnt(12)
	v_mfma_f32_16x16x32_f16 v[42:45], v[76:79], v[62:65], v[42:45]
	v_mfma_f32_16x16x32_f16 v[18:21], v[130:133], v[62:65], v[18:21]
	s_setprio 0
	ds_read_b128 v[62:65], v175
	ds_read_b128 v[76:79], v175 offset:8448
	s_setprio 1
	s_waitcnt vmcnt(11) lgkmcnt(1)
	v_mfma_f32_16x16x32_f16 v[106:109], v[62:65], v[50:53], v[110:113]
	s_waitcnt lgkmcnt(0)
	v_mfma_f32_16x16x32_f16 v[10:13], v[76:79], v[50:53], v[10:13]
	s_waitcnt vmcnt(10)
	v_mfma_f32_16x16x32_f16 v[22:25], v[62:65], v[102:105], v[22:25]
	v_mfma_f32_16x16x32_f16 v[34:37], v[76:79], v[102:105], v[34:37]
	s_waitcnt vmcnt(9)
	v_mfma_f32_16x16x32_f16 v[38:41], v[62:65], v[114:117], v[38:41]
	v_mfma_f32_16x16x32_f16 v[14:17], v[76:79], v[114:117], v[14:17]
	s_waitcnt vmcnt(8)
	v_mfma_f32_16x16x32_f16 v[42:45], v[62:65], v[118:121], v[42:45]
	v_mfma_f32_16x16x32_f16 v[18:21], v[76:79], v[118:121], v[18:21]
	s_setprio 0
	ds_read_b128 v[50:53], v176
	ds_read_b128 v[62:65], v176 offset:8448
	s_setprio 1
	s_waitcnt vmcnt(7) lgkmcnt(1)
	v_mfma_f32_16x16x32_f16 v[76:79], v[50:53], v[84:87], v[106:109]
	s_waitcnt lgkmcnt(0)
	v_mfma_f32_16x16x32_f16 v[10:13], v[62:65], v[84:87], v[10:13]
	s_waitcnt vmcnt(6)
	v_mfma_f32_16x16x32_f16 v[22:25], v[50:53], v[88:91], v[22:25]
	v_mfma_f32_16x16x32_f16 v[34:37], v[62:65], v[88:91], v[34:37]
	s_waitcnt vmcnt(5)
	v_mfma_f32_16x16x32_f16 v[38:41], v[50:53], v[92:95], v[38:41]
	v_mfma_f32_16x16x32_f16 v[14:17], v[62:65], v[92:95], v[14:17]
	s_waitcnt vmcnt(4)
	v_mfma_f32_16x16x32_f16 v[42:45], v[50:53], v[96:99], v[42:45]
	v_mfma_f32_16x16x32_f16 v[18:21], v[62:65], v[96:99], v[18:21]
	s_setprio 0
	ds_read_b128 v[50:53], v177
	ds_read_b128 v[62:65], v177 offset:8448
	s_setprio 1
	s_waitcnt vmcnt(3) lgkmcnt(1)
	v_mfma_f32_16x16x32_f16 v[76:79], v[50:53], v[46:49], v[76:79]
	s_waitcnt lgkmcnt(0)
	v_mfma_f32_16x16x32_f16 v[10:13], v[62:65], v[46:49], v[10:13]
	s_waitcnt vmcnt(2)
	v_mfma_f32_16x16x32_f16 v[22:25], v[50:53], v[54:57], v[22:25]
	v_mfma_f32_16x16x32_f16 v[34:37], v[62:65], v[54:57], v[34:37]
	s_waitcnt vmcnt(1)
	v_mfma_f32_16x16x32_f16 v[38:41], v[50:53], v[68:71], v[38:41]
	v_mfma_f32_16x16x32_f16 v[14:17], v[62:65], v[68:71], v[14:17]
	s_waitcnt vmcnt(0)
	v_mfma_f32_16x16x32_f16 v[42:45], v[50:53], v[72:75], v[42:45]
	v_mfma_f32_16x16x32_f16 v[18:21], v[62:65], v[72:75], v[18:21]
	s_setprio 0
	v_add_co_u32_e32 v108, vcc, s29, v152
	v_and_b32_e32 v67, 0x1c0, v0
	s_nop 0
	v_addc_co_u32_e32 v109, vcc, 0, v153, vcc
	v_add_co_u32_e32 v46, vcc, s52, v152
	s_movk_i32 s4, 0x50
	s_nop 0
	v_addc_co_u32_e32 v47, vcc, 0, v153, vcc
	v_add_co_u32_e32 v68, vcc, s33, v152
	v_or_b32_e32 v116, 16, v67
	s_nop 0
	v_addc_co_u32_e32 v69, vcc, 0, v153, vcc
	v_add_co_u32_e32 v110, vcc, s52, v154
	global_load_dwordx4 v[46:49], v[46:47], off
	s_nop 0
	global_load_dwordx4 v[50:53], v[68:69], off
	global_load_dwordx4 v[54:57], v[152:153], off
	global_load_dwordx4 v[62:65], v[154:155], off
	v_addc_co_u32_e32 v111, vcc, 0, v155, vcc
	v_add_co_u32_e32 v112, vcc, s52, v160
	global_load_dwordx4 v[68:71], v[156:157], off
	global_load_dwordx4 v[72:75], v[158:159], off
	global_load_dwordx4 v[84:87], v[160:161], off
	global_load_dwordx4 v[88:91], v[162:163], off
	v_addc_co_u32_e32 v113, vcc, 0, v161, vcc
	global_load_dwordx4 v[92:95], v[110:111], off
	global_load_dwordx4 v[96:99], v[112:113], off
	global_load_dwordx4 v[100:103], v[108:109], off
	global_load_dwordx4 v[104:107], v[164:165], off
	s_nop 0
	global_store_dwordx4 v[166:167], v[2:5], off sc0 sc1
	global_store_dwordx4 v[168:169], v[6:9], off sc0 sc1
	global_store_dwordx4 v[170:171], v[26:29], off sc0 sc1
	global_store_dwordx4 v[58:59], v[30:33], off sc0 sc1
	v_and_b32_e32 v4, 0x1cf, v0
	v_cvt_pk_f16_f32 v3, v78, v79
	v_cvt_pk_f16_f32 v2, v76, v77
	v_mad_u32_u24 v4, v4, s4, v80
	v_or_b32_e32 v5, v116, v81
	v_or_b32_e32 v117, 32, v67
	ds_write_b64 v4, v[2:3]
	v_cvt_pk_f16_f32 v3, v24, v25
	v_cvt_pk_f16_f32 v2, v22, v23
	v_mad_u32_u24 v5, v5, s4, v80
	v_or_b32_e32 v6, v117, v81
	v_or_b32_e32 v118, 48, v67
	ds_write_b64 v5, v[2:3]
	v_cvt_pk_f16_f32 v3, v40, v41
	v_cvt_pk_f16_f32 v2, v38, v39
	v_mad_u32_u24 v6, v6, s4, v80
	v_or_b32_e32 v7, v118, v81
	ds_write_b64 v6, v[2:3]
	v_cvt_pk_f16_f32 v3, v44, v45
	v_cvt_pk_f16_f32 v2, v42, v43
	v_mad_u32_u24 v7, v7, s4, v80
	ds_write_b64 v7, v[2:3]
	v_cvt_pk_f16_f32 v3, v12, v13
	v_cvt_pk_f16_f32 v2, v10, v11
	ds_write_b64 v4, v[2:3] offset:32
	v_cvt_pk_f16_f32 v3, v36, v37
	v_cvt_pk_f16_f32 v2, v34, v35
	ds_write_b64 v5, v[2:3] offset:32
	v_cvt_pk_f16_f32 v3, v16, v17
	v_cvt_pk_f16_f32 v2, v14, v15
	v_lshl_add_u64 v[10:11], v[60:61], 0, s[14:15]
	ds_write_b64 v6, v[2:3] offset:32
	v_cvt_pk_f16_f32 v2, v18, v19
	v_add_co_u32_e32 v18, vcc, s52, v10
	v_cvt_pk_f16_f32 v3, v20, v21
	v_lshl_add_u64 v[12:13], v[60:61], 0, s[16:17]
	v_addc_co_u32_e32 v19, vcc, 0, v11, vcc
	ds_write_b64 v7, v[2:3] offset:32
	s_waitcnt lgkmcnt(0)
	s_barrier
	global_load_dwordx4 v[2:5], v[10:11], off
	global_load_dwordx4 v[6:9], v[12:13], off
	v_lshl_add_u64 v[20:21], v[60:61], 0, s[12:13]
	global_load_dwordx4 v[10:13], v[18:19], off
	global_load_dwordx4 v[14:17], v[20:21], off
	ds_read_b128 v[18:21], v1
	ds_read_b128 v[22:25], v1 offset:8448
	s_mov_b32 s3, s27
	s_setprio 1
	s_waitcnt vmcnt(17) lgkmcnt(1)
	v_mfma_f32_16x16x32_f16 v[26:29], v[18:21], v[54:57], 0
	s_waitcnt lgkmcnt(0)
	v_mfma_f32_16x16x32_f16 v[30:33], v[22:25], v[54:57], 0
	s_waitcnt vmcnt(9)
	v_mfma_f32_16x16x32_f16 v[34:37], v[18:21], v[100:103], 0
	v_mfma_f32_16x16x32_f16 v[38:41], v[22:25], v[100:103], 0
	v_mfma_f32_16x16x32_f16 v[42:45], v[18:21], v[46:49], 0
	v_mfma_f32_16x16x32_f16 v[46:49], v[22:25], v[46:49], 0
	v_mfma_f32_16x16x32_f16 v[18:21], v[18:21], v[50:53], 0
	v_mfma_f32_16x16x32_f16 v[22:25], v[22:25], v[50:53], 0
	s_setprio 0
	v_lshl_add_u64 v[58:59], v[60:61], 0, s[10:11]
	v_add_co_u32_e32 v76, vcc, s29, v58
	s_nop 1
	v_addc_co_u32_e32 v77, vcc, 0, v59, vcc
	v_add_co_u32_e32 v108, vcc, s52, v58
	global_load_dwordx4 v[50:53], v[58:59], off
	global_load_dwordx4 v[54:57], v[76:77], off
	v_addc_co_u32_e32 v109, vcc, 0, v59, vcc
	v_add_co_u32_e32 v58, vcc, s33, v58
	s_nop 1
	v_addc_co_u32_e32 v59, vcc, 0, v59, vcc
	global_load_dwordx4 v[76:79], v[108:109], off
	global_load_dwordx4 v[100:103], v[58:59], off
	ds_read_b128 v[108:111], v82
	ds_read_b128 v[112:115], v82 offset:8448
	s_setprio 1
	s_waitcnt lgkmcnt(1)
	v_mfma_f32_16x16x32_f16 v[26:29], v[108:111], v[62:65], v[26:29]
	s_waitcnt lgkmcnt(0)
	v_mfma_f32_16x16x32_f16 v[30:33], v[112:115], v[62:65], v[30:33]
	v_mfma_f32_16x16x32_f16 v[34:37], v[108:111], v[68:71], v[34:37]
	v_mfma_f32_16x16x32_f16 v[38:41], v[112:115], v[68:71], v[38:41]
	v_mfma_f32_16x16x32_f16 v[42:45], v[108:111], v[92:95], v[42:45]
	v_mfma_f32_16x16x32_f16 v[46:49], v[112:115], v[92:95], v[46:49]
	v_mfma_f32_16x16x32_f16 v[18:21], v[108:111], v[72:75], v[18:21]
	v_mfma_f32_16x16x32_f16 v[22:25], v[112:115], v[72:75], v[22:25]
	s_setprio 0
	v_lshl_add_u64 v[58:59], v[60:61], 0, s[48:49]
	v_lshl_add_u64 v[72:73], v[60:61], 0, s[50:51]
	global_load_dwordx4 v[62:65], v[58:59], off
	global_load_dwordx4 v[68:71], v[72:73], off
	v_add_co_u32_e32 v58, vcc, s52, v58
	v_lshl_add_u64 v[82:83], v[60:61], 0, s[46:47]
	s_nop 0
	v_addc_co_u32_e32 v59, vcc, 0, v59, vcc
	global_load_dwordx4 v[72:75], v[58:59], off
	global_load_dwordx4 v[92:95], v[82:83], off
	ds_read_b128 v[108:111], v172
	ds_read_b128 v[112:115], v172 offset:8448
	s_setprio 1
	s_waitcnt lgkmcnt(1)
	v_mfma_f32_16x16x32_f16 v[26:29], v[108:111], v[84:87], v[26:29]
	s_waitcnt lgkmcnt(0)
	v_mfma_f32_16x16x32_f16 v[30:33], v[112:115], v[84:87], v[30:33]
	v_mfma_f32_16x16x32_f16 v[34:37], v[108:111], v[88:91], v[34:37]
	v_mfma_f32_16x16x32_f16 v[38:41], v[112:115], v[88:91], v[38:41]
	v_mfma_f32_16x16x32_f16 v[42:45], v[108:111], v[96:99], v[42:45]
	v_mfma_f32_16x16x32_f16 v[46:49], v[112:115], v[96:99], v[46:49]
	s_waitcnt vmcnt(16)
	v_mfma_f32_16x16x32_f16 v[18:21], v[108:111], v[104:107], v[18:21]
	v_mfma_f32_16x16x32_f16 v[22:25], v[112:115], v[104:107], v[22:25]
	s_setprio 0
	v_lshl_add_u64 v[58:59], v[60:61], 0, s[42:43]
	v_lshl_add_u64 v[90:91], v[60:61], 0, s[44:45]
	global_load_dwordx4 v[82:85], v[58:59], off
	global_load_dwordx4 v[86:89], v[90:91], off
	v_add_co_u32_e32 v58, vcc, s52, v58
	v_lshl_add_u64 v[90:91], v[60:61], 0, s[40:41]
	s_nop 0
	v_addc_co_u32_e32 v59, vcc, 0, v59, vcc
	global_load_dwordx4 v[96:99], v[58:59], off
	global_load_dwordx4 v[104:107], v[90:91], off
	ds_read_b128 v[108:111], v173
	ds_read_b128 v[112:115], v173 offset:8448
	s_setprio 1
	s_waitcnt vmcnt(15) lgkmcnt(1)
	v_mfma_f32_16x16x32_f16 v[26:29], v[108:111], v[2:5], v[26:29]
	s_waitcnt lgkmcnt(0)
	v_mfma_f32_16x16x32_f16 v[2:5], v[112:115], v[2:5], v[30:33]
	s_waitcnt vmcnt(14)
	v_mfma_f32_16x16x32_f16 v[30:33], v[108:111], v[6:9], v[34:37]
	v_mfma_f32_16x16x32_f16 v[6:9], v[112:115], v[6:9], v[38:41]
	s_waitcnt vmcnt(13)
	v_mfma_f32_16x16x32_f16 v[34:37], v[108:111], v[10:13], v[42:45]
	v_mfma_f32_16x16x32_f16 v[10:13], v[112:115], v[10:13], v[46:49]
	s_waitcnt vmcnt(12)
	v_mfma_f32_16x16x32_f16 v[18:21], v[108:111], v[14:17], v[18:21]
	v_mfma_f32_16x16x32_f16 v[14:17], v[112:115], v[14:17], v[22:25]
	s_setprio 0
	v_lshl_add_u64 v[42:43], v[60:61], 0, s[8:9]
	v_add_co_u32_e32 v58, vcc, s52, v42
	v_lshl_add_u64 v[44:45], v[60:61], 0, s[38:39]
	s_nop 0
	v_addc_co_u32_e32 v59, vcc, 0, v43, vcc
	global_load_dwordx4 v[22:25], v[42:43], off
	global_load_dwordx4 v[38:41], v[44:45], off
	v_lshl_add_u64 v[60:61], v[60:61], 0, s[6:7]
	global_load_dwordx4 v[42:45], v[58:59], off
	global_load_dwordx4 v[46:49], v[60:61], off
	ds_read_b128 v[58:61], v174
	ds_read_b128 v[108:111], v174 offset:8448
	s_setprio 1
	s_waitcnt vmcnt(15) lgkmcnt(1)
	v_mfma_f32_16x16x32_f16 v[26:29], v[58:61], v[50:53], v[26:29]
	s_waitcnt lgkmcnt(0)
	v_mfma_f32_16x16x32_f16 v[2:5], v[108:111], v[50:53], v[2:5]
	s_waitcnt vmcnt(14)
	v_mfma_f32_16x16x32_f16 v[30:33], v[58:61], v[54:57], v[30:33]
	v_mfma_f32_16x16x32_f16 v[6:9], v[108:111], v[54:57], v[6:9]
	s_waitcnt vmcnt(13)
	v_mfma_f32_16x16x32_f16 v[34:37], v[58:61], v[76:79], v[34:37]
	v_mfma_f32_16x16x32_f16 v[10:13], v[108:111], v[76:79], v[10:13]
	s_waitcnt vmcnt(12)
	v_mfma_f32_16x16x32_f16 v[18:21], v[58:61], v[100:103], v[18:21]
	v_mfma_f32_16x16x32_f16 v[14:17], v[108:111], v[100:103], v[14:17]
	s_setprio 0
	ds_read_b128 v[50:53], v175
	ds_read_b128 v[54:57], v175 offset:8448
	s_setprio 1
	s_waitcnt vmcnt(11) lgkmcnt(1)
	v_mfma_f32_16x16x32_f16 v[26:29], v[50:53], v[62:65], v[26:29]
	s_waitcnt lgkmcnt(0)
	v_mfma_f32_16x16x32_f16 v[2:5], v[54:57], v[62:65], v[2:5]
	s_waitcnt vmcnt(10)
	v_mfma_f32_16x16x32_f16 v[30:33], v[50:53], v[68:71], v[30:33]
	v_mfma_f32_16x16x32_f16 v[6:9], v[54:57], v[68:71], v[6:9]
	s_waitcnt vmcnt(9)
	v_mfma_f32_16x16x32_f16 v[34:37], v[50:53], v[72:75], v[34:37]
	v_mfma_f32_16x16x32_f16 v[10:13], v[54:57], v[72:75], v[10:13]
	s_waitcnt vmcnt(8)
	v_mfma_f32_16x16x32_f16 v[18:21], v[50:53], v[92:95], v[18:21]
	v_mfma_f32_16x16x32_f16 v[14:17], v[54:57], v[92:95], v[14:17]
	s_setprio 0
	ds_read_b128 v[50:53], v176
	ds_read_b128 v[54:57], v176 offset:8448
	s_setprio 1
	s_waitcnt vmcnt(7) lgkmcnt(1)
	v_mfma_f32_16x16x32_f16 v[26:29], v[50:53], v[82:85], v[26:29]
	s_waitcnt lgkmcnt(0)
	v_mfma_f32_16x16x32_f16 v[2:5], v[54:57], v[82:85], v[2:5]
	s_waitcnt vmcnt(6)
	v_mfma_f32_16x16x32_f16 v[30:33], v[50:53], v[86:89], v[30:33]
	v_mfma_f32_16x16x32_f16 v[6:9], v[54:57], v[86:89], v[6:9]
	s_waitcnt vmcnt(5)
	v_mfma_f32_16x16x32_f16 v[34:37], v[50:53], v[96:99], v[34:37]
	v_mfma_f32_16x16x32_f16 v[58:61], v[54:57], v[96:99], v[10:13]
	s_waitcnt vmcnt(4)
	v_mfma_f32_16x16x32_f16 v[18:21], v[50:53], v[104:107], v[18:21]
	v_mfma_f32_16x16x32_f16 v[50:53], v[54:57], v[104:107], v[14:17]
	s_setprio 0
	ds_read_b128 v[54:57], v177
	ds_read_b128 v[62:65], v177 offset:8448
	s_setprio 1
	s_waitcnt vmcnt(3) lgkmcnt(1)
	v_mfma_f32_16x16x32_f16 v[26:29], v[54:57], v[22:25], v[26:29]
	s_waitcnt lgkmcnt(0)
	v_mfma_f32_16x16x32_f16 v[14:17], v[62:65], v[22:25], v[2:5]
	s_waitcnt vmcnt(2)
	v_mfma_f32_16x16x32_f16 v[22:25], v[54:57], v[38:41], v[30:33]
	v_mfma_f32_16x16x32_f16 v[10:13], v[62:65], v[38:41], v[6:9]
	s_waitcnt vmcnt(1)
	v_mfma_f32_16x16x32_f16 v[30:33], v[54:57], v[42:45], v[34:37]
	v_mfma_f32_16x16x32_f16 v[6:9], v[62:65], v[42:45], v[58:61]
	s_waitcnt vmcnt(0)
	v_mfma_f32_16x16x32_f16 v[34:37], v[54:57], v[46:49], v[18:21]
	v_mfma_f32_16x16x32_f16 v[2:5], v[62:65], v[46:49], v[50:53]
	s_setprio 0
	s_nop 1
	v_mul_u32_u24_e32 v52, 0x50, v0
	ds_read_b128 v[18:21], v52
	s_lshl_b64 s[2:3], s[2:3], 15
	v_or_b32_e32 v0, s2, v66
	v_mov_b32_e32 v1, s3
	v_lshl_add_u64 v[50:51], s[24:25], 0, v[0:1]
	ds_read_b128 v[38:41], v52 offset:16
	ds_read_b128 v[42:45], v52 offset:32
	ds_read_b128 v[46:49], v52 offset:48
	s_waitcnt lgkmcnt(3)
	global_store_dwordx4 v[50:51], v[18:21], off sc0 sc1
	s_nop 1
	v_add_co_u32_e32 v18, vcc, s29, v50
	s_nop 1
	v_addc_co_u32_e32 v19, vcc, 0, v51, vcc
	s_waitcnt lgkmcnt(2)
	global_store_dwordx4 v[18:19], v[38:41], off sc0 sc1
	v_or_b32_e32 v18, 0x4000, v0
	v_mov_b32_e32 v19, s3
	v_lshl_add_u64 v[20:21], s[24:25], 0, v[18:19]
	s_waitcnt lgkmcnt(1)
	global_store_dwordx4 v[20:21], v[42:45], off sc0 sc1
	v_add_co_u32_e32 v20, vcc, s33, v50
	v_or_b32_e32 v39, 0x200, v81
	s_nop 0
	v_addc_co_u32_e32 v21, vcc, 0, v51, vcc
	s_waitcnt lgkmcnt(0)
	global_store_dwordx4 v[20:21], v[46:49], off sc0 sc1
	v_lshl_add_u64 v[0:1], s[0:1], 0, v[0:1]
	v_mov_b32_e32 v180, 0xbfb8aa3b
	v_mov_b32_e32 v181, 0xbfb8aa3b
	v_mov_b32_e32 v182, 1.0
	v_mov_b32_e32 v183, 1.0
	v_or_b32_e32 v184, v39, v67
	v_mad_u32_u24 v184, v184, s4, v80
	v_or_b32_e32 v185, v116, v39
	v_mad_u32_u24 v185, v185, s4, v80
	v_or_b32_e32 v186, v117, v39
	v_mad_u32_u24 v186, v186, s4, v80
	v_or_b32_e32 v187, v118, v39
	v_mad_u32_u24 v187, v187, s4, v80
	v_pk_mul_f32 v[188:189], v[26:27], v[180:181]
	v_pk_mul_f32 v[190:191], v[28:29], v[180:181]
	v_pk_mul_f32 v[196:197], v[22:23], v[180:181]
	v_pk_mul_f32 v[198:199], v[24:25], v[180:181]
	v_pk_mul_f32 v[204:205], v[30:31], v[180:181]
	v_pk_mul_f32 v[206:207], v[32:33], v[180:181]
	v_pk_mul_f32 v[212:213], v[34:35], v[180:181]
	v_pk_mul_f32 v[214:215], v[36:37], v[180:181]
	v_exp_f32_e32 v188, v188
	v_exp_f32_e32 v189, v189
	v_exp_f32_e32 v190, v190
	v_exp_f32_e32 v191, v191
	v_exp_f32_e32 v196, v196
	v_exp_f32_e32 v197, v197
	v_exp_f32_e32 v198, v198
	v_exp_f32_e32 v199, v199
	v_exp_f32_e32 v204, v204
	v_exp_f32_e32 v205, v205
	v_exp_f32_e32 v206, v206
	v_exp_f32_e32 v207, v207
	v_exp_f32_e32 v212, v212
	v_exp_f32_e32 v213, v213
	v_exp_f32_e32 v214, v214
	v_exp_f32_e32 v215, v215
	v_pk_add_f32 v[188:189], v[188:189], v[182:183]
	v_pk_add_f32 v[190:191], v[190:191], v[182:183]
	v_pk_add_f32 v[196:197], v[196:197], v[182:183]
	v_pk_add_f32 v[198:199], v[198:199], v[182:183]
	v_pk_add_f32 v[204:205], v[204:205], v[182:183]
	v_pk_add_f32 v[206:207], v[206:207], v[182:183]
	v_pk_add_f32 v[212:213], v[212:213], v[182:183]
	v_pk_add_f32 v[214:215], v[214:215], v[182:183]
	v_rcp_f32_e32 v188, v188
	v_rcp_f32_e32 v189, v189
	v_rcp_f32_e32 v190, v190
	v_rcp_f32_e32 v191, v191
	v_rcp_f32_e32 v196, v196
	v_rcp_f32_e32 v197, v197
	v_rcp_f32_e32 v198, v198
	v_rcp_f32_e32 v199, v199
	v_rcp_f32_e32 v204, v204
	v_rcp_f32_e32 v205, v205
	v_rcp_f32_e32 v206, v206
	v_rcp_f32_e32 v207, v207
	v_rcp_f32_e32 v212, v212
	v_rcp_f32_e32 v213, v213
	v_rcp_f32_e32 v214, v214
	v_rcp_f32_e32 v215, v215
	v_fma_mixlo_f16 v192, v26, v188, 0
	v_mul_f32_e32 v189, v27, v189
	v_mul_f32_e32 v190, v28, v190
	v_fma_mixlo_f16 v193, v29, v191, 0
	v_fma_mixlo_f16 v200, v22, v196, 0
	v_mul_f32_e32 v197, v23, v197
	v_mul_f32_e32 v198, v24, v198
	v_fma_mixlo_f16 v201, v25, v199, 0
	v_fma_mixlo_f16 v208, v30, v204, 0
	v_mul_f32_e32 v205, v31, v205
	v_mul_f32_e32 v206, v32, v206
	v_fma_mixlo_f16 v209, v33, v207, 0
	v_fma_mixlo_f16 v216, v34, v212, 0
	v_mul_f32_e32 v213, v35, v213
	v_mul_f32_e32 v214, v36, v214
	v_fma_mixlo_f16 v217, v37, v215, 0
	v_cvt_pk_f16_f32 v188, v189, v190
	v_cvt_pk_f16_f32 v196, v197, v198
	v_cvt_pk_f16_f32 v204, v205, v206
	v_cvt_pk_f16_f32 v212, v213, v214
	v_pack_b32_f16 v194, v192, v188
	v_alignbit_b32 v195, v193, v188, 16
	v_pack_b32_f16 v202, v200, v196
	v_alignbit_b32 v203, v201, v196, 16
	v_pack_b32_f16 v210, v208, v204
	v_alignbit_b32 v211, v209, v204, 16
	v_pack_b32_f16 v218, v216, v212
	v_alignbit_b32 v219, v217, v212, 16
	ds_write_b64 v184, v[194:195]
	ds_write_b64 v185, v[202:203]
	ds_write_b64 v186, v[210:211]
	ds_write_b64 v187, v[218:219]
	v_pk_mul_f32 v[188:189], v[14:15], v[180:181]
	v_pk_mul_f32 v[190:191], v[16:17], v[180:181]
	v_pk_mul_f32 v[196:197], v[10:11], v[180:181]
	v_pk_mul_f32 v[198:199], v[12:13], v[180:181]
	v_pk_mul_f32 v[204:205], v[6:7], v[180:181]
	v_pk_mul_f32 v[206:207], v[8:9], v[180:181]
	v_pk_mul_f32 v[212:213], v[2:3], v[180:181]
	v_pk_mul_f32 v[214:215], v[4:5], v[180:181]
	v_exp_f32_e32 v188, v188
	v_exp_f32_e32 v189, v189
	v_exp_f32_e32 v190, v190
	v_exp_f32_e32 v191, v191
	v_exp_f32_e32 v196, v196
	v_exp_f32_e32 v197, v197
	v_exp_f32_e32 v198, v198
	v_exp_f32_e32 v199, v199
	v_exp_f32_e32 v204, v204
	v_exp_f32_e32 v205, v205
	v_exp_f32_e32 v206, v206
	v_exp_f32_e32 v207, v207
	v_exp_f32_e32 v212, v212
	v_exp_f32_e32 v213, v213
	v_exp_f32_e32 v214, v214
	v_exp_f32_e32 v215, v215
	v_pk_add_f32 v[188:189], v[188:189], v[182:183]
	v_pk_add_f32 v[190:191], v[190:191], v[182:183]
	v_pk_add_f32 v[196:197], v[196:197], v[182:183]
	v_pk_add_f32 v[198:199], v[198:199], v[182:183]
	v_pk_add_f32 v[204:205], v[204:205], v[182:183]
	v_pk_add_f32 v[206:207], v[206:207], v[182:183]
	v_pk_add_f32 v[212:213], v[212:213], v[182:183]
	v_pk_add_f32 v[214:215], v[214:215], v[182:183]
	v_rcp_f32_e32 v188, v188
	v_rcp_f32_e32 v189, v189
	v_rcp_f32_e32 v190, v190
	v_rcp_f32_e32 v191, v191
	v_rcp_f32_e32 v196, v196
	v_rcp_f32_e32 v197, v197
	v_rcp_f32_e32 v198, v198
	v_rcp_f32_e32 v199, v199
	v_rcp_f32_e32 v204, v204
	v_rcp_f32_e32 v205, v205
	v_rcp_f32_e32 v206, v206
	v_rcp_f32_e32 v207, v207
	v_rcp_f32_e32 v212, v212
	v_rcp_f32_e32 v213, v213
	v_rcp_f32_e32 v214, v214
	v_rcp_f32_e32 v215, v215
	v_fma_mixlo_f16 v192, v14, v188, 0
	v_mul_f32_e32 v189, v15, v189
	v_mul_f32_e32 v190, v16, v190
	v_fma_mixlo_f16 v193, v17, v191, 0
	v_fma_mixlo_f16 v200, v10, v196, 0
	v_mul_f32_e32 v197, v11, v197
	v_mul_f32_e32 v198, v12, v198
	v_fma_mixlo_f16 v201, v13, v199, 0
	v_fma_mixlo_f16 v208, v6, v204, 0
	v_mul_f32_e32 v205, v7, v205
	v_mul_f32_e32 v206, v8, v206
	v_fma_mixlo_f16 v209, v9, v207, 0
	v_fma_mixlo_f16 v216, v2, v212, 0
	v_mul_f32_e32 v213, v3, v213
	v_mul_f32_e32 v214, v4, v214
	v_fma_mixlo_f16 v217, v5, v215, 0
	v_cvt_pk_f16_f32 v188, v189, v190
	v_cvt_pk_f16_f32 v196, v197, v198
	v_cvt_pk_f16_f32 v204, v205, v206
	v_cvt_pk_f16_f32 v212, v213, v214
	v_pack_b32_f16 v194, v192, v188
	v_alignbit_b32 v195, v193, v188, 16
	v_pack_b32_f16 v202, v200, v196
	v_alignbit_b32 v203, v201, v196, 16
	v_pack_b32_f16 v210, v208, v204
	v_alignbit_b32 v211, v209, v204, 16
	v_pack_b32_f16 v218, v216, v212
	v_alignbit_b32 v219, v217, v212, 16
	ds_write_b64 v184, v[194:195] offset:32
	ds_write_b64 v185, v[202:203] offset:32
	ds_write_b64 v186, v[210:211] offset:32
	ds_write_b64 v187, v[218:219] offset:32
	s_waitcnt lgkmcnt(0)
	s_barrier
	ds_read_b128 v[2:5], v52 offset:40960
	ds_read_b128 v[6:9], v52 offset:40976
	ds_read_b128 v[10:13], v52 offset:40992
	ds_read_b128 v[14:17], v52 offset:41008
	s_waitcnt lgkmcnt(3)
	global_store_dwordx4 v[0:1], v[2:5], off sc0 sc1
	s_nop 1
	v_add_co_u32_e32 v2, vcc, 0x2000, v0
	s_nop 1
	v_addc_co_u32_e32 v3, vcc, 0, v1, vcc
	v_add_co_u32_e32 v0, vcc, 0x6000, v0
	s_waitcnt lgkmcnt(2)
	global_store_dwordx4 v[2:3], v[6:9], off sc0 sc1
	v_lshl_add_u64 v[2:3], s[0:1], 0, v[18:19]
	v_addc_co_u32_e32 v1, vcc, 0, v1, vcc
	s_waitcnt lgkmcnt(1)
	global_store_dwordx4 v[2:3], v[10:13], off sc0 sc1
	s_waitcnt lgkmcnt(0)
	global_store_dwordx4 v[0:1], v[14:17], off sc0 sc1
	s_endpgm
	.p2align	8

amdhsa.kernels:
  - .agpr_count:     0
    .args:
      - .actual_access:  read_only
        .address_space:  global
        .offset:         0
        .size:           8
        .value_kind:     global_buffer
      - .actual_access:  write_only
        .address_space:  global
        .offset:         8
        .size:           8
        .value_kind:     global_buffer
      - .offset:         16
        .size:           4
        .value_kind:     by_value
      - .offset:         20
        .size:           4
        .value_kind:     by_value
      - .actual_access:  read_only
        .address_space:  global
        .offset:         24
        .size:           8
        .value_kind:     global_buffer
      - .actual_access:  write_only
        .address_space:  global
        .offset:         32
        .size:           8
        .value_kind:     global_buffer
      - .offset:         40
        .size:           4
        .value_kind:     by_value
      - .offset:         44
        .size:           4
        .value_kind:     by_value
      - .actual_access:  read_only
        .address_space:  global
        .offset:         48
        .size:           8
        .value_kind:     global_buffer
      - .actual_access:  write_only
        .address_space:  global
        .offset:         56
        .size:           8
        .value_kind:     global_buffer
      - .offset:         64
        .size:           4
        .value_kind:     by_value
      - .offset:         68
        .size:           4
        .value_kind:     by_value
      - .actual_access:  read_only
        .address_space:  global
        .offset:         72
        .size:           8
        .value_kind:     global_buffer
      - .actual_access:  write_only
        .address_space:  global
        .offset:         80
        .size:           8
        .value_kind:     global_buffer
      - .offset:         88
        .size:           4
        .value_kind:     by_value
      - .actual_access:  read_only
        .address_space:  global
        .offset:         96
        .size:           8
        .value_kind:     global_buffer
      - .actual_access:  write_only
        .address_space:  global
        .offset:         104
        .size:           8
        .value_kind:     global_buffer
      - .offset:         112
        .size:           4
        .value_kind:     by_value
      - .offset:         120
        .size:           4
        .value_kind:     hidden_block_count_x
      - .offset:         124
        .size:           4
        .value_kind:     hidden_block_count_y
      - .offset:         128
        .size:           4
        .value_kind:     hidden_block_count_z
      - .offset:         132
        .size:           2
        .value_kind:     hidden_group_size_x
      - .offset:         134
        .size:           2
        .value_kind:     hidden_group_size_y
      - .offset:         136
        .size:           2
        .value_kind:     hidden_group_size_z
      - .offset:         138
        .size:           2
        .value_kind:     hidden_remainder_x
      - .offset:         140
        .size:           2
        .value_kind:     hidden_remainder_y
      - .offset:         142
        .size:           2
        .value_kind:     hidden_remainder_z
      - .offset:         160
        .size:           8
        .value_kind:     hidden_global_offset_x
      - .offset:         168
        .size:           8
        .value_kind:     hidden_global_offset_y
      - .offset:         176
        .size:           8
        .value_kind:     hidden_global_offset_z
      - .offset:         184
        .size:           2
        .value_kind:     hidden_grid_dims
    .group_segment_fixed_size: 0
    .kernarg_segment_align: 8
    .kernarg_segment_size: 376
    .language:       OpenCL C
    .language_version:
      - 2
      - 0
    .max_flat_workgroup_size: 1024
    .name:           _Z5k_swzPKfPDF16_iiS0_S1_iiS0_S1_iiS0_PfiS0_S1_i
    .private_segment_fixed_size: 0
    .sgpr_count:     32
    .sgpr_spill_count: 0
    .symbol:         _Z5k_swzPKfPDF16_iiS0_S1_iiS0_S1_iiS0_PfiS0_S1_i.kd
    .uniform_work_group_size: 1
    .uses_dynamic_stack: false
    .vgpr_count:     14
    .vgpr_spill_count: 0
    .wavefront_size: 64
  - .agpr_count:     0
    .args:
      - .actual_access:  read_only
        .address_space:  global
        .offset:         0
        .size:           8
        .value_kind:     global_buffer
      - .actual_access:  read_only
        .address_space:  global
        .offset:         8
        .size:           8
        .value_kind:     global_buffer
      - .actual_access:  write_only
        .address_space:  global
        .offset:         16
        .size:           8
        .value_kind:     global_buffer
      - .actual_access:  read_only
        .address_space:  global
        .offset:         24
        .size:           8
        .value_kind:     global_buffer
      - .actual_access:  read_only
        .address_space:  global
        .offset:         32
        .size:           8
        .value_kind:     global_buffer
      - .actual_access:  read_only
        .address_space:  global
        .offset:         40
        .size:           8
        .value_kind:     global_buffer
      - .actual_access:  write_only
        .address_space:  global
        .offset:         48
        .size:           8
        .value_kind:     global_buffer
    .group_segment_fixed_size: 98816
    .kernarg_segment_align: 8
    .kernarg_segment_size: 56
    .language:       OpenCL C
    .language_version:
      - 2
      - 0
    .max_flat_workgroup_size: 512
    .name:           _Z10k_ka_firstPKfPKiPfS0_S0_PKDF16_PDF16_
    .private_segment_fixed_size: 0
    .sgpr_count:     59
    .sgpr_spill_count: 0
    .symbol:         _Z10k_ka_firstPKfPKiPfS0_S0_PKDF16_PDF16_.kd
    .uniform_work_group_size: 1
    .uses_dynamic_stack: false
    .vgpr_count:     174
    .vgpr_spill_count: 0
    .wavefront_size: 64
  - .agpr_count:     0
    .args:
      - .actual_access:  read_only
        .address_space:  global
        .offset:         0
        .size:           8
        .value_kind:     global_buffer
      - .actual_access:  read_only
        .address_space:  global
        .offset:         8
        .size:           8
        .value_kind:     global_buffer
      - .actual_access:  read_only
        .address_space:  global
        .offset:         16
        .size:           8
        .value_kind:     global_buffer
      - .actual_access:  read_only
        .address_space:  global
        .offset:         24
        .size:           8
        .value_kind:     global_buffer
      - .actual_access:  read_only
        .address_space:  global
        .offset:         32
        .size:           8
        .value_kind:     global_buffer
      - .actual_access:  read_only
        .address_space:  global
        .offset:         40
        .size:           8
        .value_kind:     global_buffer
      - .actual_access:  write_only
        .address_space:  global
        .offset:         48
        .size:           8
        .value_kind:     global_buffer
      - .actual_access:  write_only
        .address_space:  global
        .offset:         56
        .size:           8
        .value_kind:     global_buffer
      - .actual_access:  write_only
        .address_space:  global
        .offset:         64
        .size:           8
        .value_kind:     global_buffer
      - .actual_access:  read_only
        .address_space:  global
        .offset:         72
        .size:           8
        .value_kind:     global_buffer
      - .actual_access:  write_only
        .address_space:  global
        .offset:         80
        .size:           8
        .value_kind:     global_buffer
      - .actual_access:  write_only
        .address_space:  global
        .offset:         88
        .size:           8
        .value_kind:     global_buffer
    .group_segment_fixed_size: 47616
    .kernarg_segment_align: 8
    .kernarg_segment_size: 96
    .language:       OpenCL C
    .language_version:
      - 2
      - 0
    .max_flat_workgroup_size: 512
    .name:           _Z12k_conv_xprojPKDF16_PKfS2_S0_S0_S2_PDF16_S3_PfS2_S3_S4_
    .private_segment_fixed_size: 0
    .sgpr_count:     32
    .sgpr_spill_count: 0
    .symbol:         _Z12k_conv_xprojPKDF16_PKfS2_S0_S0_S2_PDF16_S3_PfS2_S3_S4_.kd
    .uniform_work_group_size: 1
    .uses_dynamic_stack: false
    .vgpr_count:     252
    .vgpr_spill_count: 0
    .wavefront_size: 64
  - .agpr_count:     0
    .args:
      - .actual_access:  read_only
        .address_space:  global
        .offset:         0
        .size:           8
        .value_kind:     global_buffer
      - .actual_access:  read_only
        .address_space:  global
        .offset:         8
        .size:           8
        .value_kind:     global_buffer
      - .actual_access:  read_only
        .address_space:  global
        .offset:         16
        .size:           8
        .value_kind:     global_buffer
      - .actual_access:  write_only
        .address_space:  global
        .offset:         24
        .size:           8
        .value_kind:     global_buffer
    .group_segment_fixed_size: 16384
    .kernarg_segment_align: 8
    .kernarg_segment_size: 32
    .language:       OpenCL C
    .language_version:
      - 2
      - 0
    .max_flat_workgroup_size: 512
    .name:           _Z11k_scan_combPKDF16_PKfS2_PDF16_
    .private_segment_fixed_size: 0
    .sgpr_count:     18
    .sgpr_spill_count: 0
    .symbol:         _Z11k_scan_combPKDF16_PKfS2_PDF16_.kd
    .uniform_work_group_size: 1
    .uses_dynamic_stack: false
    .vgpr_count:     120
    .vgpr_spill_count: 0
    .wavefront_size: 64
  - .agpr_count:     0
    .args:
      - .actual_access:  read_only
        .address_space:  global
        .offset:         0
        .size:           8
        .value_kind:     global_buffer
      - .actual_access:  read_only
        .address_space:  global
        .offset:         8
        .size:           8
        .value_kind:     global_buffer
      - .actual_access:  read_only
        .address_space:  global
        .offset:         16
        .size:           8
        .value_kind:     global_buffer
      - .actual_access:  read_only
        .address_space:  global
        .offset:         24
        .size:           8
        .value_kind:     global_buffer
      - .actual_access:  write_only
        .address_space:  global
        .offset:         32
        .size:           8
        .value_kind:     global_buffer
    .group_segment_fixed_size: 32
    .kernarg_segment_align: 8
    .kernarg_segment_size: 40
    .language:       OpenCL C
    .language_version:
      - 2
      - 0
    .max_flat_workgroup_size: 256
    .name:           _Z6k_headPKfS0_S0_S0_Pf
    .private_segment_fixed_size: 0
    .sgpr_count:     86
    .sgpr_spill_count: 0
    .symbol:         _Z6k_headPKfS0_S0_S0_Pf.kd
    .uniform_work_group_size: 1
    .uses_dynamic_stack: false
    .vgpr_count:     92
    .vgpr_spill_count: 0
    .wavefront_size: 64
  - .agpr_count:     0
    .args:
      - .actual_access:  read_only
        .address_space:  global
        .offset:         0
        .size:           8
        .value_kind:     global_buffer
      - .actual_access:  read_only
        .address_space:  global
        .offset:         8
        .size:           8
        .value_kind:     global_buffer
      - .actual_access:  read_only
        .address_space:  global
        .offset:         16
        .size:           8
        .value_kind:     global_buffer
      - .actual_access:  read_only
        .address_space:  global
        .offset:         24
        .size:           8
        .value_kind:     global_buffer
      - .actual_access:  read_only
        .address_space:  global
        .offset:         32
        .size:           8
        .value_kind:     global_buffer
      - .actual_access:  read_only
        .address_space:  global
        .offset:         40
        .size:           8
        .value_kind:     global_buffer
      - .actual_access:  read_only
        .address_space:  global
        .offset:         48
        .size:           8
        .value_kind:     global_buffer
      - .address_space:  global
        .offset:         56
        .size:           8
        .value_kind:     global_buffer
      - .actual_access:  read_only
        .address_space:  global
        .offset:         64
        .size:           8
        .value_kind:     global_buffer
      - .actual_access:  read_only
        .address_space:  global
        .offset:         72
        .size:           8
        .value_kind:     global_buffer
      - .actual_access:  read_only
        .address_space:  global
        .offset:         80
        .size:           8
        .value_kind:     global_buffer
      - .address_space:  global
        .offset:         88
        .size:           8
        .value_kind:     global_buffer
      - .actual_access:  read_only
        .address_space:  global
        .offset:         96
        .size:           8
        .value_kind:     global_buffer
      - .actual_access:  read_only
        .address_space:  global
        .offset:         104
        .size:           8
        .value_kind:     global_buffer
      - .actual_access:  read_only
        .address_space:  global
        .offset:         112
        .size:           8
        .value_kind:     global_buffer
    .group_segment_fixed_size: 98816
    .kernarg_segment_align: 8
    .kernarg_segment_size: 120
    .language:       OpenCL C
    .language_version:
      - 2
      - 0
    .max_flat_workgroup_size: 512
    .name:           _Z4k_k2ILb0EEvPKDF16_S1_PKfS3_S3_S1_S1_PfS3_S3_S1_PDF16_PKiS4_S4_
    .private_segment_fixed_size: 0
    .sgpr_count:     106
    .sgpr_spill_count: 0
    .symbol:         _Z4k_k2ILb0EEvPKDF16_S1_PKfS3_S3_S1_S1_PfS3_S3_S1_PDF16_PKiS4_S4_.kd
    .uniform_work_group_size: 1
    .uses_dynamic_stack: false
    .vgpr_count:     232
    .vgpr_spill_count: 0
    .wavefront_size: 64
  - .agpr_count:     0
    .args:
      - .actual_access:  read_only
        .address_space:  global
        .offset:         0
        .size:           8
        .value_kind:     global_buffer
      - .actual_access:  read_only
        .address_space:  global
        .offset:         8
        .size:           8
        .value_kind:     global_buffer
      - .actual_access:  read_only
        .address_space:  global
        .offset:         16
        .size:           8
        .value_kind:     global_buffer
      - .actual_access:  read_only
        .address_space:  global
        .offset:         24
        .size:           8
        .value_kind:     global_buffer
      - .actual_access:  read_only
        .address_space:  global
        .offset:         32
        .size:           8
        .value_kind:     global_buffer
      - .actual_access:  read_only
        .address_space:  global
        .offset:         40
        .size:           8
        .value_kind:     global_buffer
      - .actual_access:  read_only
        .address_space:  global
        .offset:         48
        .size:           8
        .value_kind:     global_buffer
      - .actual_access:  read_only
        .address_space:  global
        .offset:         56
        .size:           8
        .value_kind:     global_buffer
      - .actual_access:  read_only
        .address_space:  global
        .offset:         64
        .size:           8
        .value_kind:     global_buffer
      - .actual_access:  read_only
        .address_space:  global
        .offset:         72
        .size:           8
        .value_kind:     global_buffer
      - .actual_access:  read_only
        .address_space:  global
        .offset:         80
        .size:           8
        .value_kind:     global_buffer
      - .actual_access:  read_only
        .address_space:  global
        .offset:         88
        .size:           8
        .value_kind:     global_buffer
      - .actual_access:  read_only
        .address_space:  global
        .offset:         96
        .size:           8
        .value_kind:     global_buffer
      - .actual_access:  write_only
        .address_space:  global
        .offset:         104
        .size:           8
        .value_kind:     global_buffer
      - .actual_access:  write_only
        .address_space:  global
        .offset:         112
        .size:           8
        .value_kind:     global_buffer
    .group_segment_fixed_size: 98816
    .kernarg_segment_align: 8
    .kernarg_segment_size: 120
    .language:       OpenCL C
    .language_version:
      - 2
      - 0
    .max_flat_workgroup_size: 512
    .name:           _Z4k_k2ILb1EEvPKDF16_S1_PKfS3_S3_S1_S1_PfS3_S3_S1_PDF16_PKiS4_S4_
    .private_segment_fixed_size: 0
    .sgpr_count:     44
    .sgpr_spill_count: 0
    .symbol:         _Z4k_k2ILb1EEvPKDF16_S1_PKfS3_S3_S1_S1_PfS3_S3_S1_PDF16_PKiS4_S4_.kd
    .uniform_work_group_size: 1
    .uses_dynamic_stack: false
    .vgpr_count:     196
    .vgpr_spill_count: 0
    .wavefront_size: 64
